# speedup vs baseline: 1.0153x; 1.0153x over previous
_Z12k1_colsum_q8PKfPjPfS2_:
	s_load_dwordx8 s[4:11], s[0:1], 0x0
	v_and_b32_e32 v1, 63, v0
	v_lshrrev_b32_e32 v41, 6, v0
	s_mul_i32 s12, s2, 0xc35
	s_lshr_b32 s12, s12, 4
	v_readfirstlane_b32 s14, v41
	s_add_i32 s13, s2, 1
	s_mul_i32 s13, s13, 0xc35
	s_lshr_b32 s13, s13, 4
	s_sub_u32 s13, s13, s12
	s_sub_u32 s15, s13, 0xc0
	s_cmp_lt_u32 s14, s15
	s_cselect_b32 s29, 1, 0
	v_lshlrev_b32_e32 v34, 4, v1
	v_min_u32_e32 v35, 57, v1
	v_lshlrev_b32_e32 v35, 4, v35
	v_cmp_gt_u32_e64 s[18:19], 58, v1
	s_lshl_b32 s35, s14, 13
	s_add_u32 s36, s35, 0x1000
	v_add_u32_e32 v38, s35, v34
	v_lshrrev_b32_e32 v41, 5, v1
	v_mov_b32_e32 v42, 0xc35000
	v_mul_lo_u32 v39, v41, v42
	v_and_b32_e32 v42, 31, v1
	v_lshl_add_u32 v39, v42, 2, v39
	v_mov_b32_e32 v2, 0
	v_mov_b32_e32 v3, 0
	v_mov_b32_e32 v4, 0
	v_mov_b32_e32 v5, 0
	v_mov_b32_e32 v6, 0
	v_mov_b32_e32 v7, 0
	v_mov_b32_e32 v8, 0
	v_mov_b32_e32 v9, 0
	v_mov_b32_e32 v10, 0
	v_mov_b32_e32 v11, 0
	v_mov_b32_e32 v12, 0
	v_mov_b32_e32 v13, 0
	v_mov_b32_e32 v14, 0
	v_mov_b32_e32 v15, 0
	v_mov_b32_e32 v16, 0
	v_mov_b32_e32 v17, 0
	v_mov_b32_e32 v40, 0
	v_mov_b32_e32 v47, 0x42fe0000
	s_mov_b32 s32, 0x42fe0000
	s_mov_b32 s33, 0xc0c0400
	s_mov_b32 s34, 0x4000c0c
	s_add_u32 s15, s12, s14
	s_mul_i32 s37, s15, 0xfa0
	s_lshl_b32 s15, s15, 7
	s_waitcnt lgkmcnt(0)
	s_add_u32 s16, s4, s37
	s_addc_u32 s17, s5, 0
	s_add_u32 s40, s6, s15
	s_addc_u32 s41, s7, 0
	s_add_u32 s20, s40, 0
	s_addc_u32 s21, s41, 0
	s_add_u32 s22, s20, 0x186a000
	s_addc_u32 s23, s21, 0
	s_add_u32 s24, s22, 0x186a000
	s_addc_u32 s25, s23, 0
	s_add_u32 s26, s24, 0x186a000
	s_addc_u32 s27, s25, 0
	s_mov_b32 m0, s35
	s_nop 0
	global_load_lds_dwordx4 v34, s[16:17] nt
	global_load_lds_dwordx4 v34, s[16:17] offset:1024 nt
	global_load_lds_dwordx4 v34, s[16:17] offset:2048 nt
	global_load_lds_dwordx4 v35, s[16:17] offset:3072 nt
	s_add_u32 s16, s16, 0x7d00
	s_addc_u32 s17, s17, 0
	s_waitcnt vmcnt(0)
	ds_read_b128 v[18:21], v38 offset:0
	ds_read_b128 v[22:25], v38 offset:1024
	ds_read_b128 v[26:29], v38 offset:2048
	ds_read_b128 v[30:33], v38 offset:3072
	s_waitcnt lgkmcnt(0)
	s_mov_b32 m0, s36
	s_nop 0
	global_load_lds_dwordx4 v34, s[16:17] nt
	global_load_lds_dwordx4 v34, s[16:17] offset:1024 nt
	global_load_lds_dwordx4 v34, s[16:17] offset:2048 nt
	global_load_lds_dwordx4 v35, s[16:17] offset:3072 nt
	s_add_u32 s16, s16, 0x7d00
	s_addc_u32 s17, s17, 0
	v_cndmask_b32_e64 v30, 0, v30, s[18:19]
	v_cndmask_b32_e64 v31, 0, v31, s[18:19]
	v_cndmask_b32_e64 v32, 0, v32, s[18:19]
	v_cndmask_b32_e64 v33, 0, v33, s[18:19]
	v_max3_f32 v41, |v18|, |v19|, |v20|
	v_max3_f32 v42, |v21|, |v22|, |v23|
	v_max3_f32 v43, |v24|, |v25|, |v26|
	v_max3_f32 v44, |v27|, |v28|, |v29|
	v_max3_f32 v48, |v30|, |v31|, |v32|
	v_max3_f32 v41, v41, v42, |v33|
	v_max3_f32 v43, v43, v44, v48
	v_max_f32_e32 v41, v41, v43
	v_pk_add_f32 v[2:3], v[2:3], v[18:19]
	v_pk_add_f32 v[4:5], v[4:5], v[20:21]
	v_max_f32_dpp v41, v41, v41 quad_perm:[1,0,3,2] row_mask:0xf bank_mask:0xf
	v_pk_add_f32 v[6:7], v[6:7], v[22:23]
	v_pk_add_f32 v[8:9], v[8:9], v[24:25]
	v_max_f32_dpp v41, v41, v41 quad_perm:[2,3,0,1] row_mask:0xf bank_mask:0xf
	v_pk_add_f32 v[10:11], v[10:11], v[26:27]
	v_pk_add_f32 v[12:13], v[12:13], v[28:29]
	v_max_f32_dpp v41, v41, v41 row_half_mirror row_mask:0xf bank_mask:0xf
	v_pk_add_f32 v[14:15], v[14:15], v[30:31]
	v_pk_add_f32 v[16:17], v[16:17], v[32:33]
	v_max_f32_dpp v41, v41, v41 row_mirror row_mask:0xf bank_mask:0xf
	s_nop 1
	v_max_f32_dpp v41, v41, v41 row_bcast:15 row_mask:0xa bank_mask:0xf
	s_nop 1
	v_max_f32_dpp v41, v41, v41 row_bcast:31 row_mask:0xc bank_mask:0xf
	s_nop 1
	v_readlane_b32 s28, v41, 63
	s_nop 1
	v_div_scale_f32 v48, s[30:31], s28, s28, v47
	v_rcp_f32_e32 v49, v48
	s_nop 0
	v_fma_f32 v50, -v48, v49, 1.0
	v_fmac_f32_e32 v49, v50, v49
	v_mov_b32_e32 v50, s28
	v_div_scale_f32 v50, vcc, s32, v50, s32
	v_mul_f32_e32 v51, v50, v49
	v_fma_f32 v52, -v48, v51, v50
	v_fmac_f32_e32 v51, v52, v49
	v_fma_f32 v48, -v48, v51, v50
	v_div_fmas_f32 v48, v48, v49, v51
	v_div_fixup_f32 v48, v48, s28, v47
	v_cmp_gt_f32_e64 vcc, s28, 0
	v_writelane_b32 v40, s28, 0
	s_nop 0
	v_cndmask_b32_e32 v48, 0, v48, vcc
	v_fmaak_f32 v49, v18, v48, 0x4b400000
	v_fmaak_f32 v50, v19, v48, 0x4b400000
	v_fmaak_f32 v51, v20, v48, 0x4b400000
	v_fmaak_f32 v52, v21, v48, 0x4b400000
	v_perm_b32 v49, v50, v49, s33
	v_perm_b32 v51, v52, v51, s34
	v_or_b32_e32 v56, v49, v51
	v_fmaak_f32 v41, v22, v48, 0x4b400000
	v_fmaak_f32 v42, v23, v48, 0x4b400000
	v_fmaak_f32 v43, v24, v48, 0x4b400000
	v_fmaak_f32 v44, v25, v48, 0x4b400000
	v_perm_b32 v41, v42, v41, s33
	v_perm_b32 v43, v44, v43, s34
	v_or_b32_e32 v57, v41, v43
	v_fmaak_f32 v49, v26, v48, 0x4b400000
	v_fmaak_f32 v50, v27, v48, 0x4b400000
	v_fmaak_f32 v51, v28, v48, 0x4b400000
	v_fmaak_f32 v52, v29, v48, 0x4b400000
	v_perm_b32 v49, v50, v49, s33
	v_perm_b32 v51, v52, v51, s34
	v_or_b32_e32 v58, v49, v51
	v_fmaak_f32 v41, v30, v48, 0x4b400000
	v_fmaak_f32 v42, v31, v48, 0x4b400000
	v_fmaak_f32 v43, v32, v48, 0x4b400000
	v_fmaak_f32 v44, v33, v48, 0x4b400000
	v_perm_b32 v41, v42, v41, s33
	v_perm_b32 v43, v44, v43, s34
	v_or_b32_e32 v59, v41, v43
	s_waitcnt vmcnt(0)
	ds_read_b128 v[18:21], v38 offset:4096
	ds_read_b128 v[22:25], v38 offset:5120
	ds_read_b128 v[26:29], v38 offset:6144
	ds_read_b128 v[30:33], v38 offset:7168
	s_waitcnt lgkmcnt(0)
	s_mov_b32 m0, s35
	s_nop 0
	global_load_lds_dwordx4 v34, s[16:17] nt
	global_load_lds_dwordx4 v34, s[16:17] offset:1024 nt
	global_load_lds_dwordx4 v34, s[16:17] offset:2048 nt
	global_load_lds_dwordx4 v35, s[16:17] offset:3072 nt
	s_add_u32 s16, s16, 0x7d00
	s_addc_u32 s17, s17, 0
	v_cndmask_b32_e64 v30, 0, v30, s[18:19]
	v_cndmask_b32_e64 v31, 0, v31, s[18:19]
	v_cndmask_b32_e64 v32, 0, v32, s[18:19]
	v_cndmask_b32_e64 v33, 0, v33, s[18:19]
	v_max3_f32 v41, |v18|, |v19|, |v20|
	v_max3_f32 v42, |v21|, |v22|, |v23|
	v_max3_f32 v43, |v24|, |v25|, |v26|
	v_max3_f32 v44, |v27|, |v28|, |v29|
	v_max3_f32 v48, |v30|, |v31|, |v32|
	v_max3_f32 v41, v41, v42, |v33|
	v_max3_f32 v43, v43, v44, v48
	v_max_f32_e32 v41, v41, v43
	v_pk_add_f32 v[2:3], v[2:3], v[18:19]
	v_pk_add_f32 v[4:5], v[4:5], v[20:21]
	v_max_f32_dpp v41, v41, v41 quad_perm:[1,0,3,2] row_mask:0xf bank_mask:0xf
	v_pk_add_f32 v[6:7], v[6:7], v[22:23]
	v_pk_add_f32 v[8:9], v[8:9], v[24:25]
	v_max_f32_dpp v41, v41, v41 quad_perm:[2,3,0,1] row_mask:0xf bank_mask:0xf
	v_pk_add_f32 v[10:11], v[10:11], v[26:27]
	v_pk_add_f32 v[12:13], v[12:13], v[28:29]
	v_max_f32_dpp v41, v41, v41 row_half_mirror row_mask:0xf bank_mask:0xf
	v_pk_add_f32 v[14:15], v[14:15], v[30:31]
	v_pk_add_f32 v[16:17], v[16:17], v[32:33]
	v_max_f32_dpp v41, v41, v41 row_mirror row_mask:0xf bank_mask:0xf
	s_nop 1
	v_max_f32_dpp v41, v41, v41 row_bcast:15 row_mask:0xa bank_mask:0xf
	s_nop 1
	v_max_f32_dpp v41, v41, v41 row_bcast:31 row_mask:0xc bank_mask:0xf
	s_nop 1
	v_readlane_b32 s28, v41, 63
	s_nop 1
	v_div_scale_f32 v48, s[30:31], s28, s28, v47
	v_rcp_f32_e32 v49, v48
	s_nop 0
	v_fma_f32 v50, -v48, v49, 1.0
	v_fmac_f32_e32 v49, v50, v49
	v_mov_b32_e32 v50, s28
	v_div_scale_f32 v50, vcc, s32, v50, s32
	v_mul_f32_e32 v51, v50, v49
	v_fma_f32 v52, -v48, v51, v50
	v_fmac_f32_e32 v51, v52, v49
	v_fma_f32 v48, -v48, v51, v50
	v_div_fmas_f32 v48, v48, v49, v51
	v_div_fixup_f32 v48, v48, s28, v47
	v_cmp_gt_f32_e64 vcc, s28, 0
	v_writelane_b32 v40, s28, 1
	s_nop 0
	v_cndmask_b32_e32 v48, 0, v48, vcc
	v_fmaak_f32 v49, v18, v48, 0x4b400000
	v_fmaak_f32 v50, v19, v48, 0x4b400000
	v_fmaak_f32 v51, v20, v48, 0x4b400000
	v_fmaak_f32 v52, v21, v48, 0x4b400000
	v_perm_b32 v49, v50, v49, s33
	v_perm_b32 v51, v52, v51, s34
	v_or_b32_e32 v60, v49, v51
	v_fmaak_f32 v41, v22, v48, 0x4b400000
	v_fmaak_f32 v42, v23, v48, 0x4b400000
	v_fmaak_f32 v43, v24, v48, 0x4b400000
	v_fmaak_f32 v44, v25, v48, 0x4b400000
	v_perm_b32 v41, v42, v41, s33
	v_perm_b32 v43, v44, v43, s34
	v_or_b32_e32 v61, v41, v43
	v_fmaak_f32 v49, v26, v48, 0x4b400000
	v_fmaak_f32 v50, v27, v48, 0x4b400000
	v_fmaak_f32 v51, v28, v48, 0x4b400000
	v_fmaak_f32 v52, v29, v48, 0x4b400000
	v_perm_b32 v49, v50, v49, s33
	v_perm_b32 v51, v52, v51, s34
	v_or_b32_e32 v62, v49, v51
	v_fmaak_f32 v41, v30, v48, 0x4b400000
	v_fmaak_f32 v42, v31, v48, 0x4b400000
	v_fmaak_f32 v43, v32, v48, 0x4b400000
	v_fmaak_f32 v44, v33, v48, 0x4b400000
	v_perm_b32 v41, v42, v41, s33
	v_perm_b32 v43, v44, v43, s34
	v_or_b32_e32 v63, v41, v43
	s_waitcnt vmcnt(0)
	ds_read_b128 v[18:21], v38 offset:0
	ds_read_b128 v[22:25], v38 offset:1024
	ds_read_b128 v[26:29], v38 offset:2048
	ds_read_b128 v[30:33], v38 offset:3072
	s_waitcnt lgkmcnt(0)
	s_mov_b32 m0, s36
	s_nop 0
	global_load_lds_dwordx4 v34, s[16:17] nt
	global_load_lds_dwordx4 v34, s[16:17] offset:1024 nt
	global_load_lds_dwordx4 v34, s[16:17] offset:2048 nt
	global_load_lds_dwordx4 v35, s[16:17] offset:3072 nt
	s_add_u32 s16, s16, 0x7d00
	s_addc_u32 s17, s17, 0
	v_cndmask_b32_e64 v30, 0, v30, s[18:19]
	v_cndmask_b32_e64 v31, 0, v31, s[18:19]
	v_cndmask_b32_e64 v32, 0, v32, s[18:19]
	v_cndmask_b32_e64 v33, 0, v33, s[18:19]
	v_max3_f32 v41, |v18|, |v19|, |v20|
	v_max3_f32 v42, |v21|, |v22|, |v23|
	v_max3_f32 v43, |v24|, |v25|, |v26|
	v_max3_f32 v44, |v27|, |v28|, |v29|
	v_max3_f32 v48, |v30|, |v31|, |v32|
	v_max3_f32 v41, v41, v42, |v33|
	v_max3_f32 v43, v43, v44, v48
	v_max_f32_e32 v41, v41, v43
	v_pk_add_f32 v[2:3], v[2:3], v[18:19]
	v_pk_add_f32 v[4:5], v[4:5], v[20:21]
	v_max_f32_dpp v41, v41, v41 quad_perm:[1,0,3,2] row_mask:0xf bank_mask:0xf
	v_pk_add_f32 v[6:7], v[6:7], v[22:23]
	v_pk_add_f32 v[8:9], v[8:9], v[24:25]
	v_max_f32_dpp v41, v41, v41 quad_perm:[2,3,0,1] row_mask:0xf bank_mask:0xf
	v_pk_add_f32 v[10:11], v[10:11], v[26:27]
	v_pk_add_f32 v[12:13], v[12:13], v[28:29]
	v_max_f32_dpp v41, v41, v41 row_half_mirror row_mask:0xf bank_mask:0xf
	v_pk_add_f32 v[14:15], v[14:15], v[30:31]
	v_pk_add_f32 v[16:17], v[16:17], v[32:33]
	v_max_f32_dpp v41, v41, v41 row_mirror row_mask:0xf bank_mask:0xf
	s_nop 1
	v_max_f32_dpp v41, v41, v41 row_bcast:15 row_mask:0xa bank_mask:0xf
	s_nop 1
	v_max_f32_dpp v41, v41, v41 row_bcast:31 row_mask:0xc bank_mask:0xf
	s_nop 1
	v_readlane_b32 s28, v41, 63
	s_nop 1
	v_div_scale_f32 v48, s[30:31], s28, s28, v47
	v_rcp_f32_e32 v49, v48
	s_nop 0
	v_fma_f32 v50, -v48, v49, 1.0
	v_fmac_f32_e32 v49, v50, v49
	v_mov_b32_e32 v50, s28
	v_div_scale_f32 v50, vcc, s32, v50, s32
	v_mul_f32_e32 v51, v50, v49
	v_fma_f32 v52, -v48, v51, v50
	v_fmac_f32_e32 v51, v52, v49
	v_fma_f32 v48, -v48, v51, v50
	v_div_fmas_f32 v48, v48, v49, v51
	v_div_fixup_f32 v48, v48, s28, v47
	v_cmp_gt_f32_e64 vcc, s28, 0
	v_writelane_b32 v40, s28, 2
	s_nop 0
	v_cndmask_b32_e32 v48, 0, v48, vcc
	v_fmaak_f32 v49, v18, v48, 0x4b400000
	v_fmaak_f32 v50, v19, v48, 0x4b400000
	v_fmaak_f32 v51, v20, v48, 0x4b400000
	v_fmaak_f32 v52, v21, v48, 0x4b400000
	v_perm_b32 v49, v50, v49, s33
	v_perm_b32 v51, v52, v51, s34
	v_or_b32_e32 v64, v49, v51
	v_fmaak_f32 v41, v22, v48, 0x4b400000
	v_fmaak_f32 v42, v23, v48, 0x4b400000
	v_fmaak_f32 v43, v24, v48, 0x4b400000
	v_fmaak_f32 v44, v25, v48, 0x4b400000
	v_perm_b32 v41, v42, v41, s33
	v_perm_b32 v43, v44, v43, s34
	v_or_b32_e32 v65, v41, v43
	v_fmaak_f32 v49, v26, v48, 0x4b400000
	v_fmaak_f32 v50, v27, v48, 0x4b400000
	v_fmaak_f32 v51, v28, v48, 0x4b400000
	v_fmaak_f32 v52, v29, v48, 0x4b400000
	v_perm_b32 v49, v50, v49, s33
	v_perm_b32 v51, v52, v51, s34
	v_or_b32_e32 v66, v49, v51
	v_fmaak_f32 v41, v30, v48, 0x4b400000
	v_fmaak_f32 v42, v31, v48, 0x4b400000
	v_fmaak_f32 v43, v32, v48, 0x4b400000
	v_fmaak_f32 v44, v33, v48, 0x4b400000
	v_perm_b32 v41, v42, v41, s33
	v_perm_b32 v43, v44, v43, s34
	v_or_b32_e32 v67, v41, v43
	s_waitcnt vmcnt(0)
	ds_read_b128 v[18:21], v38 offset:4096
	ds_read_b128 v[22:25], v38 offset:5120
	ds_read_b128 v[26:29], v38 offset:6144
	ds_read_b128 v[30:33], v38 offset:7168
	s_waitcnt lgkmcnt(0)
	s_mov_b32 m0, s35
	s_nop 0
	global_load_lds_dwordx4 v34, s[16:17] nt
	global_load_lds_dwordx4 v34, s[16:17] offset:1024 nt
	global_load_lds_dwordx4 v34, s[16:17] offset:2048 nt
	global_load_lds_dwordx4 v35, s[16:17] offset:3072 nt
	s_add_u32 s16, s16, 0x7d00
	s_addc_u32 s17, s17, 0
	v_cndmask_b32_e64 v30, 0, v30, s[18:19]
	v_cndmask_b32_e64 v31, 0, v31, s[18:19]
	v_cndmask_b32_e64 v32, 0, v32, s[18:19]
	v_cndmask_b32_e64 v33, 0, v33, s[18:19]
	v_max3_f32 v41, |v18|, |v19|, |v20|
	v_max3_f32 v42, |v21|, |v22|, |v23|
	v_max3_f32 v43, |v24|, |v25|, |v26|
	v_max3_f32 v44, |v27|, |v28|, |v29|
	v_max3_f32 v48, |v30|, |v31|, |v32|
	v_max3_f32 v41, v41, v42, |v33|
	v_max3_f32 v43, v43, v44, v48
	v_max_f32_e32 v41, v41, v43
	v_pk_add_f32 v[2:3], v[2:3], v[18:19]
	v_pk_add_f32 v[4:5], v[4:5], v[20:21]
	v_max_f32_dpp v41, v41, v41 quad_perm:[1,0,3,2] row_mask:0xf bank_mask:0xf
	v_pk_add_f32 v[6:7], v[6:7], v[22:23]
	v_pk_add_f32 v[8:9], v[8:9], v[24:25]
	v_max_f32_dpp v41, v41, v41 quad_perm:[2,3,0,1] row_mask:0xf bank_mask:0xf
	v_pk_add_f32 v[10:11], v[10:11], v[26:27]
	v_pk_add_f32 v[12:13], v[12:13], v[28:29]
	v_max_f32_dpp v41, v41, v41 row_half_mirror row_mask:0xf bank_mask:0xf
	v_pk_add_f32 v[14:15], v[14:15], v[30:31]
	v_pk_add_f32 v[16:17], v[16:17], v[32:33]
	v_max_f32_dpp v41, v41, v41 row_mirror row_mask:0xf bank_mask:0xf
	s_nop 1
	v_max_f32_dpp v41, v41, v41 row_bcast:15 row_mask:0xa bank_mask:0xf
	s_nop 1
	v_max_f32_dpp v41, v41, v41 row_bcast:31 row_mask:0xc bank_mask:0xf
	s_nop 1
	v_readlane_b32 s28, v41, 63
	s_nop 1
	v_div_scale_f32 v48, s[30:31], s28, s28, v47
	v_rcp_f32_e32 v49, v48
	s_nop 0
	v_fma_f32 v50, -v48, v49, 1.0
	v_fmac_f32_e32 v49, v50, v49
	v_mov_b32_e32 v50, s28
	v_div_scale_f32 v50, vcc, s32, v50, s32
	v_mul_f32_e32 v51, v50, v49
	v_fma_f32 v52, -v48, v51, v50
	v_fmac_f32_e32 v51, v52, v49
	v_fma_f32 v48, -v48, v51, v50
	v_div_fmas_f32 v48, v48, v49, v51
	v_div_fixup_f32 v48, v48, s28, v47
	v_cmp_gt_f32_e64 vcc, s28, 0
	v_writelane_b32 v40, s28, 3
	s_nop 0
	v_cndmask_b32_e32 v48, 0, v48, vcc
	v_fmaak_f32 v49, v18, v48, 0x4b400000
	v_fmaak_f32 v50, v19, v48, 0x4b400000
	v_fmaak_f32 v51, v20, v48, 0x4b400000
	v_fmaak_f32 v52, v21, v48, 0x4b400000
	v_perm_b32 v49, v50, v49, s33
	v_perm_b32 v51, v52, v51, s34
	v_or_b32_e32 v68, v49, v51
	v_fmaak_f32 v41, v22, v48, 0x4b400000
	v_fmaak_f32 v42, v23, v48, 0x4b400000
	v_fmaak_f32 v43, v24, v48, 0x4b400000
	v_fmaak_f32 v44, v25, v48, 0x4b400000
	v_perm_b32 v41, v42, v41, s33
	v_perm_b32 v43, v44, v43, s34
	v_or_b32_e32 v69, v41, v43
	v_fmaak_f32 v49, v26, v48, 0x4b400000
	v_fmaak_f32 v50, v27, v48, 0x4b400000
	v_fmaak_f32 v51, v28, v48, 0x4b400000
	v_fmaak_f32 v52, v29, v48, 0x4b400000
	v_perm_b32 v49, v50, v49, s33
	v_perm_b32 v51, v52, v51, s34
	v_or_b32_e32 v70, v49, v51
	v_fmaak_f32 v41, v30, v48, 0x4b400000
	v_fmaak_f32 v42, v31, v48, 0x4b400000
	v_fmaak_f32 v43, v32, v48, 0x4b400000
	v_fmaak_f32 v44, v33, v48, 0x4b400000
	v_perm_b32 v41, v42, v41, s33
	v_perm_b32 v43, v44, v43, s34
	v_or_b32_e32 v71, v41, v43
	s_waitcnt vmcnt(0)
	ds_read_b128 v[18:21], v38 offset:0
	ds_read_b128 v[22:25], v38 offset:1024
	ds_read_b128 v[26:29], v38 offset:2048
	ds_read_b128 v[30:33], v38 offset:3072
	s_waitcnt lgkmcnt(0)
	s_mov_b32 m0, s36
	s_nop 0
	global_load_lds_dwordx4 v34, s[16:17] nt
	global_load_lds_dwordx4 v34, s[16:17] offset:1024 nt
	global_load_lds_dwordx4 v34, s[16:17] offset:2048 nt
	global_load_lds_dwordx4 v35, s[16:17] offset:3072 nt
	s_add_u32 s16, s16, 0x7d00
	s_addc_u32 s17, s17, 0
	v_cndmask_b32_e64 v30, 0, v30, s[18:19]
	v_cndmask_b32_e64 v31, 0, v31, s[18:19]
	v_cndmask_b32_e64 v32, 0, v32, s[18:19]
	v_cndmask_b32_e64 v33, 0, v33, s[18:19]
	v_max3_f32 v41, |v18|, |v19|, |v20|
	v_max3_f32 v42, |v21|, |v22|, |v23|
	v_max3_f32 v43, |v24|, |v25|, |v26|
	v_max3_f32 v44, |v27|, |v28|, |v29|
	v_max3_f32 v48, |v30|, |v31|, |v32|
	v_max3_f32 v41, v41, v42, |v33|
	v_max3_f32 v43, v43, v44, v48
	v_max_f32_e32 v41, v41, v43
	v_pk_add_f32 v[2:3], v[2:3], v[18:19]
	v_pk_add_f32 v[4:5], v[4:5], v[20:21]
	v_max_f32_dpp v41, v41, v41 quad_perm:[1,0,3,2] row_mask:0xf bank_mask:0xf
	v_pk_add_f32 v[6:7], v[6:7], v[22:23]
	v_pk_add_f32 v[8:9], v[8:9], v[24:25]
	v_max_f32_dpp v41, v41, v41 quad_perm:[2,3,0,1] row_mask:0xf bank_mask:0xf
	v_pk_add_f32 v[10:11], v[10:11], v[26:27]
	v_pk_add_f32 v[12:13], v[12:13], v[28:29]
	v_max_f32_dpp v41, v41, v41 row_half_mirror row_mask:0xf bank_mask:0xf
	v_pk_add_f32 v[14:15], v[14:15], v[30:31]
	v_pk_add_f32 v[16:17], v[16:17], v[32:33]
	v_max_f32_dpp v41, v41, v41 row_mirror row_mask:0xf bank_mask:0xf
	s_nop 1
	v_max_f32_dpp v41, v41, v41 row_bcast:15 row_mask:0xa bank_mask:0xf
	s_nop 1
	v_max_f32_dpp v41, v41, v41 row_bcast:31 row_mask:0xc bank_mask:0xf
	s_nop 1
	v_readlane_b32 s28, v41, 63
	s_nop 1
	v_div_scale_f32 v48, s[30:31], s28, s28, v47
	v_rcp_f32_e32 v49, v48
	s_nop 0
	v_fma_f32 v50, -v48, v49, 1.0
	v_fmac_f32_e32 v49, v50, v49
	v_mov_b32_e32 v50, s28
	v_div_scale_f32 v50, vcc, s32, v50, s32
	v_mul_f32_e32 v51, v50, v49
	v_fma_f32 v52, -v48, v51, v50
	v_fmac_f32_e32 v51, v52, v49
	v_fma_f32 v48, -v48, v51, v50
	v_div_fmas_f32 v48, v48, v49, v51
	v_div_fixup_f32 v48, v48, s28, v47
	v_cmp_gt_f32_e64 vcc, s28, 0
	v_writelane_b32 v40, s28, 4
	s_nop 0
	v_cndmask_b32_e32 v48, 0, v48, vcc
	v_fmaak_f32 v49, v18, v48, 0x4b400000
	v_fmaak_f32 v50, v19, v48, 0x4b400000
	v_fmaak_f32 v51, v20, v48, 0x4b400000
	v_fmaak_f32 v52, v21, v48, 0x4b400000
	v_perm_b32 v49, v50, v49, s33
	v_perm_b32 v51, v52, v51, s34
	v_or_b32_e32 v72, v49, v51
	v_fmaak_f32 v41, v22, v48, 0x4b400000
	v_fmaak_f32 v42, v23, v48, 0x4b400000
	v_fmaak_f32 v43, v24, v48, 0x4b400000
	v_fmaak_f32 v44, v25, v48, 0x4b400000
	v_perm_b32 v41, v42, v41, s33
	v_perm_b32 v43, v44, v43, s34
	v_or_b32_e32 v73, v41, v43
	v_fmaak_f32 v49, v26, v48, 0x4b400000
	v_fmaak_f32 v50, v27, v48, 0x4b400000
	v_fmaak_f32 v51, v28, v48, 0x4b400000
	v_fmaak_f32 v52, v29, v48, 0x4b400000
	v_perm_b32 v49, v50, v49, s33
	v_perm_b32 v51, v52, v51, s34
	v_or_b32_e32 v74, v49, v51
	v_fmaak_f32 v41, v30, v48, 0x4b400000
	v_fmaak_f32 v42, v31, v48, 0x4b400000
	v_fmaak_f32 v43, v32, v48, 0x4b400000
	v_fmaak_f32 v44, v33, v48, 0x4b400000
	v_perm_b32 v41, v42, v41, s33
	v_perm_b32 v43, v44, v43, s34
	v_or_b32_e32 v75, v41, v43
	s_waitcnt vmcnt(0)
	ds_read_b128 v[18:21], v38 offset:4096
	ds_read_b128 v[22:25], v38 offset:5120
	ds_read_b128 v[26:29], v38 offset:6144
	ds_read_b128 v[30:33], v38 offset:7168
	s_waitcnt lgkmcnt(0)
	s_mov_b32 m0, s35
	s_nop 0
	global_load_lds_dwordx4 v34, s[16:17] nt
	global_load_lds_dwordx4 v34, s[16:17] offset:1024 nt
	global_load_lds_dwordx4 v34, s[16:17] offset:2048 nt
	global_load_lds_dwordx4 v35, s[16:17] offset:3072 nt
	s_add_u32 s16, s16, 0x7d00
	s_addc_u32 s17, s17, 0
	v_cndmask_b32_e64 v30, 0, v30, s[18:19]
	v_cndmask_b32_e64 v31, 0, v31, s[18:19]
	v_cndmask_b32_e64 v32, 0, v32, s[18:19]
	v_cndmask_b32_e64 v33, 0, v33, s[18:19]
	v_max3_f32 v41, |v18|, |v19|, |v20|
	v_max3_f32 v42, |v21|, |v22|, |v23|
	v_max3_f32 v43, |v24|, |v25|, |v26|
	v_max3_f32 v44, |v27|, |v28|, |v29|
	v_max3_f32 v48, |v30|, |v31|, |v32|
	v_max3_f32 v41, v41, v42, |v33|
	v_max3_f32 v43, v43, v44, v48
	v_max_f32_e32 v41, v41, v43
	v_pk_add_f32 v[2:3], v[2:3], v[18:19]
	v_pk_add_f32 v[4:5], v[4:5], v[20:21]
	v_max_f32_dpp v41, v41, v41 quad_perm:[1,0,3,2] row_mask:0xf bank_mask:0xf
	v_pk_add_f32 v[6:7], v[6:7], v[22:23]
	v_pk_add_f32 v[8:9], v[8:9], v[24:25]
	v_max_f32_dpp v41, v41, v41 quad_perm:[2,3,0,1] row_mask:0xf bank_mask:0xf
	v_pk_add_f32 v[10:11], v[10:11], v[26:27]
	v_pk_add_f32 v[12:13], v[12:13], v[28:29]
	v_max_f32_dpp v41, v41, v41 row_half_mirror row_mask:0xf bank_mask:0xf
	v_pk_add_f32 v[14:15], v[14:15], v[30:31]
	v_pk_add_f32 v[16:17], v[16:17], v[32:33]
	v_max_f32_dpp v41, v41, v41 row_mirror row_mask:0xf bank_mask:0xf
	s_nop 1
	v_max_f32_dpp v41, v41, v41 row_bcast:15 row_mask:0xa bank_mask:0xf
	s_nop 1
	v_max_f32_dpp v41, v41, v41 row_bcast:31 row_mask:0xc bank_mask:0xf
	s_nop 1
	v_readlane_b32 s28, v41, 63
	s_nop 1
	v_div_scale_f32 v48, s[30:31], s28, s28, v47
	v_rcp_f32_e32 v49, v48
	s_nop 0
	v_fma_f32 v50, -v48, v49, 1.0
	v_fmac_f32_e32 v49, v50, v49
	v_mov_b32_e32 v50, s28
	v_div_scale_f32 v50, vcc, s32, v50, s32
	v_mul_f32_e32 v51, v50, v49
	v_fma_f32 v52, -v48, v51, v50
	v_fmac_f32_e32 v51, v52, v49
	v_fma_f32 v48, -v48, v51, v50
	v_div_fmas_f32 v48, v48, v49, v51
	v_div_fixup_f32 v48, v48, s28, v47
	v_cmp_gt_f32_e64 vcc, s28, 0
	v_writelane_b32 v40, s28, 5
	s_nop 0
	v_cndmask_b32_e32 v48, 0, v48, vcc
	v_fmaak_f32 v49, v18, v48, 0x4b400000
	v_fmaak_f32 v50, v19, v48, 0x4b400000
	v_fmaak_f32 v51, v20, v48, 0x4b400000
	v_fmaak_f32 v52, v21, v48, 0x4b400000
	v_perm_b32 v49, v50, v49, s33
	v_perm_b32 v51, v52, v51, s34
	v_or_b32_e32 v76, v49, v51
	v_fmaak_f32 v41, v22, v48, 0x4b400000
	v_fmaak_f32 v42, v23, v48, 0x4b400000
	v_fmaak_f32 v43, v24, v48, 0x4b400000
	v_fmaak_f32 v44, v25, v48, 0x4b400000
	v_perm_b32 v41, v42, v41, s33
	v_perm_b32 v43, v44, v43, s34
	v_or_b32_e32 v77, v41, v43
	v_fmaak_f32 v49, v26, v48, 0x4b400000
	v_fmaak_f32 v50, v27, v48, 0x4b400000
	v_fmaak_f32 v51, v28, v48, 0x4b400000
	v_fmaak_f32 v52, v29, v48, 0x4b400000
	v_perm_b32 v49, v50, v49, s33
	v_perm_b32 v51, v52, v51, s34
	v_or_b32_e32 v78, v49, v51
	v_fmaak_f32 v41, v30, v48, 0x4b400000
	v_fmaak_f32 v42, v31, v48, 0x4b400000
	v_fmaak_f32 v43, v32, v48, 0x4b400000
	v_fmaak_f32 v44, v33, v48, 0x4b400000
	v_perm_b32 v41, v42, v41, s33
	v_perm_b32 v43, v44, v43, s34
	v_or_b32_e32 v79, v41, v43
	s_waitcnt vmcnt(0)
	ds_read_b128 v[18:21], v38 offset:0
	ds_read_b128 v[22:25], v38 offset:1024
	ds_read_b128 v[26:29], v38 offset:2048
	ds_read_b128 v[30:33], v38 offset:3072
	s_waitcnt lgkmcnt(0)
	s_mov_b32 m0, s36
	s_nop 0
	global_load_lds_dwordx4 v34, s[16:17] nt
	global_load_lds_dwordx4 v34, s[16:17] offset:1024 nt
	global_load_lds_dwordx4 v34, s[16:17] offset:2048 nt
	global_load_lds_dwordx4 v35, s[16:17] offset:3072 nt
	s_add_u32 s16, s16, 0x7d00
	s_addc_u32 s17, s17, 0
	v_cndmask_b32_e64 v30, 0, v30, s[18:19]
	v_cndmask_b32_e64 v31, 0, v31, s[18:19]
	v_cndmask_b32_e64 v32, 0, v32, s[18:19]
	v_cndmask_b32_e64 v33, 0, v33, s[18:19]
	v_max3_f32 v41, |v18|, |v19|, |v20|
	v_max3_f32 v42, |v21|, |v22|, |v23|
	v_max3_f32 v43, |v24|, |v25|, |v26|
	v_max3_f32 v44, |v27|, |v28|, |v29|
	v_max3_f32 v48, |v30|, |v31|, |v32|
	v_max3_f32 v41, v41, v42, |v33|
	v_max3_f32 v43, v43, v44, v48
	v_max_f32_e32 v41, v41, v43
	v_pk_add_f32 v[2:3], v[2:3], v[18:19]
	v_pk_add_f32 v[4:5], v[4:5], v[20:21]
	v_max_f32_dpp v41, v41, v41 quad_perm:[1,0,3,2] row_mask:0xf bank_mask:0xf
	v_pk_add_f32 v[6:7], v[6:7], v[22:23]
	v_pk_add_f32 v[8:9], v[8:9], v[24:25]
	v_max_f32_dpp v41, v41, v41 quad_perm:[2,3,0,1] row_mask:0xf bank_mask:0xf
	v_pk_add_f32 v[10:11], v[10:11], v[26:27]
	v_pk_add_f32 v[12:13], v[12:13], v[28:29]
	v_max_f32_dpp v41, v41, v41 row_half_mirror row_mask:0xf bank_mask:0xf
	v_pk_add_f32 v[14:15], v[14:15], v[30:31]
	v_pk_add_f32 v[16:17], v[16:17], v[32:33]
	v_max_f32_dpp v41, v41, v41 row_mirror row_mask:0xf bank_mask:0xf
	s_nop 1
	v_max_f32_dpp v41, v41, v41 row_bcast:15 row_mask:0xa bank_mask:0xf
	s_nop 1
	v_max_f32_dpp v41, v41, v41 row_bcast:31 row_mask:0xc bank_mask:0xf
	s_nop 1
	v_readlane_b32 s28, v41, 63
	s_nop 1
	v_div_scale_f32 v48, s[30:31], s28, s28, v47
	v_rcp_f32_e32 v49, v48
	s_nop 0
	v_fma_f32 v50, -v48, v49, 1.0
	v_fmac_f32_e32 v49, v50, v49
	v_mov_b32_e32 v50, s28
	v_div_scale_f32 v50, vcc, s32, v50, s32
	v_mul_f32_e32 v51, v50, v49
	v_fma_f32 v52, -v48, v51, v50
	v_fmac_f32_e32 v51, v52, v49
	v_fma_f32 v48, -v48, v51, v50
	v_div_fmas_f32 v48, v48, v49, v51
	v_div_fixup_f32 v48, v48, s28, v47
	v_cmp_gt_f32_e64 vcc, s28, 0
	v_writelane_b32 v40, s28, 6
	s_nop 0
	v_cndmask_b32_e32 v48, 0, v48, vcc
	v_fmaak_f32 v49, v18, v48, 0x4b400000
	v_fmaak_f32 v50, v19, v48, 0x4b400000
	v_fmaak_f32 v51, v20, v48, 0x4b400000
	v_fmaak_f32 v52, v21, v48, 0x4b400000
	v_perm_b32 v49, v50, v49, s33
	v_perm_b32 v51, v52, v51, s34
	v_or_b32_e32 v80, v49, v51
	v_fmaak_f32 v41, v22, v48, 0x4b400000
	v_fmaak_f32 v42, v23, v48, 0x4b400000
	v_fmaak_f32 v43, v24, v48, 0x4b400000
	v_fmaak_f32 v44, v25, v48, 0x4b400000
	v_perm_b32 v41, v42, v41, s33
	v_perm_b32 v43, v44, v43, s34
	v_or_b32_e32 v81, v41, v43
	v_fmaak_f32 v49, v26, v48, 0x4b400000
	v_fmaak_f32 v50, v27, v48, 0x4b400000
	v_fmaak_f32 v51, v28, v48, 0x4b400000
	v_fmaak_f32 v52, v29, v48, 0x4b400000
	v_perm_b32 v49, v50, v49, s33
	v_perm_b32 v51, v52, v51, s34
	v_or_b32_e32 v82, v49, v51
	v_fmaak_f32 v41, v30, v48, 0x4b400000
	v_fmaak_f32 v42, v31, v48, 0x4b400000
	v_fmaak_f32 v43, v32, v48, 0x4b400000
	v_fmaak_f32 v44, v33, v48, 0x4b400000
	v_perm_b32 v41, v42, v41, s33
	v_perm_b32 v43, v44, v43, s34
	v_or_b32_e32 v83, v41, v43
	s_waitcnt vmcnt(0)
	ds_read_b128 v[18:21], v38 offset:4096
	ds_read_b128 v[22:25], v38 offset:5120
	ds_read_b128 v[26:29], v38 offset:6144
	ds_read_b128 v[30:33], v38 offset:7168
	s_waitcnt lgkmcnt(0)
	s_mov_b32 m0, s35
	s_nop 0
	global_load_lds_dwordx4 v34, s[16:17] nt
	global_load_lds_dwordx4 v34, s[16:17] offset:1024 nt
	global_load_lds_dwordx4 v34, s[16:17] offset:2048 nt
	global_load_lds_dwordx4 v35, s[16:17] offset:3072 nt
	s_add_u32 s16, s16, 0x7d00
	s_addc_u32 s17, s17, 0
	v_cndmask_b32_e64 v30, 0, v30, s[18:19]
	v_cndmask_b32_e64 v31, 0, v31, s[18:19]
	v_cndmask_b32_e64 v32, 0, v32, s[18:19]
	v_cndmask_b32_e64 v33, 0, v33, s[18:19]
	v_max3_f32 v41, |v18|, |v19|, |v20|
	v_max3_f32 v42, |v21|, |v22|, |v23|
	v_max3_f32 v43, |v24|, |v25|, |v26|
	v_max3_f32 v44, |v27|, |v28|, |v29|
	v_max3_f32 v48, |v30|, |v31|, |v32|
	v_max3_f32 v41, v41, v42, |v33|
	v_max3_f32 v43, v43, v44, v48
	v_max_f32_e32 v41, v41, v43
	v_pk_add_f32 v[2:3], v[2:3], v[18:19]
	v_pk_add_f32 v[4:5], v[4:5], v[20:21]
	v_max_f32_dpp v41, v41, v41 quad_perm:[1,0,3,2] row_mask:0xf bank_mask:0xf
	v_pk_add_f32 v[6:7], v[6:7], v[22:23]
	v_pk_add_f32 v[8:9], v[8:9], v[24:25]
	v_max_f32_dpp v41, v41, v41 quad_perm:[2,3,0,1] row_mask:0xf bank_mask:0xf
	v_pk_add_f32 v[10:11], v[10:11], v[26:27]
	v_pk_add_f32 v[12:13], v[12:13], v[28:29]
	v_max_f32_dpp v41, v41, v41 row_half_mirror row_mask:0xf bank_mask:0xf
	v_pk_add_f32 v[14:15], v[14:15], v[30:31]
	v_pk_add_f32 v[16:17], v[16:17], v[32:33]
	v_max_f32_dpp v41, v41, v41 row_mirror row_mask:0xf bank_mask:0xf
	s_nop 1
	v_max_f32_dpp v41, v41, v41 row_bcast:15 row_mask:0xa bank_mask:0xf
	s_nop 1
	v_max_f32_dpp v41, v41, v41 row_bcast:31 row_mask:0xc bank_mask:0xf
	s_nop 1
	v_readlane_b32 s28, v41, 63
	s_nop 1
	v_div_scale_f32 v48, s[30:31], s28, s28, v47
	v_rcp_f32_e32 v49, v48
	s_nop 0
	v_fma_f32 v50, -v48, v49, 1.0
	v_fmac_f32_e32 v49, v50, v49
	v_mov_b32_e32 v50, s28
	v_div_scale_f32 v50, vcc, s32, v50, s32
	v_mul_f32_e32 v51, v50, v49
	v_fma_f32 v52, -v48, v51, v50
	v_fmac_f32_e32 v51, v52, v49
	v_fma_f32 v48, -v48, v51, v50
	v_div_fmas_f32 v48, v48, v49, v51
	v_div_fixup_f32 v48, v48, s28, v47
	v_cmp_gt_f32_e64 vcc, s28, 0
	v_writelane_b32 v40, s28, 7
	s_nop 0
	v_cndmask_b32_e32 v48, 0, v48, vcc
	v_fmaak_f32 v49, v18, v48, 0x4b400000
	v_fmaak_f32 v50, v19, v48, 0x4b400000
	v_fmaak_f32 v51, v20, v48, 0x4b400000
	v_fmaak_f32 v52, v21, v48, 0x4b400000
	v_perm_b32 v49, v50, v49, s33
	v_perm_b32 v51, v52, v51, s34
	v_or_b32_e32 v84, v49, v51
	v_fmaak_f32 v41, v22, v48, 0x4b400000
	v_fmaak_f32 v42, v23, v48, 0x4b400000
	v_fmaak_f32 v43, v24, v48, 0x4b400000
	v_fmaak_f32 v44, v25, v48, 0x4b400000
	v_perm_b32 v41, v42, v41, s33
	v_perm_b32 v43, v44, v43, s34
	v_or_b32_e32 v85, v41, v43
	v_fmaak_f32 v49, v26, v48, 0x4b400000
	v_fmaak_f32 v50, v27, v48, 0x4b400000
	v_fmaak_f32 v51, v28, v48, 0x4b400000
	v_fmaak_f32 v52, v29, v48, 0x4b400000
	v_perm_b32 v49, v50, v49, s33
	v_perm_b32 v51, v52, v51, s34
	v_or_b32_e32 v86, v49, v51
	v_fmaak_f32 v41, v30, v48, 0x4b400000
	v_fmaak_f32 v42, v31, v48, 0x4b400000
	v_fmaak_f32 v43, v32, v48, 0x4b400000
	v_fmaak_f32 v44, v33, v48, 0x4b400000
	v_perm_b32 v41, v42, v41, s33
	v_perm_b32 v43, v44, v43, s34
	v_or_b32_e32 v87, v41, v43
	s_waitcnt vmcnt(0)
	ds_read_b128 v[18:21], v38 offset:0
	ds_read_b128 v[22:25], v38 offset:1024
	ds_read_b128 v[26:29], v38 offset:2048
	ds_read_b128 v[30:33], v38 offset:3072
	s_waitcnt lgkmcnt(0)
	s_mov_b32 m0, s36
	s_nop 0
	global_load_lds_dwordx4 v34, s[16:17] nt
	global_load_lds_dwordx4 v34, s[16:17] offset:1024 nt
	global_load_lds_dwordx4 v34, s[16:17] offset:2048 nt
	global_load_lds_dwordx4 v35, s[16:17] offset:3072 nt
	s_add_u32 s16, s16, 0x7d00
	s_addc_u32 s17, s17, 0
	v_cndmask_b32_e64 v30, 0, v30, s[18:19]
	v_cndmask_b32_e64 v31, 0, v31, s[18:19]
	v_cndmask_b32_e64 v32, 0, v32, s[18:19]
	v_cndmask_b32_e64 v33, 0, v33, s[18:19]
	v_max3_f32 v41, |v18|, |v19|, |v20|
	v_max3_f32 v42, |v21|, |v22|, |v23|
	v_max3_f32 v43, |v24|, |v25|, |v26|
	v_max3_f32 v44, |v27|, |v28|, |v29|
	v_max3_f32 v48, |v30|, |v31|, |v32|
	v_max3_f32 v41, v41, v42, |v33|
	v_max3_f32 v43, v43, v44, v48
	v_max_f32_e32 v41, v41, v43
	v_pk_add_f32 v[2:3], v[2:3], v[18:19]
	v_pk_add_f32 v[4:5], v[4:5], v[20:21]
	v_max_f32_dpp v41, v41, v41 quad_perm:[1,0,3,2] row_mask:0xf bank_mask:0xf
	v_pk_add_f32 v[6:7], v[6:7], v[22:23]
	v_pk_add_f32 v[8:9], v[8:9], v[24:25]
	v_max_f32_dpp v41, v41, v41 quad_perm:[2,3,0,1] row_mask:0xf bank_mask:0xf
	v_pk_add_f32 v[10:11], v[10:11], v[26:27]
	v_pk_add_f32 v[12:13], v[12:13], v[28:29]
	v_max_f32_dpp v41, v41, v41 row_half_mirror row_mask:0xf bank_mask:0xf
	v_pk_add_f32 v[14:15], v[14:15], v[30:31]
	v_pk_add_f32 v[16:17], v[16:17], v[32:33]
	v_max_f32_dpp v41, v41, v41 row_mirror row_mask:0xf bank_mask:0xf
	s_nop 1
	v_max_f32_dpp v41, v41, v41 row_bcast:15 row_mask:0xa bank_mask:0xf
	s_nop 1
	v_max_f32_dpp v41, v41, v41 row_bcast:31 row_mask:0xc bank_mask:0xf
	s_nop 1
	v_readlane_b32 s28, v41, 63
	s_nop 1
	v_div_scale_f32 v48, s[30:31], s28, s28, v47
	v_rcp_f32_e32 v49, v48
	s_nop 0
	v_fma_f32 v50, -v48, v49, 1.0
	v_fmac_f32_e32 v49, v50, v49
	v_mov_b32_e32 v50, s28
	v_div_scale_f32 v50, vcc, s32, v50, s32
	v_mul_f32_e32 v51, v50, v49
	v_fma_f32 v52, -v48, v51, v50
	v_fmac_f32_e32 v51, v52, v49
	v_fma_f32 v48, -v48, v51, v50
	v_div_fmas_f32 v48, v48, v49, v51
	v_div_fixup_f32 v48, v48, s28, v47
	v_cmp_gt_f32_e64 vcc, s28, 0
	v_writelane_b32 v40, s28, 8
	s_nop 0
	v_cndmask_b32_e32 v48, 0, v48, vcc
	v_fmaak_f32 v49, v18, v48, 0x4b400000
	v_fmaak_f32 v50, v19, v48, 0x4b400000
	v_fmaak_f32 v51, v20, v48, 0x4b400000
	v_fmaak_f32 v52, v21, v48, 0x4b400000
	v_perm_b32 v49, v50, v49, s33
	v_perm_b32 v51, v52, v51, s34
	v_or_b32_e32 v88, v49, v51
	v_fmaak_f32 v41, v22, v48, 0x4b400000
	v_fmaak_f32 v42, v23, v48, 0x4b400000
	v_fmaak_f32 v43, v24, v48, 0x4b400000
	v_fmaak_f32 v44, v25, v48, 0x4b400000
	v_perm_b32 v41, v42, v41, s33
	v_perm_b32 v43, v44, v43, s34
	v_or_b32_e32 v89, v41, v43
	v_fmaak_f32 v49, v26, v48, 0x4b400000
	v_fmaak_f32 v50, v27, v48, 0x4b400000
	v_fmaak_f32 v51, v28, v48, 0x4b400000
	v_fmaak_f32 v52, v29, v48, 0x4b400000
	v_perm_b32 v49, v50, v49, s33
	v_perm_b32 v51, v52, v51, s34
	v_or_b32_e32 v90, v49, v51
	v_fmaak_f32 v41, v30, v48, 0x4b400000
	v_fmaak_f32 v42, v31, v48, 0x4b400000
	v_fmaak_f32 v43, v32, v48, 0x4b400000
	v_fmaak_f32 v44, v33, v48, 0x4b400000
	v_perm_b32 v41, v42, v41, s33
	v_perm_b32 v43, v44, v43, s34
	v_or_b32_e32 v91, v41, v43
	s_waitcnt vmcnt(0)
	ds_read_b128 v[18:21], v38 offset:4096
	ds_read_b128 v[22:25], v38 offset:5120
	ds_read_b128 v[26:29], v38 offset:6144
	ds_read_b128 v[30:33], v38 offset:7168
	s_waitcnt lgkmcnt(0)
	s_mov_b32 m0, s35
	s_nop 0
	global_load_lds_dwordx4 v34, s[16:17] nt
	global_load_lds_dwordx4 v34, s[16:17] offset:1024 nt
	global_load_lds_dwordx4 v34, s[16:17] offset:2048 nt
	global_load_lds_dwordx4 v35, s[16:17] offset:3072 nt
	s_add_u32 s16, s16, 0x7d00
	s_addc_u32 s17, s17, 0
	v_cndmask_b32_e64 v30, 0, v30, s[18:19]
	v_cndmask_b32_e64 v31, 0, v31, s[18:19]
	v_cndmask_b32_e64 v32, 0, v32, s[18:19]
	v_cndmask_b32_e64 v33, 0, v33, s[18:19]
	v_max3_f32 v41, |v18|, |v19|, |v20|
	v_max3_f32 v42, |v21|, |v22|, |v23|
	v_max3_f32 v43, |v24|, |v25|, |v26|
	v_max3_f32 v44, |v27|, |v28|, |v29|
	v_max3_f32 v48, |v30|, |v31|, |v32|
	v_max3_f32 v41, v41, v42, |v33|
	v_max3_f32 v43, v43, v44, v48
	v_max_f32_e32 v41, v41, v43
	v_pk_add_f32 v[2:3], v[2:3], v[18:19]
	v_pk_add_f32 v[4:5], v[4:5], v[20:21]
	v_max_f32_dpp v41, v41, v41 quad_perm:[1,0,3,2] row_mask:0xf bank_mask:0xf
	v_pk_add_f32 v[6:7], v[6:7], v[22:23]
	v_pk_add_f32 v[8:9], v[8:9], v[24:25]
	v_max_f32_dpp v41, v41, v41 quad_perm:[2,3,0,1] row_mask:0xf bank_mask:0xf
	v_pk_add_f32 v[10:11], v[10:11], v[26:27]
	v_pk_add_f32 v[12:13], v[12:13], v[28:29]
	v_max_f32_dpp v41, v41, v41 row_half_mirror row_mask:0xf bank_mask:0xf
	v_pk_add_f32 v[14:15], v[14:15], v[30:31]
	v_pk_add_f32 v[16:17], v[16:17], v[32:33]
	v_max_f32_dpp v41, v41, v41 row_mirror row_mask:0xf bank_mask:0xf
	s_nop 1
	v_max_f32_dpp v41, v41, v41 row_bcast:15 row_mask:0xa bank_mask:0xf
	s_nop 1
	v_max_f32_dpp v41, v41, v41 row_bcast:31 row_mask:0xc bank_mask:0xf
	s_nop 1
	v_readlane_b32 s28, v41, 63
	s_nop 1
	v_div_scale_f32 v48, s[30:31], s28, s28, v47
	v_rcp_f32_e32 v49, v48
	s_nop 0
	v_fma_f32 v50, -v48, v49, 1.0
	v_fmac_f32_e32 v49, v50, v49
	v_mov_b32_e32 v50, s28
	v_div_scale_f32 v50, vcc, s32, v50, s32
	v_mul_f32_e32 v51, v50, v49
	v_fma_f32 v52, -v48, v51, v50
	v_fmac_f32_e32 v51, v52, v49
	v_fma_f32 v48, -v48, v51, v50
	v_div_fmas_f32 v48, v48, v49, v51
	v_div_fixup_f32 v48, v48, s28, v47
	v_cmp_gt_f32_e64 vcc, s28, 0
	v_writelane_b32 v40, s28, 9
	s_nop 0
	v_cndmask_b32_e32 v48, 0, v48, vcc
	v_fmaak_f32 v49, v18, v48, 0x4b400000
	v_fmaak_f32 v50, v19, v48, 0x4b400000
	v_fmaak_f32 v51, v20, v48, 0x4b400000
	v_fmaak_f32 v52, v21, v48, 0x4b400000
	v_perm_b32 v49, v50, v49, s33
	v_perm_b32 v51, v52, v51, s34
	v_or_b32_e32 v92, v49, v51
	v_fmaak_f32 v41, v22, v48, 0x4b400000
	v_fmaak_f32 v42, v23, v48, 0x4b400000
	v_fmaak_f32 v43, v24, v48, 0x4b400000
	v_fmaak_f32 v44, v25, v48, 0x4b400000
	v_perm_b32 v41, v42, v41, s33
	v_perm_b32 v43, v44, v43, s34
	v_or_b32_e32 v93, v41, v43
	v_fmaak_f32 v49, v26, v48, 0x4b400000
	v_fmaak_f32 v50, v27, v48, 0x4b400000
	v_fmaak_f32 v51, v28, v48, 0x4b400000
	v_fmaak_f32 v52, v29, v48, 0x4b400000
	v_perm_b32 v49, v50, v49, s33
	v_perm_b32 v51, v52, v51, s34
	v_or_b32_e32 v94, v49, v51
	v_fmaak_f32 v41, v30, v48, 0x4b400000
	v_fmaak_f32 v42, v31, v48, 0x4b400000
	v_fmaak_f32 v43, v32, v48, 0x4b400000
	v_fmaak_f32 v44, v33, v48, 0x4b400000
	v_perm_b32 v41, v42, v41, s33
	v_perm_b32 v43, v44, v43, s34
	v_or_b32_e32 v95, v41, v43
	s_waitcnt vmcnt(0)
	ds_read_b128 v[18:21], v38 offset:0
	ds_read_b128 v[22:25], v38 offset:1024
	ds_read_b128 v[26:29], v38 offset:2048
	ds_read_b128 v[30:33], v38 offset:3072
	s_waitcnt lgkmcnt(0)
	s_mov_b32 m0, s36
	s_nop 0
	global_load_lds_dwordx4 v34, s[16:17] nt
	global_load_lds_dwordx4 v34, s[16:17] offset:1024 nt
	global_load_lds_dwordx4 v34, s[16:17] offset:2048 nt
	global_load_lds_dwordx4 v35, s[16:17] offset:3072 nt
	s_add_u32 s16, s16, 0x7d00
	s_addc_u32 s17, s17, 0
	v_cndmask_b32_e64 v30, 0, v30, s[18:19]
	v_cndmask_b32_e64 v31, 0, v31, s[18:19]
	v_cndmask_b32_e64 v32, 0, v32, s[18:19]
	v_cndmask_b32_e64 v33, 0, v33, s[18:19]
	v_max3_f32 v41, |v18|, |v19|, |v20|
	v_max3_f32 v42, |v21|, |v22|, |v23|
	v_max3_f32 v43, |v24|, |v25|, |v26|
	v_max3_f32 v44, |v27|, |v28|, |v29|
	v_max3_f32 v48, |v30|, |v31|, |v32|
	v_max3_f32 v41, v41, v42, |v33|
	v_max3_f32 v43, v43, v44, v48
	v_max_f32_e32 v41, v41, v43
	v_pk_add_f32 v[2:3], v[2:3], v[18:19]
	v_pk_add_f32 v[4:5], v[4:5], v[20:21]
	v_max_f32_dpp v41, v41, v41 quad_perm:[1,0,3,2] row_mask:0xf bank_mask:0xf
	v_pk_add_f32 v[6:7], v[6:7], v[22:23]
	v_pk_add_f32 v[8:9], v[8:9], v[24:25]
	v_max_f32_dpp v41, v41, v41 quad_perm:[2,3,0,1] row_mask:0xf bank_mask:0xf
	v_pk_add_f32 v[10:11], v[10:11], v[26:27]
	v_pk_add_f32 v[12:13], v[12:13], v[28:29]
	v_max_f32_dpp v41, v41, v41 row_half_mirror row_mask:0xf bank_mask:0xf
	v_pk_add_f32 v[14:15], v[14:15], v[30:31]
	v_pk_add_f32 v[16:17], v[16:17], v[32:33]
	v_max_f32_dpp v41, v41, v41 row_mirror row_mask:0xf bank_mask:0xf
	s_nop 1
	v_max_f32_dpp v41, v41, v41 row_bcast:15 row_mask:0xa bank_mask:0xf
	s_nop 1
	v_max_f32_dpp v41, v41, v41 row_bcast:31 row_mask:0xc bank_mask:0xf
	s_nop 1
	v_readlane_b32 s28, v41, 63
	s_nop 1
	v_div_scale_f32 v48, s[30:31], s28, s28, v47
	v_rcp_f32_e32 v49, v48
	s_nop 0
	v_fma_f32 v50, -v48, v49, 1.0
	v_fmac_f32_e32 v49, v50, v49
	v_mov_b32_e32 v50, s28
	v_div_scale_f32 v50, vcc, s32, v50, s32
	v_mul_f32_e32 v51, v50, v49
	v_fma_f32 v52, -v48, v51, v50
	v_fmac_f32_e32 v51, v52, v49
	v_fma_f32 v48, -v48, v51, v50
	v_div_fmas_f32 v48, v48, v49, v51
	v_div_fixup_f32 v48, v48, s28, v47
	v_cmp_gt_f32_e64 vcc, s28, 0
	v_writelane_b32 v40, s28, 10
	s_nop 0
	v_cndmask_b32_e32 v48, 0, v48, vcc
	v_fmaak_f32 v49, v18, v48, 0x4b400000
	v_fmaak_f32 v50, v19, v48, 0x4b400000
	v_fmaak_f32 v51, v20, v48, 0x4b400000
	v_fmaak_f32 v52, v21, v48, 0x4b400000
	v_perm_b32 v49, v50, v49, s33
	v_perm_b32 v51, v52, v51, s34
	v_or_b32_e32 v96, v49, v51
	v_fmaak_f32 v41, v22, v48, 0x4b400000
	v_fmaak_f32 v42, v23, v48, 0x4b400000
	v_fmaak_f32 v43, v24, v48, 0x4b400000
	v_fmaak_f32 v44, v25, v48, 0x4b400000
	v_perm_b32 v41, v42, v41, s33
	v_perm_b32 v43, v44, v43, s34
	v_or_b32_e32 v97, v41, v43
	v_fmaak_f32 v49, v26, v48, 0x4b400000
	v_fmaak_f32 v50, v27, v48, 0x4b400000
	v_fmaak_f32 v51, v28, v48, 0x4b400000
	v_fmaak_f32 v52, v29, v48, 0x4b400000
	v_perm_b32 v49, v50, v49, s33
	v_perm_b32 v51, v52, v51, s34
	v_or_b32_e32 v98, v49, v51
	v_fmaak_f32 v41, v30, v48, 0x4b400000
	v_fmaak_f32 v42, v31, v48, 0x4b400000
	v_fmaak_f32 v43, v32, v48, 0x4b400000
	v_fmaak_f32 v44, v33, v48, 0x4b400000
	v_perm_b32 v41, v42, v41, s33
	v_perm_b32 v43, v44, v43, s34
	v_or_b32_e32 v99, v41, v43
	s_waitcnt vmcnt(0)
	ds_read_b128 v[18:21], v38 offset:4096
	ds_read_b128 v[22:25], v38 offset:5120
	ds_read_b128 v[26:29], v38 offset:6144
	ds_read_b128 v[30:33], v38 offset:7168
	s_waitcnt lgkmcnt(0)
	s_mov_b32 m0, s35
	s_nop 0
	global_load_lds_dwordx4 v34, s[16:17] nt
	global_load_lds_dwordx4 v34, s[16:17] offset:1024 nt
	global_load_lds_dwordx4 v34, s[16:17] offset:2048 nt
	global_load_lds_dwordx4 v35, s[16:17] offset:3072 nt
	s_add_u32 s16, s16, 0x7d00
	s_addc_u32 s17, s17, 0
	v_cndmask_b32_e64 v30, 0, v30, s[18:19]
	v_cndmask_b32_e64 v31, 0, v31, s[18:19]
	v_cndmask_b32_e64 v32, 0, v32, s[18:19]
	v_cndmask_b32_e64 v33, 0, v33, s[18:19]
	v_max3_f32 v41, |v18|, |v19|, |v20|
	v_max3_f32 v42, |v21|, |v22|, |v23|
	v_max3_f32 v43, |v24|, |v25|, |v26|
	v_max3_f32 v44, |v27|, |v28|, |v29|
	v_max3_f32 v48, |v30|, |v31|, |v32|
	v_max3_f32 v41, v41, v42, |v33|
	v_max3_f32 v43, v43, v44, v48
	v_max_f32_e32 v41, v41, v43
	v_pk_add_f32 v[2:3], v[2:3], v[18:19]
	v_pk_add_f32 v[4:5], v[4:5], v[20:21]
	v_max_f32_dpp v41, v41, v41 quad_perm:[1,0,3,2] row_mask:0xf bank_mask:0xf
	v_pk_add_f32 v[6:7], v[6:7], v[22:23]
	v_pk_add_f32 v[8:9], v[8:9], v[24:25]
	v_max_f32_dpp v41, v41, v41 quad_perm:[2,3,0,1] row_mask:0xf bank_mask:0xf
	v_pk_add_f32 v[10:11], v[10:11], v[26:27]
	v_pk_add_f32 v[12:13], v[12:13], v[28:29]
	v_max_f32_dpp v41, v41, v41 row_half_mirror row_mask:0xf bank_mask:0xf
	v_pk_add_f32 v[14:15], v[14:15], v[30:31]
	v_pk_add_f32 v[16:17], v[16:17], v[32:33]
	v_max_f32_dpp v41, v41, v41 row_mirror row_mask:0xf bank_mask:0xf
	s_nop 1
	v_max_f32_dpp v41, v41, v41 row_bcast:15 row_mask:0xa bank_mask:0xf
	s_nop 1
	v_max_f32_dpp v41, v41, v41 row_bcast:31 row_mask:0xc bank_mask:0xf
	s_nop 1
	v_readlane_b32 s28, v41, 63
	s_nop 1
	v_div_scale_f32 v48, s[30:31], s28, s28, v47
	v_rcp_f32_e32 v49, v48
	s_nop 0
	v_fma_f32 v50, -v48, v49, 1.0
	v_fmac_f32_e32 v49, v50, v49
	v_mov_b32_e32 v50, s28
	v_div_scale_f32 v50, vcc, s32, v50, s32
	v_mul_f32_e32 v51, v50, v49
	v_fma_f32 v52, -v48, v51, v50
	v_fmac_f32_e32 v51, v52, v49
	v_fma_f32 v48, -v48, v51, v50
	v_div_fmas_f32 v48, v48, v49, v51
	v_div_fixup_f32 v48, v48, s28, v47
	v_cmp_gt_f32_e64 vcc, s28, 0
	v_writelane_b32 v40, s28, 11
	s_nop 0
	v_cndmask_b32_e32 v48, 0, v48, vcc
	v_fmaak_f32 v49, v18, v48, 0x4b400000
	v_fmaak_f32 v50, v19, v48, 0x4b400000
	v_fmaak_f32 v51, v20, v48, 0x4b400000
	v_fmaak_f32 v52, v21, v48, 0x4b400000
	v_perm_b32 v49, v50, v49, s33
	v_perm_b32 v51, v52, v51, s34
	v_or_b32_e32 v100, v49, v51
	v_fmaak_f32 v41, v22, v48, 0x4b400000
	v_fmaak_f32 v42, v23, v48, 0x4b400000
	v_fmaak_f32 v43, v24, v48, 0x4b400000
	v_fmaak_f32 v44, v25, v48, 0x4b400000
	v_perm_b32 v41, v42, v41, s33
	v_perm_b32 v43, v44, v43, s34
	v_or_b32_e32 v101, v41, v43
	v_fmaak_f32 v49, v26, v48, 0x4b400000
	v_fmaak_f32 v50, v27, v48, 0x4b400000
	v_fmaak_f32 v51, v28, v48, 0x4b400000
	v_fmaak_f32 v52, v29, v48, 0x4b400000
	v_perm_b32 v49, v50, v49, s33
	v_perm_b32 v51, v52, v51, s34
	v_or_b32_e32 v102, v49, v51
	v_fmaak_f32 v41, v30, v48, 0x4b400000
	v_fmaak_f32 v42, v31, v48, 0x4b400000
	v_fmaak_f32 v43, v32, v48, 0x4b400000
	v_fmaak_f32 v44, v33, v48, 0x4b400000
	v_perm_b32 v41, v42, v41, s33
	v_perm_b32 v43, v44, v43, s34
	v_or_b32_e32 v103, v41, v43
	s_waitcnt vmcnt(0)
	ds_read_b128 v[18:21], v38 offset:0
	ds_read_b128 v[22:25], v38 offset:1024
	ds_read_b128 v[26:29], v38 offset:2048
	ds_read_b128 v[30:33], v38 offset:3072
	s_waitcnt lgkmcnt(0)
	s_mov_b32 m0, s36
	s_nop 0
	global_load_lds_dwordx4 v34, s[16:17] nt
	global_load_lds_dwordx4 v34, s[16:17] offset:1024 nt
	global_load_lds_dwordx4 v34, s[16:17] offset:2048 nt
	global_load_lds_dwordx4 v35, s[16:17] offset:3072 nt
	s_add_u32 s16, s16, 0x7d00
	s_addc_u32 s17, s17, 0
	v_cndmask_b32_e64 v30, 0, v30, s[18:19]
	v_cndmask_b32_e64 v31, 0, v31, s[18:19]
	v_cndmask_b32_e64 v32, 0, v32, s[18:19]
	v_cndmask_b32_e64 v33, 0, v33, s[18:19]
	v_max3_f32 v41, |v18|, |v19|, |v20|
	v_max3_f32 v42, |v21|, |v22|, |v23|
	v_max3_f32 v43, |v24|, |v25|, |v26|
	v_max3_f32 v44, |v27|, |v28|, |v29|
	v_max3_f32 v48, |v30|, |v31|, |v32|
	v_max3_f32 v41, v41, v42, |v33|
	v_max3_f32 v43, v43, v44, v48
	v_max_f32_e32 v41, v41, v43
	v_pk_add_f32 v[2:3], v[2:3], v[18:19]
	v_pk_add_f32 v[4:5], v[4:5], v[20:21]
	v_max_f32_dpp v41, v41, v41 quad_perm:[1,0,3,2] row_mask:0xf bank_mask:0xf
	v_pk_add_f32 v[6:7], v[6:7], v[22:23]
	v_pk_add_f32 v[8:9], v[8:9], v[24:25]
	v_max_f32_dpp v41, v41, v41 quad_perm:[2,3,0,1] row_mask:0xf bank_mask:0xf
	v_pk_add_f32 v[10:11], v[10:11], v[26:27]
	v_pk_add_f32 v[12:13], v[12:13], v[28:29]
	v_max_f32_dpp v41, v41, v41 row_half_mirror row_mask:0xf bank_mask:0xf
	v_pk_add_f32 v[14:15], v[14:15], v[30:31]
	v_pk_add_f32 v[16:17], v[16:17], v[32:33]
	v_max_f32_dpp v41, v41, v41 row_mirror row_mask:0xf bank_mask:0xf
	s_nop 1
	v_max_f32_dpp v41, v41, v41 row_bcast:15 row_mask:0xa bank_mask:0xf
	s_nop 1
	v_max_f32_dpp v41, v41, v41 row_bcast:31 row_mask:0xc bank_mask:0xf
	s_nop 1
	v_readlane_b32 s28, v41, 63
	s_nop 1
	v_div_scale_f32 v48, s[30:31], s28, s28, v47
	v_rcp_f32_e32 v49, v48
	s_nop 0
	v_fma_f32 v50, -v48, v49, 1.0
	v_fmac_f32_e32 v49, v50, v49
	v_mov_b32_e32 v50, s28
	v_div_scale_f32 v50, vcc, s32, v50, s32
	v_mul_f32_e32 v51, v50, v49
	v_fma_f32 v52, -v48, v51, v50
	v_fmac_f32_e32 v51, v52, v49
	v_fma_f32 v48, -v48, v51, v50
	v_div_fmas_f32 v48, v48, v49, v51
	v_div_fixup_f32 v48, v48, s28, v47
	v_cmp_gt_f32_e64 vcc, s28, 0
	v_writelane_b32 v40, s28, 12
	s_nop 0
	v_cndmask_b32_e32 v48, 0, v48, vcc
	v_fmaak_f32 v49, v18, v48, 0x4b400000
	v_fmaak_f32 v50, v19, v48, 0x4b400000
	v_fmaak_f32 v51, v20, v48, 0x4b400000
	v_fmaak_f32 v52, v21, v48, 0x4b400000
	v_perm_b32 v49, v50, v49, s33
	v_perm_b32 v51, v52, v51, s34
	v_or_b32_e32 v104, v49, v51
	v_fmaak_f32 v41, v22, v48, 0x4b400000
	v_fmaak_f32 v42, v23, v48, 0x4b400000
	v_fmaak_f32 v43, v24, v48, 0x4b400000
	v_fmaak_f32 v44, v25, v48, 0x4b400000
	v_perm_b32 v41, v42, v41, s33
	v_perm_b32 v43, v44, v43, s34
	v_or_b32_e32 v105, v41, v43
	v_fmaak_f32 v49, v26, v48, 0x4b400000
	v_fmaak_f32 v50, v27, v48, 0x4b400000
	v_fmaak_f32 v51, v28, v48, 0x4b400000
	v_fmaak_f32 v52, v29, v48, 0x4b400000
	v_perm_b32 v49, v50, v49, s33
	v_perm_b32 v51, v52, v51, s34
	v_or_b32_e32 v106, v49, v51
	v_fmaak_f32 v41, v30, v48, 0x4b400000
	v_fmaak_f32 v42, v31, v48, 0x4b400000
	v_fmaak_f32 v43, v32, v48, 0x4b400000
	v_fmaak_f32 v44, v33, v48, 0x4b400000
	v_perm_b32 v41, v42, v41, s33
	v_perm_b32 v43, v44, v43, s34
	v_or_b32_e32 v107, v41, v43
	s_waitcnt vmcnt(0)
	ds_read_b128 v[18:21], v38 offset:4096
	ds_read_b128 v[22:25], v38 offset:5120
	ds_read_b128 v[26:29], v38 offset:6144
	ds_read_b128 v[30:33], v38 offset:7168
	s_waitcnt lgkmcnt(0)
	s_mov_b32 m0, s35
	s_nop 0
	global_load_lds_dwordx4 v34, s[16:17] nt
	global_load_lds_dwordx4 v34, s[16:17] offset:1024 nt
	global_load_lds_dwordx4 v34, s[16:17] offset:2048 nt
	global_load_lds_dwordx4 v35, s[16:17] offset:3072 nt
	s_add_u32 s16, s16, 0x7d00
	s_addc_u32 s17, s17, 0
	v_cndmask_b32_e64 v30, 0, v30, s[18:19]
	v_cndmask_b32_e64 v31, 0, v31, s[18:19]
	v_cndmask_b32_e64 v32, 0, v32, s[18:19]
	v_cndmask_b32_e64 v33, 0, v33, s[18:19]
	v_max3_f32 v41, |v18|, |v19|, |v20|
	v_max3_f32 v42, |v21|, |v22|, |v23|
	v_max3_f32 v43, |v24|, |v25|, |v26|
	v_max3_f32 v44, |v27|, |v28|, |v29|
	v_max3_f32 v48, |v30|, |v31|, |v32|
	v_max3_f32 v41, v41, v42, |v33|
	v_max3_f32 v43, v43, v44, v48
	v_max_f32_e32 v41, v41, v43
	v_pk_add_f32 v[2:3], v[2:3], v[18:19]
	v_pk_add_f32 v[4:5], v[4:5], v[20:21]
	v_max_f32_dpp v41, v41, v41 quad_perm:[1,0,3,2] row_mask:0xf bank_mask:0xf
	v_pk_add_f32 v[6:7], v[6:7], v[22:23]
	v_pk_add_f32 v[8:9], v[8:9], v[24:25]
	v_max_f32_dpp v41, v41, v41 quad_perm:[2,3,0,1] row_mask:0xf bank_mask:0xf
	v_pk_add_f32 v[10:11], v[10:11], v[26:27]
	v_pk_add_f32 v[12:13], v[12:13], v[28:29]
	v_max_f32_dpp v41, v41, v41 row_half_mirror row_mask:0xf bank_mask:0xf
	v_pk_add_f32 v[14:15], v[14:15], v[30:31]
	v_pk_add_f32 v[16:17], v[16:17], v[32:33]
	v_max_f32_dpp v41, v41, v41 row_mirror row_mask:0xf bank_mask:0xf
	s_nop 1
	v_max_f32_dpp v41, v41, v41 row_bcast:15 row_mask:0xa bank_mask:0xf
	s_nop 1
	v_max_f32_dpp v41, v41, v41 row_bcast:31 row_mask:0xc bank_mask:0xf
	s_nop 1
	v_readlane_b32 s28, v41, 63
	s_nop 1
	v_div_scale_f32 v48, s[30:31], s28, s28, v47
	v_rcp_f32_e32 v49, v48
	s_nop 0
	v_fma_f32 v50, -v48, v49, 1.0
	v_fmac_f32_e32 v49, v50, v49
	v_mov_b32_e32 v50, s28
	v_div_scale_f32 v50, vcc, s32, v50, s32
	v_mul_f32_e32 v51, v50, v49
	v_fma_f32 v52, -v48, v51, v50
	v_fmac_f32_e32 v51, v52, v49
	v_fma_f32 v48, -v48, v51, v50
	v_div_fmas_f32 v48, v48, v49, v51
	v_div_fixup_f32 v48, v48, s28, v47
	v_cmp_gt_f32_e64 vcc, s28, 0
	v_writelane_b32 v40, s28, 13
	s_nop 0
	v_cndmask_b32_e32 v48, 0, v48, vcc
	v_fmaak_f32 v49, v18, v48, 0x4b400000
	v_fmaak_f32 v50, v19, v48, 0x4b400000
	v_fmaak_f32 v51, v20, v48, 0x4b400000
	v_fmaak_f32 v52, v21, v48, 0x4b400000
	v_perm_b32 v49, v50, v49, s33
	v_perm_b32 v51, v52, v51, s34
	v_or_b32_e32 v108, v49, v51
	v_fmaak_f32 v41, v22, v48, 0x4b400000
	v_fmaak_f32 v42, v23, v48, 0x4b400000
	v_fmaak_f32 v43, v24, v48, 0x4b400000
	v_fmaak_f32 v44, v25, v48, 0x4b400000
	v_perm_b32 v41, v42, v41, s33
	v_perm_b32 v43, v44, v43, s34
	v_or_b32_e32 v109, v41, v43
	v_fmaak_f32 v49, v26, v48, 0x4b400000
	v_fmaak_f32 v50, v27, v48, 0x4b400000
	v_fmaak_f32 v51, v28, v48, 0x4b400000
	v_fmaak_f32 v52, v29, v48, 0x4b400000
	v_perm_b32 v49, v50, v49, s33
	v_perm_b32 v51, v52, v51, s34
	v_or_b32_e32 v110, v49, v51
	v_fmaak_f32 v41, v30, v48, 0x4b400000
	v_fmaak_f32 v42, v31, v48, 0x4b400000
	v_fmaak_f32 v43, v32, v48, 0x4b400000
	v_fmaak_f32 v44, v33, v48, 0x4b400000
	v_perm_b32 v41, v42, v41, s33
	v_perm_b32 v43, v44, v43, s34
	v_or_b32_e32 v111, v41, v43
	s_waitcnt vmcnt(0)
	ds_read_b128 v[18:21], v38 offset:0
	ds_read_b128 v[22:25], v38 offset:1024
	ds_read_b128 v[26:29], v38 offset:2048
	ds_read_b128 v[30:33], v38 offset:3072
	s_waitcnt lgkmcnt(0)
	s_mov_b32 m0, s36
	s_nop 0
	global_load_lds_dwordx4 v34, s[16:17] nt
	global_load_lds_dwordx4 v34, s[16:17] offset:1024 nt
	global_load_lds_dwordx4 v34, s[16:17] offset:2048 nt
	global_load_lds_dwordx4 v35, s[16:17] offset:3072 nt
	s_add_u32 s16, s16, 0x7d00
	s_addc_u32 s17, s17, 0
	v_cndmask_b32_e64 v30, 0, v30, s[18:19]
	v_cndmask_b32_e64 v31, 0, v31, s[18:19]
	v_cndmask_b32_e64 v32, 0, v32, s[18:19]
	v_cndmask_b32_e64 v33, 0, v33, s[18:19]
	v_max3_f32 v41, |v18|, |v19|, |v20|
	v_max3_f32 v42, |v21|, |v22|, |v23|
	v_max3_f32 v43, |v24|, |v25|, |v26|
	v_max3_f32 v44, |v27|, |v28|, |v29|
	v_max3_f32 v48, |v30|, |v31|, |v32|
	v_max3_f32 v41, v41, v42, |v33|
	v_max3_f32 v43, v43, v44, v48
	v_max_f32_e32 v41, v41, v43
	v_pk_add_f32 v[2:3], v[2:3], v[18:19]
	v_pk_add_f32 v[4:5], v[4:5], v[20:21]
	v_max_f32_dpp v41, v41, v41 quad_perm:[1,0,3,2] row_mask:0xf bank_mask:0xf
	v_pk_add_f32 v[6:7], v[6:7], v[22:23]
	v_pk_add_f32 v[8:9], v[8:9], v[24:25]
	v_max_f32_dpp v41, v41, v41 quad_perm:[2,3,0,1] row_mask:0xf bank_mask:0xf
	v_pk_add_f32 v[10:11], v[10:11], v[26:27]
	v_pk_add_f32 v[12:13], v[12:13], v[28:29]
	v_max_f32_dpp v41, v41, v41 row_half_mirror row_mask:0xf bank_mask:0xf
	v_pk_add_f32 v[14:15], v[14:15], v[30:31]
	v_pk_add_f32 v[16:17], v[16:17], v[32:33]
	v_max_f32_dpp v41, v41, v41 row_mirror row_mask:0xf bank_mask:0xf
	s_nop 1
	v_max_f32_dpp v41, v41, v41 row_bcast:15 row_mask:0xa bank_mask:0xf
	s_nop 1
	v_max_f32_dpp v41, v41, v41 row_bcast:31 row_mask:0xc bank_mask:0xf
	s_nop 1
	v_readlane_b32 s28, v41, 63
	s_nop 1
	v_div_scale_f32 v48, s[30:31], s28, s28, v47
	v_rcp_f32_e32 v49, v48
	s_nop 0
	v_fma_f32 v50, -v48, v49, 1.0
	v_fmac_f32_e32 v49, v50, v49
	v_mov_b32_e32 v50, s28
	v_div_scale_f32 v50, vcc, s32, v50, s32
	v_mul_f32_e32 v51, v50, v49
	v_fma_f32 v52, -v48, v51, v50
	v_fmac_f32_e32 v51, v52, v49
	v_fma_f32 v48, -v48, v51, v50
	v_div_fmas_f32 v48, v48, v49, v51
	v_div_fixup_f32 v48, v48, s28, v47
	v_cmp_gt_f32_e64 vcc, s28, 0
	v_writelane_b32 v40, s28, 14
	s_nop 0
	v_cndmask_b32_e32 v48, 0, v48, vcc
	v_fmaak_f32 v49, v18, v48, 0x4b400000
	v_fmaak_f32 v50, v19, v48, 0x4b400000
	v_fmaak_f32 v51, v20, v48, 0x4b400000
	v_fmaak_f32 v52, v21, v48, 0x4b400000
	v_perm_b32 v49, v50, v49, s33
	v_perm_b32 v51, v52, v51, s34
	v_or_b32_e32 v112, v49, v51
	v_fmaak_f32 v41, v22, v48, 0x4b400000
	v_fmaak_f32 v42, v23, v48, 0x4b400000
	v_fmaak_f32 v43, v24, v48, 0x4b400000
	v_fmaak_f32 v44, v25, v48, 0x4b400000
	v_perm_b32 v41, v42, v41, s33
	v_perm_b32 v43, v44, v43, s34
	v_or_b32_e32 v113, v41, v43
	v_fmaak_f32 v49, v26, v48, 0x4b400000
	v_fmaak_f32 v50, v27, v48, 0x4b400000
	v_fmaak_f32 v51, v28, v48, 0x4b400000
	v_fmaak_f32 v52, v29, v48, 0x4b400000
	v_perm_b32 v49, v50, v49, s33
	v_perm_b32 v51, v52, v51, s34
	v_or_b32_e32 v114, v49, v51
	v_fmaak_f32 v41, v30, v48, 0x4b400000
	v_fmaak_f32 v42, v31, v48, 0x4b400000
	v_fmaak_f32 v43, v32, v48, 0x4b400000
	v_fmaak_f32 v44, v33, v48, 0x4b400000
	v_perm_b32 v41, v42, v41, s33
	v_perm_b32 v43, v44, v43, s34
	v_or_b32_e32 v115, v41, v43
	s_waitcnt vmcnt(0)
	ds_read_b128 v[18:21], v38 offset:4096
	ds_read_b128 v[22:25], v38 offset:5120
	ds_read_b128 v[26:29], v38 offset:6144
	ds_read_b128 v[30:33], v38 offset:7168
	s_waitcnt lgkmcnt(0)
	s_mov_b32 m0, s35
	s_nop 0
	global_load_lds_dwordx4 v34, s[16:17] nt
	global_load_lds_dwordx4 v34, s[16:17] offset:1024 nt
	global_load_lds_dwordx4 v34, s[16:17] offset:2048 nt
	global_load_lds_dwordx4 v35, s[16:17] offset:3072 nt
	s_add_u32 s16, s16, 0x7d00
	s_addc_u32 s17, s17, 0
	v_cndmask_b32_e64 v30, 0, v30, s[18:19]
	v_cndmask_b32_e64 v31, 0, v31, s[18:19]
	v_cndmask_b32_e64 v32, 0, v32, s[18:19]
	v_cndmask_b32_e64 v33, 0, v33, s[18:19]
	v_max3_f32 v41, |v18|, |v19|, |v20|
	v_max3_f32 v42, |v21|, |v22|, |v23|
	v_max3_f32 v43, |v24|, |v25|, |v26|
	v_max3_f32 v44, |v27|, |v28|, |v29|
	v_max3_f32 v48, |v30|, |v31|, |v32|
	v_max3_f32 v41, v41, v42, |v33|
	v_max3_f32 v43, v43, v44, v48
	v_max_f32_e32 v41, v41, v43
	v_pk_add_f32 v[2:3], v[2:3], v[18:19]
	v_pk_add_f32 v[4:5], v[4:5], v[20:21]
	v_max_f32_dpp v41, v41, v41 quad_perm:[1,0,3,2] row_mask:0xf bank_mask:0xf
	v_pk_add_f32 v[6:7], v[6:7], v[22:23]
	v_pk_add_f32 v[8:9], v[8:9], v[24:25]
	v_max_f32_dpp v41, v41, v41 quad_perm:[2,3,0,1] row_mask:0xf bank_mask:0xf
	v_pk_add_f32 v[10:11], v[10:11], v[26:27]
	v_pk_add_f32 v[12:13], v[12:13], v[28:29]
	v_max_f32_dpp v41, v41, v41 row_half_mirror row_mask:0xf bank_mask:0xf
	v_pk_add_f32 v[14:15], v[14:15], v[30:31]
	v_pk_add_f32 v[16:17], v[16:17], v[32:33]
	v_max_f32_dpp v41, v41, v41 row_mirror row_mask:0xf bank_mask:0xf
	s_nop 1
	v_max_f32_dpp v41, v41, v41 row_bcast:15 row_mask:0xa bank_mask:0xf
	s_nop 1
	v_max_f32_dpp v41, v41, v41 row_bcast:31 row_mask:0xc bank_mask:0xf
	s_nop 1
	v_readlane_b32 s28, v41, 63
	s_nop 1
	v_div_scale_f32 v48, s[30:31], s28, s28, v47
	v_rcp_f32_e32 v49, v48
	s_nop 0
	v_fma_f32 v50, -v48, v49, 1.0
	v_fmac_f32_e32 v49, v50, v49
	v_mov_b32_e32 v50, s28
	v_div_scale_f32 v50, vcc, s32, v50, s32
	v_mul_f32_e32 v51, v50, v49
	v_fma_f32 v52, -v48, v51, v50
	v_fmac_f32_e32 v51, v52, v49
	v_fma_f32 v48, -v48, v51, v50
	v_div_fmas_f32 v48, v48, v49, v51
	v_div_fixup_f32 v48, v48, s28, v47
	v_cmp_gt_f32_e64 vcc, s28, 0
	v_writelane_b32 v40, s28, 15
	s_nop 0
	v_cndmask_b32_e32 v48, 0, v48, vcc
	v_fmaak_f32 v49, v18, v48, 0x4b400000
	v_fmaak_f32 v50, v19, v48, 0x4b400000
	v_fmaak_f32 v51, v20, v48, 0x4b400000
	v_fmaak_f32 v52, v21, v48, 0x4b400000
	v_perm_b32 v49, v50, v49, s33
	v_perm_b32 v51, v52, v51, s34
	v_or_b32_e32 v116, v49, v51
	v_fmaak_f32 v41, v22, v48, 0x4b400000
	v_fmaak_f32 v42, v23, v48, 0x4b400000
	v_fmaak_f32 v43, v24, v48, 0x4b400000
	v_fmaak_f32 v44, v25, v48, 0x4b400000
	v_perm_b32 v41, v42, v41, s33
	v_perm_b32 v43, v44, v43, s34
	v_or_b32_e32 v117, v41, v43
	v_fmaak_f32 v49, v26, v48, 0x4b400000
	v_fmaak_f32 v50, v27, v48, 0x4b400000
	v_fmaak_f32 v51, v28, v48, 0x4b400000
	v_fmaak_f32 v52, v29, v48, 0x4b400000
	v_perm_b32 v49, v50, v49, s33
	v_perm_b32 v51, v52, v51, s34
	v_or_b32_e32 v118, v49, v51
	v_fmaak_f32 v41, v30, v48, 0x4b400000
	v_fmaak_f32 v42, v31, v48, 0x4b400000
	v_fmaak_f32 v43, v32, v48, 0x4b400000
	v_fmaak_f32 v44, v33, v48, 0x4b400000
	v_perm_b32 v41, v42, v41, s33
	v_perm_b32 v43, v44, v43, s34
	v_or_b32_e32 v119, v41, v43
	s_waitcnt vmcnt(0)
	ds_read_b128 v[18:21], v38 offset:0
	ds_read_b128 v[22:25], v38 offset:1024
	ds_read_b128 v[26:29], v38 offset:2048
	ds_read_b128 v[30:33], v38 offset:3072
	s_waitcnt lgkmcnt(0)
	s_mov_b32 m0, s36
	s_nop 0
	global_load_lds_dwordx4 v34, s[16:17] nt
	global_load_lds_dwordx4 v34, s[16:17] offset:1024 nt
	global_load_lds_dwordx4 v34, s[16:17] offset:2048 nt
	global_load_lds_dwordx4 v35, s[16:17] offset:3072 nt
	s_add_u32 s16, s16, 0x7d00
	s_addc_u32 s17, s17, 0
	v_cndmask_b32_e64 v30, 0, v30, s[18:19]
	v_cndmask_b32_e64 v31, 0, v31, s[18:19]
	v_cndmask_b32_e64 v32, 0, v32, s[18:19]
	v_cndmask_b32_e64 v33, 0, v33, s[18:19]
	v_max3_f32 v41, |v18|, |v19|, |v20|
	v_max3_f32 v42, |v21|, |v22|, |v23|
	v_max3_f32 v43, |v24|, |v25|, |v26|
	v_max3_f32 v44, |v27|, |v28|, |v29|
	v_max3_f32 v48, |v30|, |v31|, |v32|
	v_max3_f32 v41, v41, v42, |v33|
	v_max3_f32 v43, v43, v44, v48
	v_max_f32_e32 v41, v41, v43
	v_pk_add_f32 v[2:3], v[2:3], v[18:19]
	v_pk_add_f32 v[4:5], v[4:5], v[20:21]
	v_max_f32_dpp v41, v41, v41 quad_perm:[1,0,3,2] row_mask:0xf bank_mask:0xf
	v_pk_add_f32 v[6:7], v[6:7], v[22:23]
	v_pk_add_f32 v[8:9], v[8:9], v[24:25]
	v_max_f32_dpp v41, v41, v41 quad_perm:[2,3,0,1] row_mask:0xf bank_mask:0xf
	v_pk_add_f32 v[10:11], v[10:11], v[26:27]
	v_pk_add_f32 v[12:13], v[12:13], v[28:29]
	v_max_f32_dpp v41, v41, v41 row_half_mirror row_mask:0xf bank_mask:0xf
	v_pk_add_f32 v[14:15], v[14:15], v[30:31]
	v_pk_add_f32 v[16:17], v[16:17], v[32:33]
	v_max_f32_dpp v41, v41, v41 row_mirror row_mask:0xf bank_mask:0xf
	s_nop 1
	v_max_f32_dpp v41, v41, v41 row_bcast:15 row_mask:0xa bank_mask:0xf
	s_nop 1
	v_max_f32_dpp v41, v41, v41 row_bcast:31 row_mask:0xc bank_mask:0xf
	s_nop 1
	v_readlane_b32 s28, v41, 63
	s_nop 1
	v_div_scale_f32 v48, s[30:31], s28, s28, v47
	v_rcp_f32_e32 v49, v48
	s_nop 0
	v_fma_f32 v50, -v48, v49, 1.0
	v_fmac_f32_e32 v49, v50, v49
	v_mov_b32_e32 v50, s28
	v_div_scale_f32 v50, vcc, s32, v50, s32
	v_mul_f32_e32 v51, v50, v49
	v_fma_f32 v52, -v48, v51, v50
	v_fmac_f32_e32 v51, v52, v49
	v_fma_f32 v48, -v48, v51, v50
	v_div_fmas_f32 v48, v48, v49, v51
	v_div_fixup_f32 v48, v48, s28, v47
	v_cmp_gt_f32_e64 vcc, s28, 0
	v_writelane_b32 v40, s28, 16
	s_nop 0
	v_cndmask_b32_e32 v48, 0, v48, vcc
	v_fmaak_f32 v49, v18, v48, 0x4b400000
	v_fmaak_f32 v50, v19, v48, 0x4b400000
	v_fmaak_f32 v51, v20, v48, 0x4b400000
	v_fmaak_f32 v52, v21, v48, 0x4b400000
	v_perm_b32 v49, v50, v49, s33
	v_perm_b32 v51, v52, v51, s34
	v_or_b32_e32 v120, v49, v51
	v_fmaak_f32 v41, v22, v48, 0x4b400000
	v_fmaak_f32 v42, v23, v48, 0x4b400000
	v_fmaak_f32 v43, v24, v48, 0x4b400000
	v_fmaak_f32 v44, v25, v48, 0x4b400000
	v_perm_b32 v41, v42, v41, s33
	v_perm_b32 v43, v44, v43, s34
	v_or_b32_e32 v121, v41, v43
	v_fmaak_f32 v49, v26, v48, 0x4b400000
	v_fmaak_f32 v50, v27, v48, 0x4b400000
	v_fmaak_f32 v51, v28, v48, 0x4b400000
	v_fmaak_f32 v52, v29, v48, 0x4b400000
	v_perm_b32 v49, v50, v49, s33
	v_perm_b32 v51, v52, v51, s34
	v_or_b32_e32 v122, v49, v51
	v_fmaak_f32 v41, v30, v48, 0x4b400000
	v_fmaak_f32 v42, v31, v48, 0x4b400000
	v_fmaak_f32 v43, v32, v48, 0x4b400000
	v_fmaak_f32 v44, v33, v48, 0x4b400000
	v_perm_b32 v41, v42, v41, s33
	v_perm_b32 v43, v44, v43, s34
	v_or_b32_e32 v123, v41, v43
	s_waitcnt vmcnt(0)
	ds_read_b128 v[18:21], v38 offset:4096
	ds_read_b128 v[22:25], v38 offset:5120
	ds_read_b128 v[26:29], v38 offset:6144
	ds_read_b128 v[30:33], v38 offset:7168
	s_waitcnt lgkmcnt(0)
	s_mov_b32 m0, s35
	s_nop 0
	global_load_lds_dwordx4 v34, s[16:17] nt
	global_load_lds_dwordx4 v34, s[16:17] offset:1024 nt
	global_load_lds_dwordx4 v34, s[16:17] offset:2048 nt
	global_load_lds_dwordx4 v35, s[16:17] offset:3072 nt
	s_add_u32 s16, s16, 0x7d00
	s_addc_u32 s17, s17, 0
	v_cndmask_b32_e64 v30, 0, v30, s[18:19]
	v_cndmask_b32_e64 v31, 0, v31, s[18:19]
	v_cndmask_b32_e64 v32, 0, v32, s[18:19]
	v_cndmask_b32_e64 v33, 0, v33, s[18:19]
	v_max3_f32 v41, |v18|, |v19|, |v20|
	v_max3_f32 v42, |v21|, |v22|, |v23|
	v_max3_f32 v43, |v24|, |v25|, |v26|
	v_max3_f32 v44, |v27|, |v28|, |v29|
	v_max3_f32 v48, |v30|, |v31|, |v32|
	v_max3_f32 v41, v41, v42, |v33|
	v_max3_f32 v43, v43, v44, v48
	v_max_f32_e32 v41, v41, v43
	v_pk_add_f32 v[2:3], v[2:3], v[18:19]
	v_pk_add_f32 v[4:5], v[4:5], v[20:21]
	v_max_f32_dpp v41, v41, v41 quad_perm:[1,0,3,2] row_mask:0xf bank_mask:0xf
	v_pk_add_f32 v[6:7], v[6:7], v[22:23]
	v_pk_add_f32 v[8:9], v[8:9], v[24:25]
	v_max_f32_dpp v41, v41, v41 quad_perm:[2,3,0,1] row_mask:0xf bank_mask:0xf
	v_pk_add_f32 v[10:11], v[10:11], v[26:27]
	v_pk_add_f32 v[12:13], v[12:13], v[28:29]
	v_max_f32_dpp v41, v41, v41 row_half_mirror row_mask:0xf bank_mask:0xf
	v_pk_add_f32 v[14:15], v[14:15], v[30:31]
	v_pk_add_f32 v[16:17], v[16:17], v[32:33]
	v_max_f32_dpp v41, v41, v41 row_mirror row_mask:0xf bank_mask:0xf
	s_nop 1
	v_max_f32_dpp v41, v41, v41 row_bcast:15 row_mask:0xa bank_mask:0xf
	s_nop 1
	v_max_f32_dpp v41, v41, v41 row_bcast:31 row_mask:0xc bank_mask:0xf
	s_nop 1
	v_readlane_b32 s28, v41, 63
	s_nop 1
	v_div_scale_f32 v48, s[30:31], s28, s28, v47
	v_rcp_f32_e32 v49, v48
	s_nop 0
	v_fma_f32 v50, -v48, v49, 1.0
	v_fmac_f32_e32 v49, v50, v49
	v_mov_b32_e32 v50, s28
	v_div_scale_f32 v50, vcc, s32, v50, s32
	v_mul_f32_e32 v51, v50, v49
	v_fma_f32 v52, -v48, v51, v50
	v_fmac_f32_e32 v51, v52, v49
	v_fma_f32 v48, -v48, v51, v50
	v_div_fmas_f32 v48, v48, v49, v51
	v_div_fixup_f32 v48, v48, s28, v47
	v_cmp_gt_f32_e64 vcc, s28, 0
	v_writelane_b32 v40, s28, 17
	s_nop 0
	v_cndmask_b32_e32 v48, 0, v48, vcc
	v_fmaak_f32 v49, v18, v48, 0x4b400000
	v_fmaak_f32 v50, v19, v48, 0x4b400000
	v_fmaak_f32 v51, v20, v48, 0x4b400000
	v_fmaak_f32 v52, v21, v48, 0x4b400000
	v_perm_b32 v49, v50, v49, s33
	v_perm_b32 v51, v52, v51, s34
	v_or_b32_e32 v124, v49, v51
	v_fmaak_f32 v41, v22, v48, 0x4b400000
	v_fmaak_f32 v42, v23, v48, 0x4b400000
	v_fmaak_f32 v43, v24, v48, 0x4b400000
	v_fmaak_f32 v44, v25, v48, 0x4b400000
	v_perm_b32 v41, v42, v41, s33
	v_perm_b32 v43, v44, v43, s34
	v_or_b32_e32 v125, v41, v43
	v_fmaak_f32 v49, v26, v48, 0x4b400000
	v_fmaak_f32 v50, v27, v48, 0x4b400000
	v_fmaak_f32 v51, v28, v48, 0x4b400000
	v_fmaak_f32 v52, v29, v48, 0x4b400000
	v_perm_b32 v49, v50, v49, s33
	v_perm_b32 v51, v52, v51, s34
	v_or_b32_e32 v126, v49, v51
	v_fmaak_f32 v41, v30, v48, 0x4b400000
	v_fmaak_f32 v42, v31, v48, 0x4b400000
	v_fmaak_f32 v43, v32, v48, 0x4b400000
	v_fmaak_f32 v44, v33, v48, 0x4b400000
	v_perm_b32 v41, v42, v41, s33
	v_perm_b32 v43, v44, v43, s34
	v_or_b32_e32 v127, v41, v43
	s_waitcnt vmcnt(0)
	ds_read_b128 v[18:21], v38 offset:0
	ds_read_b128 v[22:25], v38 offset:1024
	ds_read_b128 v[26:29], v38 offset:2048
	ds_read_b128 v[30:33], v38 offset:3072
	s_waitcnt lgkmcnt(0)
	s_mov_b32 m0, s36
	s_nop 0
	global_load_lds_dwordx4 v34, s[16:17] nt
	global_load_lds_dwordx4 v34, s[16:17] offset:1024 nt
	global_load_lds_dwordx4 v34, s[16:17] offset:2048 nt
	global_load_lds_dwordx4 v35, s[16:17] offset:3072 nt
	s_add_u32 s16, s16, 0x7d00
	s_addc_u32 s17, s17, 0
	v_cndmask_b32_e64 v30, 0, v30, s[18:19]
	v_cndmask_b32_e64 v31, 0, v31, s[18:19]
	v_cndmask_b32_e64 v32, 0, v32, s[18:19]
	v_cndmask_b32_e64 v33, 0, v33, s[18:19]
	v_max3_f32 v41, |v18|, |v19|, |v20|
	v_max3_f32 v42, |v21|, |v22|, |v23|
	v_max3_f32 v43, |v24|, |v25|, |v26|
	v_max3_f32 v44, |v27|, |v28|, |v29|
	v_max3_f32 v48, |v30|, |v31|, |v32|
	v_max3_f32 v41, v41, v42, |v33|
	v_max3_f32 v43, v43, v44, v48
	v_max_f32_e32 v41, v41, v43
	v_pk_add_f32 v[2:3], v[2:3], v[18:19]
	v_pk_add_f32 v[4:5], v[4:5], v[20:21]
	v_max_f32_dpp v41, v41, v41 quad_perm:[1,0,3,2] row_mask:0xf bank_mask:0xf
	v_pk_add_f32 v[6:7], v[6:7], v[22:23]
	v_pk_add_f32 v[8:9], v[8:9], v[24:25]
	v_max_f32_dpp v41, v41, v41 quad_perm:[2,3,0,1] row_mask:0xf bank_mask:0xf
	v_pk_add_f32 v[10:11], v[10:11], v[26:27]
	v_pk_add_f32 v[12:13], v[12:13], v[28:29]
	v_max_f32_dpp v41, v41, v41 row_half_mirror row_mask:0xf bank_mask:0xf
	v_pk_add_f32 v[14:15], v[14:15], v[30:31]
	v_pk_add_f32 v[16:17], v[16:17], v[32:33]
	v_max_f32_dpp v41, v41, v41 row_mirror row_mask:0xf bank_mask:0xf
	s_nop 1
	v_max_f32_dpp v41, v41, v41 row_bcast:15 row_mask:0xa bank_mask:0xf
	s_nop 1
	v_max_f32_dpp v41, v41, v41 row_bcast:31 row_mask:0xc bank_mask:0xf
	s_nop 1
	v_readlane_b32 s28, v41, 63
	s_nop 1
	v_div_scale_f32 v48, s[30:31], s28, s28, v47
	v_rcp_f32_e32 v49, v48
	s_nop 0
	v_fma_f32 v50, -v48, v49, 1.0
	v_fmac_f32_e32 v49, v50, v49
	v_mov_b32_e32 v50, s28
	v_div_scale_f32 v50, vcc, s32, v50, s32
	v_mul_f32_e32 v51, v50, v49
	v_fma_f32 v52, -v48, v51, v50
	v_fmac_f32_e32 v51, v52, v49
	v_fma_f32 v48, -v48, v51, v50
	v_div_fmas_f32 v48, v48, v49, v51
	v_div_fixup_f32 v48, v48, s28, v47
	v_cmp_gt_f32_e64 vcc, s28, 0
	v_writelane_b32 v40, s28, 18
	s_nop 0
	v_cndmask_b32_e32 v48, 0, v48, vcc
	v_fmaak_f32 v49, v18, v48, 0x4b400000
	v_fmaak_f32 v50, v19, v48, 0x4b400000
	v_fmaak_f32 v51, v20, v48, 0x4b400000
	v_fmaak_f32 v52, v21, v48, 0x4b400000
	v_perm_b32 v49, v50, v49, s33
	v_perm_b32 v51, v52, v51, s34
	v_or_b32_e32 v49, v49, v51
	s_add_u32 s20, s20, 0x4800
	s_addc_u32 s21, s21, 0
	s_add_u32 s22, s22, 0x4800
	s_addc_u32 s23, s23, 0
	s_add_u32 s24, s24, 0x4800
	s_addc_u32 s25, s25, 0
	s_add_u32 s26, s26, 0x4800
	s_addc_u32 s27, s27, 0
	global_store_dword v39, v49, s[20:21]
	v_fmaak_f32 v41, v22, v48, 0x4b400000
	v_fmaak_f32 v42, v23, v48, 0x4b400000
	v_fmaak_f32 v43, v24, v48, 0x4b400000
	v_fmaak_f32 v44, v25, v48, 0x4b400000
	v_perm_b32 v41, v42, v41, s33
	v_perm_b32 v43, v44, v43, s34
	v_or_b32_e32 v41, v41, v43
	global_store_dword v39, v41, s[22:23]
	v_fmaak_f32 v49, v26, v48, 0x4b400000
	v_fmaak_f32 v50, v27, v48, 0x4b400000
	v_fmaak_f32 v51, v28, v48, 0x4b400000
	v_fmaak_f32 v52, v29, v48, 0x4b400000
	v_perm_b32 v49, v50, v49, s33
	v_perm_b32 v51, v52, v51, s34
	v_or_b32_e32 v49, v49, v51
	global_store_dword v39, v49, s[24:25]
	v_fmaak_f32 v41, v30, v48, 0x4b400000
	v_fmaak_f32 v42, v31, v48, 0x4b400000
	v_fmaak_f32 v43, v32, v48, 0x4b400000
	v_fmaak_f32 v44, v33, v48, 0x4b400000
	v_perm_b32 v41, v42, v41, s33
	v_perm_b32 v43, v44, v43, s34
	v_or_b32_e32 v41, v41, v43
	global_store_dword v39, v41, s[26:27]
	s_waitcnt vmcnt(4)
	ds_read_b128 v[18:21], v38 offset:4096
	ds_read_b128 v[22:25], v38 offset:5120
	ds_read_b128 v[26:29], v38 offset:6144
	ds_read_b128 v[30:33], v38 offset:7168
	s_waitcnt lgkmcnt(0)
	s_mov_b32 m0, s35
	s_nop 0
	global_load_lds_dwordx4 v34, s[16:17] nt
	global_load_lds_dwordx4 v34, s[16:17] offset:1024 nt
	global_load_lds_dwordx4 v34, s[16:17] offset:2048 nt
	global_load_lds_dwordx4 v35, s[16:17] offset:3072 nt
	s_add_u32 s16, s16, 0x7d00
	s_addc_u32 s17, s17, 0
	v_cndmask_b32_e64 v30, 0, v30, s[18:19]
	v_cndmask_b32_e64 v31, 0, v31, s[18:19]
	v_cndmask_b32_e64 v32, 0, v32, s[18:19]
	v_cndmask_b32_e64 v33, 0, v33, s[18:19]
	v_max3_f32 v41, |v18|, |v19|, |v20|
	v_max3_f32 v42, |v21|, |v22|, |v23|
	v_max3_f32 v43, |v24|, |v25|, |v26|
	v_max3_f32 v44, |v27|, |v28|, |v29|
	v_max3_f32 v48, |v30|, |v31|, |v32|
	v_max3_f32 v41, v41, v42, |v33|
	v_max3_f32 v43, v43, v44, v48
	v_max_f32_e32 v41, v41, v43
	v_pk_add_f32 v[2:3], v[2:3], v[18:19]
	v_pk_add_f32 v[4:5], v[4:5], v[20:21]
	v_max_f32_dpp v41, v41, v41 quad_perm:[1,0,3,2] row_mask:0xf bank_mask:0xf
	v_pk_add_f32 v[6:7], v[6:7], v[22:23]
	v_pk_add_f32 v[8:9], v[8:9], v[24:25]
	v_max_f32_dpp v41, v41, v41 quad_perm:[2,3,0,1] row_mask:0xf bank_mask:0xf
	v_pk_add_f32 v[10:11], v[10:11], v[26:27]
	v_pk_add_f32 v[12:13], v[12:13], v[28:29]
	v_max_f32_dpp v41, v41, v41 row_half_mirror row_mask:0xf bank_mask:0xf
	v_pk_add_f32 v[14:15], v[14:15], v[30:31]
	v_pk_add_f32 v[16:17], v[16:17], v[32:33]
	v_max_f32_dpp v41, v41, v41 row_mirror row_mask:0xf bank_mask:0xf
	s_nop 1
	v_max_f32_dpp v41, v41, v41 row_bcast:15 row_mask:0xa bank_mask:0xf
	s_nop 1
	v_max_f32_dpp v41, v41, v41 row_bcast:31 row_mask:0xc bank_mask:0xf
	s_nop 1
	v_readlane_b32 s28, v41, 63
	s_nop 1
	v_div_scale_f32 v48, s[30:31], s28, s28, v47
	v_rcp_f32_e32 v49, v48
	s_nop 0
	v_fma_f32 v50, -v48, v49, 1.0
	v_fmac_f32_e32 v49, v50, v49
	v_mov_b32_e32 v50, s28
	v_div_scale_f32 v50, vcc, s32, v50, s32
	v_mul_f32_e32 v51, v50, v49
	v_fma_f32 v52, -v48, v51, v50
	v_fmac_f32_e32 v51, v52, v49
	v_fma_f32 v48, -v48, v51, v50
	v_div_fmas_f32 v48, v48, v49, v51
	v_div_fixup_f32 v48, v48, s28, v47
	v_cmp_gt_f32_e64 vcc, s28, 0
	v_writelane_b32 v40, s28, 19
	s_nop 0
	v_cndmask_b32_e32 v48, 0, v48, vcc
	v_fmaak_f32 v49, v18, v48, 0x4b400000
	v_fmaak_f32 v50, v19, v48, 0x4b400000
	v_fmaak_f32 v51, v20, v48, 0x4b400000
	v_fmaak_f32 v52, v21, v48, 0x4b400000
	v_perm_b32 v49, v50, v49, s33
	v_perm_b32 v51, v52, v51, s34
	v_or_b32_e32 v49, v49, v51
	s_add_u32 s20, s20, 0x400
	s_addc_u32 s21, s21, 0
	s_add_u32 s22, s22, 0x400
	s_addc_u32 s23, s23, 0
	s_add_u32 s24, s24, 0x400
	s_addc_u32 s25, s25, 0
	s_add_u32 s26, s26, 0x400
	s_addc_u32 s27, s27, 0
	global_store_dword v39, v49, s[20:21]
	v_fmaak_f32 v41, v22, v48, 0x4b400000
	v_fmaak_f32 v42, v23, v48, 0x4b400000
	v_fmaak_f32 v43, v24, v48, 0x4b400000
	v_fmaak_f32 v44, v25, v48, 0x4b400000
	v_perm_b32 v41, v42, v41, s33
	v_perm_b32 v43, v44, v43, s34
	v_or_b32_e32 v41, v41, v43
	global_store_dword v39, v41, s[22:23]
	v_fmaak_f32 v49, v26, v48, 0x4b400000
	v_fmaak_f32 v50, v27, v48, 0x4b400000
	v_fmaak_f32 v51, v28, v48, 0x4b400000
	v_fmaak_f32 v52, v29, v48, 0x4b400000
	v_perm_b32 v49, v50, v49, s33
	v_perm_b32 v51, v52, v51, s34
	v_or_b32_e32 v49, v49, v51
	global_store_dword v39, v49, s[24:25]
	v_fmaak_f32 v41, v30, v48, 0x4b400000
	v_fmaak_f32 v42, v31, v48, 0x4b400000
	v_fmaak_f32 v43, v32, v48, 0x4b400000
	v_fmaak_f32 v44, v33, v48, 0x4b400000
	v_perm_b32 v41, v42, v41, s33
	v_perm_b32 v43, v44, v43, s34
	v_or_b32_e32 v41, v41, v43
	global_store_dword v39, v41, s[26:27]
	s_waitcnt vmcnt(4)
	ds_read_b128 v[18:21], v38 offset:0
	ds_read_b128 v[22:25], v38 offset:1024
	ds_read_b128 v[26:29], v38 offset:2048
	ds_read_b128 v[30:33], v38 offset:3072
	s_waitcnt lgkmcnt(0)
	s_mov_b32 m0, s36
	s_nop 0
	global_load_lds_dwordx4 v34, s[16:17] nt
	global_load_lds_dwordx4 v34, s[16:17] offset:1024 nt
	global_load_lds_dwordx4 v34, s[16:17] offset:2048 nt
	global_load_lds_dwordx4 v35, s[16:17] offset:3072 nt
	s_add_u32 s16, s16, 0x7d00
	s_addc_u32 s17, s17, 0
	v_cndmask_b32_e64 v30, 0, v30, s[18:19]
	v_cndmask_b32_e64 v31, 0, v31, s[18:19]
	v_cndmask_b32_e64 v32, 0, v32, s[18:19]
	v_cndmask_b32_e64 v33, 0, v33, s[18:19]
	v_max3_f32 v41, |v18|, |v19|, |v20|
	v_max3_f32 v42, |v21|, |v22|, |v23|
	v_max3_f32 v43, |v24|, |v25|, |v26|
	v_max3_f32 v44, |v27|, |v28|, |v29|
	v_max3_f32 v48, |v30|, |v31|, |v32|
	v_max3_f32 v41, v41, v42, |v33|
	v_max3_f32 v43, v43, v44, v48
	v_max_f32_e32 v41, v41, v43
	v_pk_add_f32 v[2:3], v[2:3], v[18:19]
	v_pk_add_f32 v[4:5], v[4:5], v[20:21]
	v_max_f32_dpp v41, v41, v41 quad_perm:[1,0,3,2] row_mask:0xf bank_mask:0xf
	v_pk_add_f32 v[6:7], v[6:7], v[22:23]
	v_pk_add_f32 v[8:9], v[8:9], v[24:25]
	v_max_f32_dpp v41, v41, v41 quad_perm:[2,3,0,1] row_mask:0xf bank_mask:0xf
	v_pk_add_f32 v[10:11], v[10:11], v[26:27]
	v_pk_add_f32 v[12:13], v[12:13], v[28:29]
	v_max_f32_dpp v41, v41, v41 row_half_mirror row_mask:0xf bank_mask:0xf
	v_pk_add_f32 v[14:15], v[14:15], v[30:31]
	v_pk_add_f32 v[16:17], v[16:17], v[32:33]
	v_max_f32_dpp v41, v41, v41 row_mirror row_mask:0xf bank_mask:0xf
	s_nop 1
	v_max_f32_dpp v41, v41, v41 row_bcast:15 row_mask:0xa bank_mask:0xf
	s_nop 1
	v_max_f32_dpp v41, v41, v41 row_bcast:31 row_mask:0xc bank_mask:0xf
	s_nop 1
	v_readlane_b32 s28, v41, 63
	s_nop 1
	v_div_scale_f32 v48, s[30:31], s28, s28, v47
	v_rcp_f32_e32 v49, v48
	s_nop 0
	v_fma_f32 v50, -v48, v49, 1.0
	v_fmac_f32_e32 v49, v50, v49
	v_mov_b32_e32 v50, s28
	v_div_scale_f32 v50, vcc, s32, v50, s32
	v_mul_f32_e32 v51, v50, v49
	v_fma_f32 v52, -v48, v51, v50
	v_fmac_f32_e32 v51, v52, v49
	v_fma_f32 v48, -v48, v51, v50
	v_div_fmas_f32 v48, v48, v49, v51
	v_div_fixup_f32 v48, v48, s28, v47
	v_cmp_gt_f32_e64 vcc, s28, 0
	v_writelane_b32 v40, s28, 20
	s_nop 0
	v_cndmask_b32_e32 v48, 0, v48, vcc
	v_fmaak_f32 v49, v18, v48, 0x4b400000
	v_fmaak_f32 v50, v19, v48, 0x4b400000
	v_fmaak_f32 v51, v20, v48, 0x4b400000
	v_fmaak_f32 v52, v21, v48, 0x4b400000
	v_perm_b32 v49, v50, v49, s33
	v_perm_b32 v51, v52, v51, s34
	v_or_b32_e32 v49, v49, v51
	s_add_u32 s20, s20, 0x400
	s_addc_u32 s21, s21, 0
	s_add_u32 s22, s22, 0x400
	s_addc_u32 s23, s23, 0
	s_add_u32 s24, s24, 0x400
	s_addc_u32 s25, s25, 0
	s_add_u32 s26, s26, 0x400
	s_addc_u32 s27, s27, 0
	global_store_dword v39, v49, s[20:21]
	v_fmaak_f32 v41, v22, v48, 0x4b400000
	v_fmaak_f32 v42, v23, v48, 0x4b400000
	v_fmaak_f32 v43, v24, v48, 0x4b400000
	v_fmaak_f32 v44, v25, v48, 0x4b400000
	v_perm_b32 v41, v42, v41, s33
	v_perm_b32 v43, v44, v43, s34
	v_or_b32_e32 v41, v41, v43
	global_store_dword v39, v41, s[22:23]
	v_fmaak_f32 v49, v26, v48, 0x4b400000
	v_fmaak_f32 v50, v27, v48, 0x4b400000
	v_fmaak_f32 v51, v28, v48, 0x4b400000
	v_fmaak_f32 v52, v29, v48, 0x4b400000
	v_perm_b32 v49, v50, v49, s33
	v_perm_b32 v51, v52, v51, s34
	v_or_b32_e32 v49, v49, v51
	global_store_dword v39, v49, s[24:25]
	v_fmaak_f32 v41, v30, v48, 0x4b400000
	v_fmaak_f32 v42, v31, v48, 0x4b400000
	v_fmaak_f32 v43, v32, v48, 0x4b400000
	v_fmaak_f32 v44, v33, v48, 0x4b400000
	v_perm_b32 v41, v42, v41, s33
	v_perm_b32 v43, v44, v43, s34
	v_or_b32_e32 v41, v41, v43
	global_store_dword v39, v41, s[26:27]
	s_waitcnt vmcnt(4)
	ds_read_b128 v[18:21], v38 offset:4096
	ds_read_b128 v[22:25], v38 offset:5120
	ds_read_b128 v[26:29], v38 offset:6144
	ds_read_b128 v[30:33], v38 offset:7168
	s_waitcnt lgkmcnt(0)
	s_mov_b32 m0, s35
	s_nop 0
	global_load_lds_dwordx4 v34, s[16:17] nt
	global_load_lds_dwordx4 v34, s[16:17] offset:1024 nt
	global_load_lds_dwordx4 v34, s[16:17] offset:2048 nt
	global_load_lds_dwordx4 v35, s[16:17] offset:3072 nt
	s_add_u32 s16, s16, 0x7d00
	s_addc_u32 s17, s17, 0
	v_cndmask_b32_e64 v30, 0, v30, s[18:19]
	v_cndmask_b32_e64 v31, 0, v31, s[18:19]
	v_cndmask_b32_e64 v32, 0, v32, s[18:19]
	v_cndmask_b32_e64 v33, 0, v33, s[18:19]
	v_max3_f32 v41, |v18|, |v19|, |v20|
	v_max3_f32 v42, |v21|, |v22|, |v23|
	v_max3_f32 v43, |v24|, |v25|, |v26|
	v_max3_f32 v44, |v27|, |v28|, |v29|
	v_max3_f32 v48, |v30|, |v31|, |v32|
	v_max3_f32 v41, v41, v42, |v33|
	v_max3_f32 v43, v43, v44, v48
	v_max_f32_e32 v41, v41, v43
	v_pk_add_f32 v[2:3], v[2:3], v[18:19]
	v_pk_add_f32 v[4:5], v[4:5], v[20:21]
	v_max_f32_dpp v41, v41, v41 quad_perm:[1,0,3,2] row_mask:0xf bank_mask:0xf
	v_pk_add_f32 v[6:7], v[6:7], v[22:23]
	v_pk_add_f32 v[8:9], v[8:9], v[24:25]
	v_max_f32_dpp v41, v41, v41 quad_perm:[2,3,0,1] row_mask:0xf bank_mask:0xf
	v_pk_add_f32 v[10:11], v[10:11], v[26:27]
	v_pk_add_f32 v[12:13], v[12:13], v[28:29]
	v_max_f32_dpp v41, v41, v41 row_half_mirror row_mask:0xf bank_mask:0xf
	v_pk_add_f32 v[14:15], v[14:15], v[30:31]
	v_pk_add_f32 v[16:17], v[16:17], v[32:33]
	v_max_f32_dpp v41, v41, v41 row_mirror row_mask:0xf bank_mask:0xf
	s_nop 1
	v_max_f32_dpp v41, v41, v41 row_bcast:15 row_mask:0xa bank_mask:0xf
	s_nop 1
	v_max_f32_dpp v41, v41, v41 row_bcast:31 row_mask:0xc bank_mask:0xf
	s_nop 1
	v_readlane_b32 s28, v41, 63
	s_nop 1
	v_div_scale_f32 v48, s[30:31], s28, s28, v47
	v_rcp_f32_e32 v49, v48
	s_nop 0
	v_fma_f32 v50, -v48, v49, 1.0
	v_fmac_f32_e32 v49, v50, v49
	v_mov_b32_e32 v50, s28
	v_div_scale_f32 v50, vcc, s32, v50, s32
	v_mul_f32_e32 v51, v50, v49
	v_fma_f32 v52, -v48, v51, v50
	v_fmac_f32_e32 v51, v52, v49
	v_fma_f32 v48, -v48, v51, v50
	v_div_fmas_f32 v48, v48, v49, v51
	v_div_fixup_f32 v48, v48, s28, v47
	v_cmp_gt_f32_e64 vcc, s28, 0
	v_writelane_b32 v40, s28, 21
	s_nop 0
	v_cndmask_b32_e32 v48, 0, v48, vcc
	v_fmaak_f32 v49, v18, v48, 0x4b400000
	v_fmaak_f32 v50, v19, v48, 0x4b400000
	v_fmaak_f32 v51, v20, v48, 0x4b400000
	v_fmaak_f32 v52, v21, v48, 0x4b400000
	v_perm_b32 v49, v50, v49, s33
	v_perm_b32 v51, v52, v51, s34
	v_or_b32_e32 v49, v49, v51
	s_add_u32 s20, s20, 0x400
	s_addc_u32 s21, s21, 0
	s_add_u32 s22, s22, 0x400
	s_addc_u32 s23, s23, 0
	s_add_u32 s24, s24, 0x400
	s_addc_u32 s25, s25, 0
	s_add_u32 s26, s26, 0x400
	s_addc_u32 s27, s27, 0
	global_store_dword v39, v49, s[20:21]
	v_fmaak_f32 v41, v22, v48, 0x4b400000
	v_fmaak_f32 v42, v23, v48, 0x4b400000
	v_fmaak_f32 v43, v24, v48, 0x4b400000
	v_fmaak_f32 v44, v25, v48, 0x4b400000
	v_perm_b32 v41, v42, v41, s33
	v_perm_b32 v43, v44, v43, s34
	v_or_b32_e32 v41, v41, v43
	global_store_dword v39, v41, s[22:23]
	v_fmaak_f32 v49, v26, v48, 0x4b400000
	v_fmaak_f32 v50, v27, v48, 0x4b400000
	v_fmaak_f32 v51, v28, v48, 0x4b400000
	v_fmaak_f32 v52, v29, v48, 0x4b400000
	v_perm_b32 v49, v50, v49, s33
	v_perm_b32 v51, v52, v51, s34
	v_or_b32_e32 v49, v49, v51
	global_store_dword v39, v49, s[24:25]
	v_fmaak_f32 v41, v30, v48, 0x4b400000
	v_fmaak_f32 v42, v31, v48, 0x4b400000
	v_fmaak_f32 v43, v32, v48, 0x4b400000
	v_fmaak_f32 v44, v33, v48, 0x4b400000
	v_perm_b32 v41, v42, v41, s33
	v_perm_b32 v43, v44, v43, s34
	v_or_b32_e32 v41, v41, v43
	global_store_dword v39, v41, s[26:27]
	s_waitcnt vmcnt(4)
	ds_read_b128 v[18:21], v38 offset:0
	ds_read_b128 v[22:25], v38 offset:1024
	ds_read_b128 v[26:29], v38 offset:2048
	ds_read_b128 v[30:33], v38 offset:3072
	s_waitcnt lgkmcnt(0)
	s_mov_b32 m0, s36
	s_nop 0
	global_load_lds_dwordx4 v34, s[16:17] nt
	global_load_lds_dwordx4 v34, s[16:17] offset:1024 nt
	global_load_lds_dwordx4 v34, s[16:17] offset:2048 nt
	global_load_lds_dwordx4 v35, s[16:17] offset:3072 nt
	s_add_u32 s16, s16, 0x7d00
	s_addc_u32 s17, s17, 0
	v_cndmask_b32_e64 v30, 0, v30, s[18:19]
	v_cndmask_b32_e64 v31, 0, v31, s[18:19]
	v_cndmask_b32_e64 v32, 0, v32, s[18:19]
	v_cndmask_b32_e64 v33, 0, v33, s[18:19]
	v_max3_f32 v41, |v18|, |v19|, |v20|
	v_max3_f32 v42, |v21|, |v22|, |v23|
	v_max3_f32 v43, |v24|, |v25|, |v26|
	v_max3_f32 v44, |v27|, |v28|, |v29|
	v_max3_f32 v48, |v30|, |v31|, |v32|
	v_max3_f32 v41, v41, v42, |v33|
	v_max3_f32 v43, v43, v44, v48
	v_max_f32_e32 v41, v41, v43
	v_pk_add_f32 v[2:3], v[2:3], v[18:19]
	v_pk_add_f32 v[4:5], v[4:5], v[20:21]
	v_max_f32_dpp v41, v41, v41 quad_perm:[1,0,3,2] row_mask:0xf bank_mask:0xf
	v_pk_add_f32 v[6:7], v[6:7], v[22:23]
	v_pk_add_f32 v[8:9], v[8:9], v[24:25]
	v_max_f32_dpp v41, v41, v41 quad_perm:[2,3,0,1] row_mask:0xf bank_mask:0xf
	v_pk_add_f32 v[10:11], v[10:11], v[26:27]
	v_pk_add_f32 v[12:13], v[12:13], v[28:29]
	v_max_f32_dpp v41, v41, v41 row_half_mirror row_mask:0xf bank_mask:0xf
	v_pk_add_f32 v[14:15], v[14:15], v[30:31]
	v_pk_add_f32 v[16:17], v[16:17], v[32:33]
	v_max_f32_dpp v41, v41, v41 row_mirror row_mask:0xf bank_mask:0xf
	s_nop 1
	v_max_f32_dpp v41, v41, v41 row_bcast:15 row_mask:0xa bank_mask:0xf
	s_nop 1
	v_max_f32_dpp v41, v41, v41 row_bcast:31 row_mask:0xc bank_mask:0xf
	s_nop 1
	v_readlane_b32 s28, v41, 63
	s_nop 1
	v_div_scale_f32 v48, s[30:31], s28, s28, v47
	v_rcp_f32_e32 v49, v48
	s_nop 0
	v_fma_f32 v50, -v48, v49, 1.0
	v_fmac_f32_e32 v49, v50, v49
	v_mov_b32_e32 v50, s28
	v_div_scale_f32 v50, vcc, s32, v50, s32
	v_mul_f32_e32 v51, v50, v49
	v_fma_f32 v52, -v48, v51, v50
	v_fmac_f32_e32 v51, v52, v49
	v_fma_f32 v48, -v48, v51, v50
	v_div_fmas_f32 v48, v48, v49, v51
	v_div_fixup_f32 v48, v48, s28, v47
	v_cmp_gt_f32_e64 vcc, s28, 0
	v_writelane_b32 v40, s28, 22
	s_nop 0
	v_cndmask_b32_e32 v48, 0, v48, vcc
	v_fmaak_f32 v49, v18, v48, 0x4b400000
	v_fmaak_f32 v50, v19, v48, 0x4b400000
	v_fmaak_f32 v51, v20, v48, 0x4b400000
	v_fmaak_f32 v52, v21, v48, 0x4b400000
	v_perm_b32 v49, v50, v49, s33
	v_perm_b32 v51, v52, v51, s34
	v_or_b32_e32 v49, v49, v51
	s_add_u32 s20, s20, 0x400
	s_addc_u32 s21, s21, 0
	s_add_u32 s22, s22, 0x400
	s_addc_u32 s23, s23, 0
	s_add_u32 s24, s24, 0x400
	s_addc_u32 s25, s25, 0
	s_add_u32 s26, s26, 0x400
	s_addc_u32 s27, s27, 0
	global_store_dword v39, v49, s[20:21]
	v_fmaak_f32 v41, v22, v48, 0x4b400000
	v_fmaak_f32 v42, v23, v48, 0x4b400000
	v_fmaak_f32 v43, v24, v48, 0x4b400000
	v_fmaak_f32 v44, v25, v48, 0x4b400000
	v_perm_b32 v41, v42, v41, s33
	v_perm_b32 v43, v44, v43, s34
	v_or_b32_e32 v41, v41, v43
	global_store_dword v39, v41, s[22:23]
	v_fmaak_f32 v49, v26, v48, 0x4b400000
	v_fmaak_f32 v50, v27, v48, 0x4b400000
	v_fmaak_f32 v51, v28, v48, 0x4b400000
	v_fmaak_f32 v52, v29, v48, 0x4b400000
	v_perm_b32 v49, v50, v49, s33
	v_perm_b32 v51, v52, v51, s34
	v_or_b32_e32 v49, v49, v51
	global_store_dword v39, v49, s[24:25]
	v_fmaak_f32 v41, v30, v48, 0x4b400000
	v_fmaak_f32 v42, v31, v48, 0x4b400000
	v_fmaak_f32 v43, v32, v48, 0x4b400000
	v_fmaak_f32 v44, v33, v48, 0x4b400000
	v_perm_b32 v41, v42, v41, s33
	v_perm_b32 v43, v44, v43, s34
	v_or_b32_e32 v41, v41, v43
	global_store_dword v39, v41, s[26:27]
	s_waitcnt vmcnt(4)
	ds_read_b128 v[18:21], v38 offset:4096
	ds_read_b128 v[22:25], v38 offset:5120
	ds_read_b128 v[26:29], v38 offset:6144
	ds_read_b128 v[30:33], v38 offset:7168
	s_waitcnt lgkmcnt(0)
	s_cmp_eq_u32 s29, 1
	s_cbranch_scc0 .Lk1_nodma24
	s_mov_b32 m0, s35
	s_nop 0
	global_load_lds_dwordx4 v34, s[16:17] nt
	global_load_lds_dwordx4 v34, s[16:17] offset:1024 nt
	global_load_lds_dwordx4 v34, s[16:17] offset:2048 nt
	global_load_lds_dwordx4 v35, s[16:17] offset:3072 nt
	s_add_u32 s16, s16, 0x7d00
	s_addc_u32 s17, s17, 0

_Z15k3_pairs_slicedPKDv4_jPKfPKiS5_PiPf:
	s_load_dwordx8 s[4:11], s[0:1], 0x0
	s_load_dwordx2 s[12:13], s[0:1], 0x20
	v_and_b32_e32 v1, 63, v0
	v_lshrrev_b32_e32 v2, 6, v0
	s_and_b32 s14, s2, 7
	s_lshr_b32 s15, s2, 3
	v_readfirstlane_b32 s16, v2
	s_lshl_b32 s17, s15, 10
	s_lshl_b32 s24, s16, 8
	s_add_u32 s17, s17, s24
	v_and_b32_e32 v2, 7, v1
	v_lshrrev_b32_e32 v3, 3, v1
	v_cmp_eq_u32_e64 s[40:41], 0, v2
	v_cmp_eq_u32_e64 s[42:43], 1, v2
	v_cmp_eq_u32_e64 s[44:45], 2, v2
	v_cmp_eq_u32_e64 s[46:47], 3, v2
	v_cmp_eq_u32_e64 s[48:49], 4, v2
	v_cmp_eq_u32_e64 s[50:51], 5, v2
	v_cmp_eq_u32_e64 s[52:53], 6, v2
	v_cmp_eq_u32_e64 s[54:55], 7, v2
	v_lshl_add_u32 v28, v2, 3, v3
	v_lshlrev_b32_e32 v28, 2, v28
	v_lshlrev_b32_e32 v3, 2, v3
	v_lshlrev_b32_e32 v2, 4, v2
	v_lshlrev_b32_e32 v29, 2, v1
	v_lshlrev_b32_e32 v30, 2, v2
	s_lshl_b32 s26, s17, 2
	s_lshl_b32 s27, s14, 9
	s_mul_i32 s34, s14, 0xc35000
	s_waitcnt lgkmcnt(0)
	s_add_u32 s24, s8, s26
	s_addc_u32 s25, s9, 0
	s_add_u32 s28, s10, s26
	s_addc_u32 s29, s11, 0
	global_load_dword v20, v29, s[24:25]
	global_load_dword v24, v29, s[28:29]
	global_load_dword v21, v29, s[24:25] offset:256
	global_load_dword v25, v29, s[28:29] offset:256
	global_load_dword v22, v29, s[24:25] offset:512
	global_load_dword v26, v29, s[28:29] offset:512
	global_load_dword v23, v29, s[24:25] offset:768
	global_load_dword v27, v29, s[28:29] offset:768
	s_add_u32 s30, s6, s27
	s_addc_u32 s31, s7, 0
	global_load_dwordx4 v[4:7], v30, s[30:31]
	global_load_dwordx4 v[8:11], v30, s[30:31] offset:16
	global_load_dwordx4 v[12:15], v30, s[30:31] offset:32
	global_load_dwordx4 v[16:19], v30, s[30:31] offset:48
	s_add_u32 s18, s4, s34
	s_addc_u32 s19, s5, 0
	s_add_u32 s21, s14, 2
	s_cmp_lt_u32 s14, 2
	s_cselect_b32 s21, s14, s21
	s_lshl_b32 s21, s21, 19
	s_add_u32 s22, s14, 10
	s_lshl_b32 s22, s22, 19
	s_sub_u32 s23, s14, 6
	s_lshl_b32 s23, s23, 19
	s_sub_u32 s23, s23, 0x262a80
	s_cmp_lt_u32 s14, 6
	s_cselect_b32 s33, s22, s23
	s_ashr_i32 s35, s33, 31
	s_mov_b64 s[20:21], s[12:13]
	s_add_u32 s22, s12, 0x80000
	s_addc_u32 s23, s13, 0
	s_add_u32 s20, s20, s26
	s_addc_u32 s21, s21, 0
	s_add_u32 s22, s22, s26
	s_addc_u32 s23, s23, 0
	s_waitcnt vmcnt(4)
	ds_bpermute_b32 v104, v3, v20
	ds_bpermute_b32 v105, v3, v24
	s_waitcnt lgkmcnt(0)
	v_lshl_add_u32 v106, v104, 7, v2
	v_lshl_add_u32 v107, v105, 7, v2
	global_load_dwordx4 v[32:35], v106, s[18:19]
	global_load_dwordx4 v[36:39], v107, s[18:19]
	ds_bpermute_b32 v104, v3, v20 offset:32
	ds_bpermute_b32 v105, v3, v24 offset:32
	s_waitcnt lgkmcnt(0)
	v_lshl_add_u32 v106, v104, 7, v2
	v_lshl_add_u32 v107, v105, 7, v2
	global_load_dwordx4 v[40:43], v106, s[18:19]
	global_load_dwordx4 v[44:47], v107, s[18:19]
	ds_bpermute_b32 v104, v3, v20 offset:64
	ds_bpermute_b32 v105, v3, v24 offset:64
	s_waitcnt lgkmcnt(0)
	v_lshl_add_u32 v106, v104, 7, v2
	v_lshl_add_u32 v107, v105, 7, v2
	global_load_dwordx4 v[48:51], v106, s[18:19]
	global_load_dwordx4 v[52:55], v107, s[18:19]
	ds_bpermute_b32 v104, v3, v20 offset:96
	ds_bpermute_b32 v105, v3, v24 offset:96
	s_waitcnt lgkmcnt(0)
	v_lshl_add_u32 v106, v104, 7, v2
	v_lshl_add_u32 v107, v105, 7, v2
	global_load_dwordx4 v[56:59], v106, s[18:19]
	global_load_dwordx4 v[60:63], v107, s[18:19]
	ds_bpermute_b32 v104, v3, v20 offset:128
	ds_bpermute_b32 v105, v3, v24 offset:128
	s_waitcnt lgkmcnt(0)
	v_lshl_add_u32 v106, v104, 7, v2
	v_lshl_add_u32 v107, v105, 7, v2
	global_load_dwordx4 v[64:67], v106, s[18:19]
	global_load_dwordx4 v[68:71], v107, s[18:19]
	ds_bpermute_b32 v104, v3, v20 offset:160
	ds_bpermute_b32 v105, v3, v24 offset:160
	s_waitcnt lgkmcnt(0)
	v_lshl_add_u32 v106, v104, 7, v2
	v_lshl_add_u32 v107, v105, 7, v2
	global_load_dwordx4 v[72:75], v106, s[18:19]
	global_load_dwordx4 v[76:79], v107, s[18:19]
	ds_bpermute_b32 v104, v3, v20 offset:192
	ds_bpermute_b32 v105, v3, v24 offset:192
	s_waitcnt lgkmcnt(0)
	v_lshl_add_u32 v106, v104, 7, v2
	v_lshl_add_u32 v107, v105, 7, v2
	global_load_dwordx4 v[80:83], v106, s[18:19]
	global_load_dwordx4 v[84:87], v107, s[18:19]
	ds_bpermute_b32 v104, v3, v20 offset:224
	ds_bpermute_b32 v105, v3, v24 offset:224
	s_waitcnt lgkmcnt(0)
	v_lshl_add_u32 v106, v104, 7, v2
	v_lshl_add_u32 v107, v105, 7, v2
	global_load_dwordx4 v[88:91], v106, s[18:19]
	global_load_dwordx4 v[92:95], v107, s[18:19]
	ds_bpermute_b32 v104, v3, v21
	ds_bpermute_b32 v105, v3, v25
	s_waitcnt vmcnt(14)
	v_mov_b32_e32 v96, 0
	v_dot4c_i32_i8_e32 v96, v32, v36
	v_cvt_f32_i32_sdwa v98, sext(v32) dst_sel:DWORD dst_unused:UNUSED_PAD src0_sel:BYTE_0
	v_cvt_f32_i32_sdwa v99, sext(v33) dst_sel:DWORD dst_unused:UNUSED_PAD src0_sel:BYTE_0
	v_dot4c_i32_i8_e32 v96, v33, v37
	v_cvt_f32_i32_sdwa v100, sext(v34) dst_sel:DWORD dst_unused:UNUSED_PAD src0_sel:BYTE_0
	v_dot4c_i32_i8_e32 v96, v34, v38
	v_cvt_f32_i32_sdwa v101, sext(v35) dst_sel:DWORD dst_unused:UNUSED_PAD src0_sel:BYTE_0
	v_dot4c_i32_i8_e32 v96, v35, v39
	v_fma_f32 v97, v98, v4, 0
	v_cvt_f32_i32_sdwa v98, sext(v32) dst_sel:DWORD dst_unused:UNUSED_PAD src0_sel:BYTE_1
	v_fmac_f32_e32 v97, v99, v8
	v_cvt_f32_i32_sdwa v99, sext(v33) dst_sel:DWORD dst_unused:UNUSED_PAD src0_sel:BYTE_1
	v_fmac_f32_e32 v97, v100, v12
	v_cvt_f32_i32_sdwa v100, sext(v34) dst_sel:DWORD dst_unused:UNUSED_PAD src0_sel:BYTE_1
	v_fmac_f32_e32 v97, v101, v16
	v_cvt_f32_i32_sdwa v101, sext(v35) dst_sel:DWORD dst_unused:UNUSED_PAD src0_sel:BYTE_1
	v_add_u32_dpp v96, v96, v96 quad_perm:[1,0,3,2] row_mask:0xf bank_mask:0xf bound_ctrl:1
	v_fmac_f32_e32 v97, v98, v5
	v_cvt_f32_i32_sdwa v98, sext(v32) dst_sel:DWORD dst_unused:UNUSED_PAD src0_sel:BYTE_2
	v_fmac_f32_e32 v97, v99, v9
	v_cvt_f32_i32_sdwa v99, sext(v33) dst_sel:DWORD dst_unused:UNUSED_PAD src0_sel:BYTE_2
	v_fmac_f32_e32 v97, v100, v13
	v_cvt_f32_i32_sdwa v100, sext(v34) dst_sel:DWORD dst_unused:UNUSED_PAD src0_sel:BYTE_2
	v_add_u32_dpp v96, v96, v96 quad_perm:[2,3,0,1] row_mask:0xf bank_mask:0xf bound_ctrl:1
	v_fmac_f32_e32 v97, v101, v17
	v_cvt_f32_i32_sdwa v101, sext(v35) dst_sel:DWORD dst_unused:UNUSED_PAD src0_sel:BYTE_2
	v_fmac_f32_e32 v97, v98, v6
	v_cvt_f32_i32_sdwa v98, sext(v32) dst_sel:DWORD dst_unused:UNUSED_PAD src0_sel:BYTE_3
	v_fmac_f32_e32 v97, v99, v10
	v_cvt_f32_i32_sdwa v99, sext(v33) dst_sel:DWORD dst_unused:UNUSED_PAD src0_sel:BYTE_3
	v_add_u32_dpp v96, v96, v96 row_half_mirror row_mask:0xf bank_mask:0xf bound_ctrl:1
	v_fmac_f32_e32 v97, v100, v14
	v_cvt_f32_i32_sdwa v100, sext(v34) dst_sel:DWORD dst_unused:UNUSED_PAD src0_sel:BYTE_3
	v_fmac_f32_e32 v97, v101, v18
	v_cvt_f32_i32_sdwa v101, sext(v35) dst_sel:DWORD dst_unused:UNUSED_PAD src0_sel:BYTE_3
	v_fmac_f32_e32 v97, v98, v7
	v_fmac_f32_e32 v97, v99, v11
	v_fmac_f32_e32 v97, v100, v15
	v_fmac_f32_e32 v97, v101, v19
	v_cndmask_b32_e64 v102, 0, v96, s[40:41]
	s_waitcnt lgkmcnt(0)
	v_add_f32_dpp v97, v97, v97 quad_perm:[1,0,3,2] row_mask:0xf bank_mask:0xf bound_ctrl:1
	v_lshl_add_u32 v106, v104, 7, v2
	v_lshl_add_u32 v107, v105, 7, v2
	v_add_f32_dpp v97, v97, v97 quad_perm:[2,3,0,1] row_mask:0xf bank_mask:0xf bound_ctrl:1
	global_load_dwordx4 v[32:35], v106, s[18:19]
	global_load_dwordx4 v[36:39], v107, s[18:19]
	v_add_f32_dpp v97, v97, v97 row_half_mirror row_mask:0xf bank_mask:0xf bound_ctrl:1
	v_cndmask_b32_e64 v103, 0, v97, s[40:41]
	ds_bpermute_b32 v104, v3, v21 offset:32
	ds_bpermute_b32 v105, v3, v25 offset:32
	s_waitcnt vmcnt(14)
	v_mov_b32_e32 v96, 0
	v_dot4c_i32_i8_e32 v96, v40, v44
	v_cvt_f32_i32_sdwa v98, sext(v40) dst_sel:DWORD dst_unused:UNUSED_PAD src0_sel:BYTE_0
	v_cvt_f32_i32_sdwa v99, sext(v41) dst_sel:DWORD dst_unused:UNUSED_PAD src0_sel:BYTE_0
	v_dot4c_i32_i8_e32 v96, v41, v45
	v_cvt_f32_i32_sdwa v100, sext(v42) dst_sel:DWORD dst_unused:UNUSED_PAD src0_sel:BYTE_0
	v_dot4c_i32_i8_e32 v96, v42, v46
	v_cvt_f32_i32_sdwa v101, sext(v43) dst_sel:DWORD dst_unused:UNUSED_PAD src0_sel:BYTE_0
	v_dot4c_i32_i8_e32 v96, v43, v47
	v_fma_f32 v97, v98, v4, 0
	v_cvt_f32_i32_sdwa v98, sext(v40) dst_sel:DWORD dst_unused:UNUSED_PAD src0_sel:BYTE_1
	v_fmac_f32_e32 v97, v99, v8
	v_cvt_f32_i32_sdwa v99, sext(v41) dst_sel:DWORD dst_unused:UNUSED_PAD src0_sel:BYTE_1
	v_fmac_f32_e32 v97, v100, v12
	v_cvt_f32_i32_sdwa v100, sext(v42) dst_sel:DWORD dst_unused:UNUSED_PAD src0_sel:BYTE_1
	v_fmac_f32_e32 v97, v101, v16
	v_cvt_f32_i32_sdwa v101, sext(v43) dst_sel:DWORD dst_unused:UNUSED_PAD src0_sel:BYTE_1
	v_add_u32_dpp v96, v96, v96 quad_perm:[1,0,3,2] row_mask:0xf bank_mask:0xf bound_ctrl:1
	v_fmac_f32_e32 v97, v98, v5
	v_cvt_f32_i32_sdwa v98, sext(v40) dst_sel:DWORD dst_unused:UNUSED_PAD src0_sel:BYTE_2
	v_fmac_f32_e32 v97, v99, v9
	v_cvt_f32_i32_sdwa v99, sext(v41) dst_sel:DWORD dst_unused:UNUSED_PAD src0_sel:BYTE_2
	v_fmac_f32_e32 v97, v100, v13
	v_cvt_f32_i32_sdwa v100, sext(v42) dst_sel:DWORD dst_unused:UNUSED_PAD src0_sel:BYTE_2
	v_add_u32_dpp v96, v96, v96 quad_perm:[2,3,0,1] row_mask:0xf bank_mask:0xf bound_ctrl:1
	v_fmac_f32_e32 v97, v101, v17
	v_cvt_f32_i32_sdwa v101, sext(v43) dst_sel:DWORD dst_unused:UNUSED_PAD src0_sel:BYTE_2
	v_fmac_f32_e32 v97, v98, v6
	v_cvt_f32_i32_sdwa v98, sext(v40) dst_sel:DWORD dst_unused:UNUSED_PAD src0_sel:BYTE_3
	v_fmac_f32_e32 v97, v99, v10
	v_cvt_f32_i32_sdwa v99, sext(v41) dst_sel:DWORD dst_unused:UNUSED_PAD src0_sel:BYTE_3
	v_add_u32_dpp v96, v96, v96 row_half_mirror row_mask:0xf bank_mask:0xf bound_ctrl:1
	v_fmac_f32_e32 v97, v100, v14
	v_cvt_f32_i32_sdwa v100, sext(v42) dst_sel:DWORD dst_unused:UNUSED_PAD src0_sel:BYTE_3
	v_fmac_f32_e32 v97, v101, v18
	v_cvt_f32_i32_sdwa v101, sext(v43) dst_sel:DWORD dst_unused:UNUSED_PAD src0_sel:BYTE_3
	v_fmac_f32_e32 v97, v98, v7
	v_fmac_f32_e32 v97, v99, v11
	v_fmac_f32_e32 v97, v100, v15
	v_fmac_f32_e32 v97, v101, v19
	v_cndmask_b32_e64 v102, v102, v96, s[42:43]
	s_waitcnt lgkmcnt(0)
	v_add_f32_dpp v97, v97, v97 quad_perm:[1,0,3,2] row_mask:0xf bank_mask:0xf bound_ctrl:1
	v_lshl_add_u32 v106, v104, 7, v2
	v_lshl_add_u32 v107, v105, 7, v2
	v_add_f32_dpp v97, v97, v97 quad_perm:[2,3,0,1] row_mask:0xf bank_mask:0xf bound_ctrl:1
	global_load_dwordx4 v[40:43], v106, s[18:19]
	global_load_dwordx4 v[44:47], v107, s[18:19]
	v_add_f32_dpp v97, v97, v97 row_half_mirror row_mask:0xf bank_mask:0xf bound_ctrl:1
	v_cndmask_b32_e64 v103, v103, v97, s[42:43]
	ds_bpermute_b32 v104, v3, v21 offset:64
	ds_bpermute_b32 v105, v3, v25 offset:64
	s_waitcnt vmcnt(14)
	v_mov_b32_e32 v96, 0
	v_dot4c_i32_i8_e32 v96, v48, v52
	v_cvt_f32_i32_sdwa v98, sext(v48) dst_sel:DWORD dst_unused:UNUSED_PAD src0_sel:BYTE_0
	v_cvt_f32_i32_sdwa v99, sext(v49) dst_sel:DWORD dst_unused:UNUSED_PAD src0_sel:BYTE_0
	v_dot4c_i32_i8_e32 v96, v49, v53
	v_cvt_f32_i32_sdwa v100, sext(v50) dst_sel:DWORD dst_unused:UNUSED_PAD src0_sel:BYTE_0
	v_dot4c_i32_i8_e32 v96, v50, v54
	v_cvt_f32_i32_sdwa v101, sext(v51) dst_sel:DWORD dst_unused:UNUSED_PAD src0_sel:BYTE_0
	v_dot4c_i32_i8_e32 v96, v51, v55
	v_fma_f32 v97, v98, v4, 0
	v_cvt_f32_i32_sdwa v98, sext(v48) dst_sel:DWORD dst_unused:UNUSED_PAD src0_sel:BYTE_1
	v_fmac_f32_e32 v97, v99, v8
	v_cvt_f32_i32_sdwa v99, sext(v49) dst_sel:DWORD dst_unused:UNUSED_PAD src0_sel:BYTE_1
	v_fmac_f32_e32 v97, v100, v12
	v_cvt_f32_i32_sdwa v100, sext(v50) dst_sel:DWORD dst_unused:UNUSED_PAD src0_sel:BYTE_1
	v_fmac_f32_e32 v97, v101, v16
	v_cvt_f32_i32_sdwa v101, sext(v51) dst_sel:DWORD dst_unused:UNUSED_PAD src0_sel:BYTE_1
	v_add_u32_dpp v96, v96, v96 quad_perm:[1,0,3,2] row_mask:0xf bank_mask:0xf bound_ctrl:1
	v_fmac_f32_e32 v97, v98, v5
	v_cvt_f32_i32_sdwa v98, sext(v48) dst_sel:DWORD dst_unused:UNUSED_PAD src0_sel:BYTE_2
	v_fmac_f32_e32 v97, v99, v9
	v_cvt_f32_i32_sdwa v99, sext(v49) dst_sel:DWORD dst_unused:UNUSED_PAD src0_sel:BYTE_2
	v_fmac_f32_e32 v97, v100, v13
	v_cvt_f32_i32_sdwa v100, sext(v50) dst_sel:DWORD dst_unused:UNUSED_PAD src0_sel:BYTE_2
	v_add_u32_dpp v96, v96, v96 quad_perm:[2,3,0,1] row_mask:0xf bank_mask:0xf bound_ctrl:1
	v_fmac_f32_e32 v97, v101, v17
	v_cvt_f32_i32_sdwa v101, sext(v51) dst_sel:DWORD dst_unused:UNUSED_PAD src0_sel:BYTE_2
	v_fmac_f32_e32 v97, v98, v6
	v_cvt_f32_i32_sdwa v98, sext(v48) dst_sel:DWORD dst_unused:UNUSED_PAD src0_sel:BYTE_3
	v_fmac_f32_e32 v97, v99, v10
	v_cvt_f32_i32_sdwa v99, sext(v49) dst_sel:DWORD dst_unused:UNUSED_PAD src0_sel:BYTE_3
	v_add_u32_dpp v96, v96, v96 row_half_mirror row_mask:0xf bank_mask:0xf bound_ctrl:1
	v_fmac_f32_e32 v97, v100, v14
	v_cvt_f32_i32_sdwa v100, sext(v50) dst_sel:DWORD dst_unused:UNUSED_PAD src0_sel:BYTE_3
	v_fmac_f32_e32 v97, v101, v18
	v_cvt_f32_i32_sdwa v101, sext(v51) dst_sel:DWORD dst_unused:UNUSED_PAD src0_sel:BYTE_3
	v_fmac_f32_e32 v97, v98, v7
	v_fmac_f32_e32 v97, v99, v11
	v_fmac_f32_e32 v97, v100, v15
	v_fmac_f32_e32 v97, v101, v19
	v_cndmask_b32_e64 v102, v102, v96, s[44:45]
	s_waitcnt lgkmcnt(0)
	v_add_f32_dpp v97, v97, v97 quad_perm:[1,0,3,2] row_mask:0xf bank_mask:0xf bound_ctrl:1
	v_lshl_add_u32 v106, v104, 7, v2
	v_lshl_add_u32 v107, v105, 7, v2
	v_add_f32_dpp v97, v97, v97 quad_perm:[2,3,0,1] row_mask:0xf bank_mask:0xf bound_ctrl:1
	global_load_dwordx4 v[48:51], v106, s[18:19]
	global_load_dwordx4 v[52:55], v107, s[18:19]
	v_add_f32_dpp v97, v97, v97 row_half_mirror row_mask:0xf bank_mask:0xf bound_ctrl:1
	v_cndmask_b32_e64 v103, v103, v97, s[44:45]
	ds_bpermute_b32 v104, v3, v21 offset:96
	ds_bpermute_b32 v105, v3, v25 offset:96
	s_waitcnt vmcnt(14)
	v_mov_b32_e32 v96, 0
	v_dot4c_i32_i8_e32 v96, v56, v60
	v_cvt_f32_i32_sdwa v98, sext(v56) dst_sel:DWORD dst_unused:UNUSED_PAD src0_sel:BYTE_0
	v_cvt_f32_i32_sdwa v99, sext(v57) dst_sel:DWORD dst_unused:UNUSED_PAD src0_sel:BYTE_0
	v_dot4c_i32_i8_e32 v96, v57, v61
	v_cvt_f32_i32_sdwa v100, sext(v58) dst_sel:DWORD dst_unused:UNUSED_PAD src0_sel:BYTE_0
	v_dot4c_i32_i8_e32 v96, v58, v62
	v_cvt_f32_i32_sdwa v101, sext(v59) dst_sel:DWORD dst_unused:UNUSED_PAD src0_sel:BYTE_0
	v_dot4c_i32_i8_e32 v96, v59, v63
	v_fma_f32 v97, v98, v4, 0
	v_cvt_f32_i32_sdwa v98, sext(v56) dst_sel:DWORD dst_unused:UNUSED_PAD src0_sel:BYTE_1
	v_fmac_f32_e32 v97, v99, v8
	v_cvt_f32_i32_sdwa v99, sext(v57) dst_sel:DWORD dst_unused:UNUSED_PAD src0_sel:BYTE_1
	v_fmac_f32_e32 v97, v100, v12
	v_cvt_f32_i32_sdwa v100, sext(v58) dst_sel:DWORD dst_unused:UNUSED_PAD src0_sel:BYTE_1
	v_fmac_f32_e32 v97, v101, v16
	v_cvt_f32_i32_sdwa v101, sext(v59) dst_sel:DWORD dst_unused:UNUSED_PAD src0_sel:BYTE_1
	v_add_u32_dpp v96, v96, v96 quad_perm:[1,0,3,2] row_mask:0xf bank_mask:0xf bound_ctrl:1
	v_fmac_f32_e32 v97, v98, v5
	v_cvt_f32_i32_sdwa v98, sext(v56) dst_sel:DWORD dst_unused:UNUSED_PAD src0_sel:BYTE_2
	v_fmac_f32_e32 v97, v99, v9
	v_cvt_f32_i32_sdwa v99, sext(v57) dst_sel:DWORD dst_unused:UNUSED_PAD src0_sel:BYTE_2
	v_fmac_f32_e32 v97, v100, v13
	v_cvt_f32_i32_sdwa v100, sext(v58) dst_sel:DWORD dst_unused:UNUSED_PAD src0_sel:BYTE_2
	v_add_u32_dpp v96, v96, v96 quad_perm:[2,3,0,1] row_mask:0xf bank_mask:0xf bound_ctrl:1
	v_fmac_f32_e32 v97, v101, v17
	v_cvt_f32_i32_sdwa v101, sext(v59) dst_sel:DWORD dst_unused:UNUSED_PAD src0_sel:BYTE_2
	v_fmac_f32_e32 v97, v98, v6
	v_cvt_f32_i32_sdwa v98, sext(v56) dst_sel:DWORD dst_unused:UNUSED_PAD src0_sel:BYTE_3
	v_fmac_f32_e32 v97, v99, v10
	v_cvt_f32_i32_sdwa v99, sext(v57) dst_sel:DWORD dst_unused:UNUSED_PAD src0_sel:BYTE_3
	v_add_u32_dpp v96, v96, v96 row_half_mirror row_mask:0xf bank_mask:0xf bound_ctrl:1
	v_fmac_f32_e32 v97, v100, v14
	v_cvt_f32_i32_sdwa v100, sext(v58) dst_sel:DWORD dst_unused:UNUSED_PAD src0_sel:BYTE_3
	v_fmac_f32_e32 v97, v101, v18
	v_cvt_f32_i32_sdwa v101, sext(v59) dst_sel:DWORD dst_unused:UNUSED_PAD src0_sel:BYTE_3
	v_fmac_f32_e32 v97, v98, v7
	v_fmac_f32_e32 v97, v99, v11
	v_fmac_f32_e32 v97, v100, v15
	v_fmac_f32_e32 v97, v101, v19
	v_cndmask_b32_e64 v102, v102, v96, s[46:47]
	s_waitcnt lgkmcnt(0)
	v_add_f32_dpp v97, v97, v97 quad_perm:[1,0,3,2] row_mask:0xf bank_mask:0xf bound_ctrl:1
	v_lshl_add_u32 v106, v104, 7, v2
	v_lshl_add_u32 v107, v105, 7, v2
	v_add_f32_dpp v97, v97, v97 quad_perm:[2,3,0,1] row_mask:0xf bank_mask:0xf bound_ctrl:1
	global_load_dwordx4 v[56:59], v106, s[18:19]
	global_load_dwordx4 v[60:63], v107, s[18:19]
	v_add_f32_dpp v97, v97, v97 row_half_mirror row_mask:0xf bank_mask:0xf bound_ctrl:1
	v_cndmask_b32_e64 v103, v103, v97, s[46:47]
	ds_bpermute_b32 v104, v3, v21 offset:128
	ds_bpermute_b32 v105, v3, v25 offset:128
	s_waitcnt vmcnt(14)
	v_mov_b32_e32 v96, 0
	v_dot4c_i32_i8_e32 v96, v64, v68
	v_cvt_f32_i32_sdwa v98, sext(v64) dst_sel:DWORD dst_unused:UNUSED_PAD src0_sel:BYTE_0
	v_cvt_f32_i32_sdwa v99, sext(v65) dst_sel:DWORD dst_unused:UNUSED_PAD src0_sel:BYTE_0
	v_dot4c_i32_i8_e32 v96, v65, v69
	v_cvt_f32_i32_sdwa v100, sext(v66) dst_sel:DWORD dst_unused:UNUSED_PAD src0_sel:BYTE_0
	v_dot4c_i32_i8_e32 v96, v66, v70
	v_cvt_f32_i32_sdwa v101, sext(v67) dst_sel:DWORD dst_unused:UNUSED_PAD src0_sel:BYTE_0
	v_dot4c_i32_i8_e32 v96, v67, v71
	v_fma_f32 v97, v98, v4, 0
	v_cvt_f32_i32_sdwa v98, sext(v64) dst_sel:DWORD dst_unused:UNUSED_PAD src0_sel:BYTE_1
	v_fmac_f32_e32 v97, v99, v8
	v_cvt_f32_i32_sdwa v99, sext(v65) dst_sel:DWORD dst_unused:UNUSED_PAD src0_sel:BYTE_1
	v_fmac_f32_e32 v97, v100, v12
	v_cvt_f32_i32_sdwa v100, sext(v66) dst_sel:DWORD dst_unused:UNUSED_PAD src0_sel:BYTE_1
	v_fmac_f32_e32 v97, v101, v16
	v_cvt_f32_i32_sdwa v101, sext(v67) dst_sel:DWORD dst_unused:UNUSED_PAD src0_sel:BYTE_1
	v_add_u32_dpp v96, v96, v96 quad_perm:[1,0,3,2] row_mask:0xf bank_mask:0xf bound_ctrl:1
	v_fmac_f32_e32 v97, v98, v5
	v_cvt_f32_i32_sdwa v98, sext(v64) dst_sel:DWORD dst_unused:UNUSED_PAD src0_sel:BYTE_2
	v_fmac_f32_e32 v97, v99, v9
	v_cvt_f32_i32_sdwa v99, sext(v65) dst_sel:DWORD dst_unused:UNUSED_PAD src0_sel:BYTE_2
	v_fmac_f32_e32 v97, v100, v13
	v_cvt_f32_i32_sdwa v100, sext(v66) dst_sel:DWORD dst_unused:UNUSED_PAD src0_sel:BYTE_2
	v_add_u32_dpp v96, v96, v96 quad_perm:[2,3,0,1] row_mask:0xf bank_mask:0xf bound_ctrl:1
	v_fmac_f32_e32 v97, v101, v17
	v_cvt_f32_i32_sdwa v101, sext(v67) dst_sel:DWORD dst_unused:UNUSED_PAD src0_sel:BYTE_2
	v_fmac_f32_e32 v97, v98, v6
	v_cvt_f32_i32_sdwa v98, sext(v64) dst_sel:DWORD dst_unused:UNUSED_PAD src0_sel:BYTE_3
	v_fmac_f32_e32 v97, v99, v10
	v_cvt_f32_i32_sdwa v99, sext(v65) dst_sel:DWORD dst_unused:UNUSED_PAD src0_sel:BYTE_3
	v_add_u32_dpp v96, v96, v96 row_half_mirror row_mask:0xf bank_mask:0xf bound_ctrl:1
	v_fmac_f32_e32 v97, v100, v14
	v_cvt_f32_i32_sdwa v100, sext(v66) dst_sel:DWORD dst_unused:UNUSED_PAD src0_sel:BYTE_3
	v_fmac_f32_e32 v97, v101, v18
	v_cvt_f32_i32_sdwa v101, sext(v67) dst_sel:DWORD dst_unused:UNUSED_PAD src0_sel:BYTE_3
	v_fmac_f32_e32 v97, v98, v7
	v_fmac_f32_e32 v97, v99, v11
	v_fmac_f32_e32 v97, v100, v15
	v_fmac_f32_e32 v97, v101, v19
	v_cndmask_b32_e64 v102, v102, v96, s[48:49]
	s_waitcnt lgkmcnt(0)
	v_add_f32_dpp v97, v97, v97 quad_perm:[1,0,3,2] row_mask:0xf bank_mask:0xf bound_ctrl:1
	v_lshl_add_u32 v106, v104, 7, v2
	v_lshl_add_u32 v107, v105, 7, v2
	v_add_f32_dpp v97, v97, v97 quad_perm:[2,3,0,1] row_mask:0xf bank_mask:0xf bound_ctrl:1
	global_load_dwordx4 v[64:67], v106, s[18:19]
	global_load_dwordx4 v[68:71], v107, s[18:19]
	v_add_f32_dpp v97, v97, v97 row_half_mirror row_mask:0xf bank_mask:0xf bound_ctrl:1
	v_cndmask_b32_e64 v103, v103, v97, s[48:49]
	ds_bpermute_b32 v104, v3, v21 offset:160
	ds_bpermute_b32 v105, v3, v25 offset:160
	s_waitcnt vmcnt(14)
	v_mov_b32_e32 v96, 0
	v_dot4c_i32_i8_e32 v96, v72, v76
	v_cvt_f32_i32_sdwa v98, sext(v72) dst_sel:DWORD dst_unused:UNUSED_PAD src0_sel:BYTE_0
	v_cvt_f32_i32_sdwa v99, sext(v73) dst_sel:DWORD dst_unused:UNUSED_PAD src0_sel:BYTE_0
	v_dot4c_i32_i8_e32 v96, v73, v77
	v_cvt_f32_i32_sdwa v100, sext(v74) dst_sel:DWORD dst_unused:UNUSED_PAD src0_sel:BYTE_0
	v_dot4c_i32_i8_e32 v96, v74, v78
	v_cvt_f32_i32_sdwa v101, sext(v75) dst_sel:DWORD dst_unused:UNUSED_PAD src0_sel:BYTE_0
	v_dot4c_i32_i8_e32 v96, v75, v79
	v_fma_f32 v97, v98, v4, 0
	v_cvt_f32_i32_sdwa v98, sext(v72) dst_sel:DWORD dst_unused:UNUSED_PAD src0_sel:BYTE_1
	v_fmac_f32_e32 v97, v99, v8
	v_cvt_f32_i32_sdwa v99, sext(v73) dst_sel:DWORD dst_unused:UNUSED_PAD src0_sel:BYTE_1
	v_fmac_f32_e32 v97, v100, v12
	v_cvt_f32_i32_sdwa v100, sext(v74) dst_sel:DWORD dst_unused:UNUSED_PAD src0_sel:BYTE_1
	v_fmac_f32_e32 v97, v101, v16
	v_cvt_f32_i32_sdwa v101, sext(v75) dst_sel:DWORD dst_unused:UNUSED_PAD src0_sel:BYTE_1
	v_add_u32_dpp v96, v96, v96 quad_perm:[1,0,3,2] row_mask:0xf bank_mask:0xf bound_ctrl:1
	v_fmac_f32_e32 v97, v98, v5
	v_cvt_f32_i32_sdwa v98, sext(v72) dst_sel:DWORD dst_unused:UNUSED_PAD src0_sel:BYTE_2
	v_fmac_f32_e32 v97, v99, v9
	v_cvt_f32_i32_sdwa v99, sext(v73) dst_sel:DWORD dst_unused:UNUSED_PAD src0_sel:BYTE_2
	v_fmac_f32_e32 v97, v100, v13
	v_cvt_f32_i32_sdwa v100, sext(v74) dst_sel:DWORD dst_unused:UNUSED_PAD src0_sel:BYTE_2
	v_add_u32_dpp v96, v96, v96 quad_perm:[2,3,0,1] row_mask:0xf bank_mask:0xf bound_ctrl:1
	v_fmac_f32_e32 v97, v101, v17
	v_cvt_f32_i32_sdwa v101, sext(v75) dst_sel:DWORD dst_unused:UNUSED_PAD src0_sel:BYTE_2
	v_fmac_f32_e32 v97, v98, v6
	v_cvt_f32_i32_sdwa v98, sext(v72) dst_sel:DWORD dst_unused:UNUSED_PAD src0_sel:BYTE_3
	v_fmac_f32_e32 v97, v99, v10
	v_cvt_f32_i32_sdwa v99, sext(v73) dst_sel:DWORD dst_unused:UNUSED_PAD src0_sel:BYTE_3
	v_add_u32_dpp v96, v96, v96 row_half_mirror row_mask:0xf bank_mask:0xf bound_ctrl:1
	v_fmac_f32_e32 v97, v100, v14
	v_cvt_f32_i32_sdwa v100, sext(v74) dst_sel:DWORD dst_unused:UNUSED_PAD src0_sel:BYTE_3
	v_fmac_f32_e32 v97, v101, v18
	v_cvt_f32_i32_sdwa v101, sext(v75) dst_sel:DWORD dst_unused:UNUSED_PAD src0_sel:BYTE_3
	v_fmac_f32_e32 v97, v98, v7
	v_fmac_f32_e32 v97, v99, v11
	v_fmac_f32_e32 v97, v100, v15
	v_fmac_f32_e32 v97, v101, v19
	v_cndmask_b32_e64 v102, v102, v96, s[50:51]
	s_waitcnt lgkmcnt(0)
	v_add_f32_dpp v97, v97, v97 quad_perm:[1,0,3,2] row_mask:0xf bank_mask:0xf bound_ctrl:1
	v_lshl_add_u32 v106, v104, 7, v2
	v_lshl_add_u32 v107, v105, 7, v2
	v_add_f32_dpp v97, v97, v97 quad_perm:[2,3,0,1] row_mask:0xf bank_mask:0xf bound_ctrl:1
	global_load_dwordx4 v[72:75], v106, s[18:19]
	global_load_dwordx4 v[76:79], v107, s[18:19]
	v_add_f32_dpp v97, v97, v97 row_half_mirror row_mask:0xf bank_mask:0xf bound_ctrl:1
	v_cndmask_b32_e64 v103, v103, v97, s[50:51]
	ds_bpermute_b32 v104, v3, v21 offset:192
	ds_bpermute_b32 v105, v3, v25 offset:192
	s_waitcnt vmcnt(14)
	v_mov_b32_e32 v96, 0
	v_dot4c_i32_i8_e32 v96, v80, v84
	v_cvt_f32_i32_sdwa v98, sext(v80) dst_sel:DWORD dst_unused:UNUSED_PAD src0_sel:BYTE_0
	v_cvt_f32_i32_sdwa v99, sext(v81) dst_sel:DWORD dst_unused:UNUSED_PAD src0_sel:BYTE_0
	v_dot4c_i32_i8_e32 v96, v81, v85
	v_cvt_f32_i32_sdwa v100, sext(v82) dst_sel:DWORD dst_unused:UNUSED_PAD src0_sel:BYTE_0
	v_dot4c_i32_i8_e32 v96, v82, v86
	v_cvt_f32_i32_sdwa v101, sext(v83) dst_sel:DWORD dst_unused:UNUSED_PAD src0_sel:BYTE_0
	v_dot4c_i32_i8_e32 v96, v83, v87
	v_fma_f32 v97, v98, v4, 0
	v_cvt_f32_i32_sdwa v98, sext(v80) dst_sel:DWORD dst_unused:UNUSED_PAD src0_sel:BYTE_1
	v_fmac_f32_e32 v97, v99, v8
	v_cvt_f32_i32_sdwa v99, sext(v81) dst_sel:DWORD dst_unused:UNUSED_PAD src0_sel:BYTE_1
	v_fmac_f32_e32 v97, v100, v12
	v_cvt_f32_i32_sdwa v100, sext(v82) dst_sel:DWORD dst_unused:UNUSED_PAD src0_sel:BYTE_1
	v_fmac_f32_e32 v97, v101, v16
	v_cvt_f32_i32_sdwa v101, sext(v83) dst_sel:DWORD dst_unused:UNUSED_PAD src0_sel:BYTE_1
	v_add_u32_dpp v96, v96, v96 quad_perm:[1,0,3,2] row_mask:0xf bank_mask:0xf bound_ctrl:1
	v_fmac_f32_e32 v97, v98, v5
	v_cvt_f32_i32_sdwa v98, sext(v80) dst_sel:DWORD dst_unused:UNUSED_PAD src0_sel:BYTE_2
	v_fmac_f32_e32 v97, v99, v9
	v_cvt_f32_i32_sdwa v99, sext(v81) dst_sel:DWORD dst_unused:UNUSED_PAD src0_sel:BYTE_2
	v_fmac_f32_e32 v97, v100, v13
	v_cvt_f32_i32_sdwa v100, sext(v82) dst_sel:DWORD dst_unused:UNUSED_PAD src0_sel:BYTE_2
	v_add_u32_dpp v96, v96, v96 quad_perm:[2,3,0,1] row_mask:0xf bank_mask:0xf bound_ctrl:1
	v_fmac_f32_e32 v97, v101, v17
	v_cvt_f32_i32_sdwa v101, sext(v83) dst_sel:DWORD dst_unused:UNUSED_PAD src0_sel:BYTE_2
	v_fmac_f32_e32 v97, v98, v6
	v_cvt_f32_i32_sdwa v98, sext(v80) dst_sel:DWORD dst_unused:UNUSED_PAD src0_sel:BYTE_3
	v_fmac_f32_e32 v97, v99, v10
	v_cvt_f32_i32_sdwa v99, sext(v81) dst_sel:DWORD dst_unused:UNUSED_PAD src0_sel:BYTE_3
	v_add_u32_dpp v96, v96, v96 row_half_mirror row_mask:0xf bank_mask:0xf bound_ctrl:1
	v_fmac_f32_e32 v97, v100, v14
	v_cvt_f32_i32_sdwa v100, sext(v82) dst_sel:DWORD dst_unused:UNUSED_PAD src0_sel:BYTE_3
	v_fmac_f32_e32 v97, v101, v18
	v_cvt_f32_i32_sdwa v101, sext(v83) dst_sel:DWORD dst_unused:UNUSED_PAD src0_sel:BYTE_3
	v_fmac_f32_e32 v97, v98, v7
	v_fmac_f32_e32 v97, v99, v11
	v_fmac_f32_e32 v97, v100, v15
	v_fmac_f32_e32 v97, v101, v19
	v_cndmask_b32_e64 v102, v102, v96, s[52:53]
	s_waitcnt lgkmcnt(0)
	v_add_f32_dpp v97, v97, v97 quad_perm:[1,0,3,2] row_mask:0xf bank_mask:0xf bound_ctrl:1
	v_lshl_add_u32 v106, v104, 7, v2
	v_lshl_add_u32 v107, v105, 7, v2
	v_add_f32_dpp v97, v97, v97 quad_perm:[2,3,0,1] row_mask:0xf bank_mask:0xf bound_ctrl:1
	global_load_dwordx4 v[80:83], v106, s[18:19]
	global_load_dwordx4 v[84:87], v107, s[18:19]
	v_add_f32_dpp v97, v97, v97 row_half_mirror row_mask:0xf bank_mask:0xf bound_ctrl:1
	v_cndmask_b32_e64 v103, v103, v97, s[52:53]
	ds_bpermute_b32 v104, v3, v21 offset:224
	ds_bpermute_b32 v105, v3, v25 offset:224
	s_waitcnt vmcnt(14)
	v_mov_b32_e32 v96, 0
	v_dot4c_i32_i8_e32 v96, v88, v92
	v_cvt_f32_i32_sdwa v98, sext(v88) dst_sel:DWORD dst_unused:UNUSED_PAD src0_sel:BYTE_0
	v_cvt_f32_i32_sdwa v99, sext(v89) dst_sel:DWORD dst_unused:UNUSED_PAD src0_sel:BYTE_0
	v_dot4c_i32_i8_e32 v96, v89, v93
	v_cvt_f32_i32_sdwa v100, sext(v90) dst_sel:DWORD dst_unused:UNUSED_PAD src0_sel:BYTE_0
	v_dot4c_i32_i8_e32 v96, v90, v94
	v_cvt_f32_i32_sdwa v101, sext(v91) dst_sel:DWORD dst_unused:UNUSED_PAD src0_sel:BYTE_0
	v_dot4c_i32_i8_e32 v96, v91, v95
	v_fma_f32 v97, v98, v4, 0
	v_cvt_f32_i32_sdwa v98, sext(v88) dst_sel:DWORD dst_unused:UNUSED_PAD src0_sel:BYTE_1
	v_fmac_f32_e32 v97, v99, v8
	v_cvt_f32_i32_sdwa v99, sext(v89) dst_sel:DWORD dst_unused:UNUSED_PAD src0_sel:BYTE_1
	v_fmac_f32_e32 v97, v100, v12
	v_cvt_f32_i32_sdwa v100, sext(v90) dst_sel:DWORD dst_unused:UNUSED_PAD src0_sel:BYTE_1
	v_fmac_f32_e32 v97, v101, v16
	v_cvt_f32_i32_sdwa v101, sext(v91) dst_sel:DWORD dst_unused:UNUSED_PAD src0_sel:BYTE_1
	v_add_u32_dpp v96, v96, v96 quad_perm:[1,0,3,2] row_mask:0xf bank_mask:0xf bound_ctrl:1
	v_fmac_f32_e32 v97, v98, v5
	v_cvt_f32_i32_sdwa v98, sext(v88) dst_sel:DWORD dst_unused:UNUSED_PAD src0_sel:BYTE_2
	v_fmac_f32_e32 v97, v99, v9
	v_cvt_f32_i32_sdwa v99, sext(v89) dst_sel:DWORD dst_unused:UNUSED_PAD src0_sel:BYTE_2
	v_fmac_f32_e32 v97, v100, v13
	v_cvt_f32_i32_sdwa v100, sext(v90) dst_sel:DWORD dst_unused:UNUSED_PAD src0_sel:BYTE_2
	v_add_u32_dpp v96, v96, v96 quad_perm:[2,3,0,1] row_mask:0xf bank_mask:0xf bound_ctrl:1
	v_fmac_f32_e32 v97, v101, v17
	v_cvt_f32_i32_sdwa v101, sext(v91) dst_sel:DWORD dst_unused:UNUSED_PAD src0_sel:BYTE_2
	v_fmac_f32_e32 v97, v98, v6
	v_cvt_f32_i32_sdwa v98, sext(v88) dst_sel:DWORD dst_unused:UNUSED_PAD src0_sel:BYTE_3
	v_fmac_f32_e32 v97, v99, v10
	v_cvt_f32_i32_sdwa v99, sext(v89) dst_sel:DWORD dst_unused:UNUSED_PAD src0_sel:BYTE_3
	v_add_u32_dpp v96, v96, v96 row_half_mirror row_mask:0xf bank_mask:0xf bound_ctrl:1
	v_fmac_f32_e32 v97, v100, v14
	v_cvt_f32_i32_sdwa v100, sext(v90) dst_sel:DWORD dst_unused:UNUSED_PAD src0_sel:BYTE_3
	v_fmac_f32_e32 v97, v101, v18
	v_cvt_f32_i32_sdwa v101, sext(v91) dst_sel:DWORD dst_unused:UNUSED_PAD src0_sel:BYTE_3
	v_fmac_f32_e32 v97, v98, v7
	v_fmac_f32_e32 v97, v99, v11
	v_fmac_f32_e32 v97, v100, v15
	v_fmac_f32_e32 v97, v101, v19
	v_cndmask_b32_e64 v102, v102, v96, s[54:55]
	s_waitcnt lgkmcnt(0)
	v_add_f32_dpp v97, v97, v97 quad_perm:[1,0,3,2] row_mask:0xf bank_mask:0xf bound_ctrl:1
	v_lshl_add_u32 v106, v104, 7, v2
	v_lshl_add_u32 v107, v105, 7, v2
	v_add_f32_dpp v97, v97, v97 quad_perm:[2,3,0,1] row_mask:0xf bank_mask:0xf bound_ctrl:1
	global_load_dwordx4 v[88:91], v106, s[18:19]
	global_load_dwordx4 v[92:95], v107, s[18:19]
	v_add_f32_dpp v97, v97, v97 row_half_mirror row_mask:0xf bank_mask:0xf bound_ctrl:1
	v_cndmask_b32_e64 v103, v103, v97, s[54:55]
	global_atomic_add v28, v102, s[20:21]
	global_atomic_add_f32 v28, v103, s[22:23]
	ds_bpermute_b32 v104, v3, v22
	ds_bpermute_b32 v105, v3, v26
	s_waitcnt vmcnt(16)
	v_mov_b32_e32 v96, 0
	v_dot4c_i32_i8_e32 v96, v32, v36
	v_cvt_f32_i32_sdwa v98, sext(v32) dst_sel:DWORD dst_unused:UNUSED_PAD src0_sel:BYTE_0
	v_cvt_f32_i32_sdwa v99, sext(v33) dst_sel:DWORD dst_unused:UNUSED_PAD src0_sel:BYTE_0
	v_dot4c_i32_i8_e32 v96, v33, v37
	v_cvt_f32_i32_sdwa v100, sext(v34) dst_sel:DWORD dst_unused:UNUSED_PAD src0_sel:BYTE_0
	v_dot4c_i32_i8_e32 v96, v34, v38
	v_cvt_f32_i32_sdwa v101, sext(v35) dst_sel:DWORD dst_unused:UNUSED_PAD src0_sel:BYTE_0
	v_dot4c_i32_i8_e32 v96, v35, v39
	v_fma_f32 v97, v98, v4, 0
	v_cvt_f32_i32_sdwa v98, sext(v32) dst_sel:DWORD dst_unused:UNUSED_PAD src0_sel:BYTE_1
	v_fmac_f32_e32 v97, v99, v8
	v_cvt_f32_i32_sdwa v99, sext(v33) dst_sel:DWORD dst_unused:UNUSED_PAD src0_sel:BYTE_1
	v_fmac_f32_e32 v97, v100, v12
	v_cvt_f32_i32_sdwa v100, sext(v34) dst_sel:DWORD dst_unused:UNUSED_PAD src0_sel:BYTE_1
	v_fmac_f32_e32 v97, v101, v16
	v_cvt_f32_i32_sdwa v101, sext(v35) dst_sel:DWORD dst_unused:UNUSED_PAD src0_sel:BYTE_1
	v_add_u32_dpp v96, v96, v96 quad_perm:[1,0,3,2] row_mask:0xf bank_mask:0xf bound_ctrl:1
	v_fmac_f32_e32 v97, v98, v5
	v_cvt_f32_i32_sdwa v98, sext(v32) dst_sel:DWORD dst_unused:UNUSED_PAD src0_sel:BYTE_2
	v_fmac_f32_e32 v97, v99, v9
	v_cvt_f32_i32_sdwa v99, sext(v33) dst_sel:DWORD dst_unused:UNUSED_PAD src0_sel:BYTE_2
	v_fmac_f32_e32 v97, v100, v13
	v_cvt_f32_i32_sdwa v100, sext(v34) dst_sel:DWORD dst_unused:UNUSED_PAD src0_sel:BYTE_2
	v_add_u32_dpp v96, v96, v96 quad_perm:[2,3,0,1] row_mask:0xf bank_mask:0xf bound_ctrl:1
	v_fmac_f32_e32 v97, v101, v17
	v_cvt_f32_i32_sdwa v101, sext(v35) dst_sel:DWORD dst_unused:UNUSED_PAD src0_sel:BYTE_2
	v_fmac_f32_e32 v97, v98, v6
	v_cvt_f32_i32_sdwa v98, sext(v32) dst_sel:DWORD dst_unused:UNUSED_PAD src0_sel:BYTE_3
	v_fmac_f32_e32 v97, v99, v10
	v_cvt_f32_i32_sdwa v99, sext(v33) dst_sel:DWORD dst_unused:UNUSED_PAD src0_sel:BYTE_3
	v_add_u32_dpp v96, v96, v96 row_half_mirror row_mask:0xf bank_mask:0xf bound_ctrl:1
	v_fmac_f32_e32 v97, v100, v14
	v_cvt_f32_i32_sdwa v100, sext(v34) dst_sel:DWORD dst_unused:UNUSED_PAD src0_sel:BYTE_3
	v_fmac_f32_e32 v97, v101, v18
	v_cvt_f32_i32_sdwa v101, sext(v35) dst_sel:DWORD dst_unused:UNUSED_PAD src0_sel:BYTE_3
	v_fmac_f32_e32 v97, v98, v7
	v_fmac_f32_e32 v97, v99, v11
	v_fmac_f32_e32 v97, v100, v15
	v_fmac_f32_e32 v97, v101, v19
	v_cndmask_b32_e64 v102, 0, v96, s[40:41]
	s_waitcnt lgkmcnt(0)
	v_add_f32_dpp v97, v97, v97 quad_perm:[1,0,3,2] row_mask:0xf bank_mask:0xf bound_ctrl:1
	v_lshl_add_u32 v106, v104, 7, v2
	v_lshl_add_u32 v107, v105, 7, v2
	v_add_f32_dpp v97, v97, v97 quad_perm:[2,3,0,1] row_mask:0xf bank_mask:0xf bound_ctrl:1
	global_load_dwordx4 v[32:35], v106, s[18:19]
	global_load_dwordx4 v[36:39], v107, s[18:19]
	v_add_f32_dpp v97, v97, v97 row_half_mirror row_mask:0xf bank_mask:0xf bound_ctrl:1
	v_cndmask_b32_e64 v103, 0, v97, s[40:41]
	ds_bpermute_b32 v104, v3, v22 offset:32
	ds_bpermute_b32 v105, v3, v26 offset:32
	s_waitcnt vmcnt(16)
	v_mov_b32_e32 v96, 0
	v_dot4c_i32_i8_e32 v96, v40, v44
	v_cvt_f32_i32_sdwa v98, sext(v40) dst_sel:DWORD dst_unused:UNUSED_PAD src0_sel:BYTE_0
	v_cvt_f32_i32_sdwa v99, sext(v41) dst_sel:DWORD dst_unused:UNUSED_PAD src0_sel:BYTE_0
	v_dot4c_i32_i8_e32 v96, v41, v45
	v_cvt_f32_i32_sdwa v100, sext(v42) dst_sel:DWORD dst_unused:UNUSED_PAD src0_sel:BYTE_0
	v_dot4c_i32_i8_e32 v96, v42, v46
	v_cvt_f32_i32_sdwa v101, sext(v43) dst_sel:DWORD dst_unused:UNUSED_PAD src0_sel:BYTE_0
	v_dot4c_i32_i8_e32 v96, v43, v47
	v_fma_f32 v97, v98, v4, 0
	v_cvt_f32_i32_sdwa v98, sext(v40) dst_sel:DWORD dst_unused:UNUSED_PAD src0_sel:BYTE_1
	v_fmac_f32_e32 v97, v99, v8
	v_cvt_f32_i32_sdwa v99, sext(v41) dst_sel:DWORD dst_unused:UNUSED_PAD src0_sel:BYTE_1
	v_fmac_f32_e32 v97, v100, v12
	v_cvt_f32_i32_sdwa v100, sext(v42) dst_sel:DWORD dst_unused:UNUSED_PAD src0_sel:BYTE_1
	v_fmac_f32_e32 v97, v101, v16
	v_cvt_f32_i32_sdwa v101, sext(v43) dst_sel:DWORD dst_unused:UNUSED_PAD src0_sel:BYTE_1
	v_add_u32_dpp v96, v96, v96 quad_perm:[1,0,3,2] row_mask:0xf bank_mask:0xf bound_ctrl:1
	v_fmac_f32_e32 v97, v98, v5
	v_cvt_f32_i32_sdwa v98, sext(v40) dst_sel:DWORD dst_unused:UNUSED_PAD src0_sel:BYTE_2
	v_fmac_f32_e32 v97, v99, v9
	v_cvt_f32_i32_sdwa v99, sext(v41) dst_sel:DWORD dst_unused:UNUSED_PAD src0_sel:BYTE_2
	v_fmac_f32_e32 v97, v100, v13
	v_cvt_f32_i32_sdwa v100, sext(v42) dst_sel:DWORD dst_unused:UNUSED_PAD src0_sel:BYTE_2
	v_add_u32_dpp v96, v96, v96 quad_perm:[2,3,0,1] row_mask:0xf bank_mask:0xf bound_ctrl:1
	v_fmac_f32_e32 v97, v101, v17
	v_cvt_f32_i32_sdwa v101, sext(v43) dst_sel:DWORD dst_unused:UNUSED_PAD src0_sel:BYTE_2
	v_fmac_f32_e32 v97, v98, v6
	v_cvt_f32_i32_sdwa v98, sext(v40) dst_sel:DWORD dst_unused:UNUSED_PAD src0_sel:BYTE_3
	v_fmac_f32_e32 v97, v99, v10
	v_cvt_f32_i32_sdwa v99, sext(v41) dst_sel:DWORD dst_unused:UNUSED_PAD src0_sel:BYTE_3
	v_add_u32_dpp v96, v96, v96 row_half_mirror row_mask:0xf bank_mask:0xf bound_ctrl:1
	v_fmac_f32_e32 v97, v100, v14
	v_cvt_f32_i32_sdwa v100, sext(v42) dst_sel:DWORD dst_unused:UNUSED_PAD src0_sel:BYTE_3
	v_fmac_f32_e32 v97, v101, v18
	v_cvt_f32_i32_sdwa v101, sext(v43) dst_sel:DWORD dst_unused:UNUSED_PAD src0_sel:BYTE_3
	v_fmac_f32_e32 v97, v98, v7
	v_fmac_f32_e32 v97, v99, v11
	v_fmac_f32_e32 v97, v100, v15
	v_fmac_f32_e32 v97, v101, v19
	v_cndmask_b32_e64 v102, v102, v96, s[42:43]
	s_waitcnt lgkmcnt(0)
	v_add_f32_dpp v97, v97, v97 quad_perm:[1,0,3,2] row_mask:0xf bank_mask:0xf bound_ctrl:1
	v_lshl_add_u32 v106, v104, 7, v2
	v_lshl_add_u32 v107, v105, 7, v2
	v_add_f32_dpp v97, v97, v97 quad_perm:[2,3,0,1] row_mask:0xf bank_mask:0xf bound_ctrl:1
	global_load_dwordx4 v[40:43], v106, s[18:19]
	global_load_dwordx4 v[44:47], v107, s[18:19]
	v_add_f32_dpp v97, v97, v97 row_half_mirror row_mask:0xf bank_mask:0xf bound_ctrl:1
	v_cndmask_b32_e64 v103, v103, v97, s[42:43]
	ds_bpermute_b32 v104, v3, v22 offset:64
	ds_bpermute_b32 v105, v3, v26 offset:64
	s_waitcnt vmcnt(16)
	v_mov_b32_e32 v96, 0
	v_dot4c_i32_i8_e32 v96, v48, v52
	v_cvt_f32_i32_sdwa v98, sext(v48) dst_sel:DWORD dst_unused:UNUSED_PAD src0_sel:BYTE_0
	v_cvt_f32_i32_sdwa v99, sext(v49) dst_sel:DWORD dst_unused:UNUSED_PAD src0_sel:BYTE_0
	v_dot4c_i32_i8_e32 v96, v49, v53
	v_cvt_f32_i32_sdwa v100, sext(v50) dst_sel:DWORD dst_unused:UNUSED_PAD src0_sel:BYTE_0
	v_dot4c_i32_i8_e32 v96, v50, v54
	v_cvt_f32_i32_sdwa v101, sext(v51) dst_sel:DWORD dst_unused:UNUSED_PAD src0_sel:BYTE_0
	v_dot4c_i32_i8_e32 v96, v51, v55
	v_fma_f32 v97, v98, v4, 0
	v_cvt_f32_i32_sdwa v98, sext(v48) dst_sel:DWORD dst_unused:UNUSED_PAD src0_sel:BYTE_1
	v_fmac_f32_e32 v97, v99, v8
	v_cvt_f32_i32_sdwa v99, sext(v49) dst_sel:DWORD dst_unused:UNUSED_PAD src0_sel:BYTE_1
	v_fmac_f32_e32 v97, v100, v12
	v_cvt_f32_i32_sdwa v100, sext(v50) dst_sel:DWORD dst_unused:UNUSED_PAD src0_sel:BYTE_1
	v_fmac_f32_e32 v97, v101, v16
	v_cvt_f32_i32_sdwa v101, sext(v51) dst_sel:DWORD dst_unused:UNUSED_PAD src0_sel:BYTE_1
	v_add_u32_dpp v96, v96, v96 quad_perm:[1,0,3,2] row_mask:0xf bank_mask:0xf bound_ctrl:1
	v_fmac_f32_e32 v97, v98, v5
	v_cvt_f32_i32_sdwa v98, sext(v48) dst_sel:DWORD dst_unused:UNUSED_PAD src0_sel:BYTE_2
	v_fmac_f32_e32 v97, v99, v9
	v_cvt_f32_i32_sdwa v99, sext(v49) dst_sel:DWORD dst_unused:UNUSED_PAD src0_sel:BYTE_2
	v_fmac_f32_e32 v97, v100, v13
	v_cvt_f32_i32_sdwa v100, sext(v50) dst_sel:DWORD dst_unused:UNUSED_PAD src0_sel:BYTE_2
	v_add_u32_dpp v96, v96, v96 quad_perm:[2,3,0,1] row_mask:0xf bank_mask:0xf bound_ctrl:1
	v_fmac_f32_e32 v97, v101, v17
	v_cvt_f32_i32_sdwa v101, sext(v51) dst_sel:DWORD dst_unused:UNUSED_PAD src0_sel:BYTE_2
	v_fmac_f32_e32 v97, v98, v6
	v_cvt_f32_i32_sdwa v98, sext(v48) dst_sel:DWORD dst_unused:UNUSED_PAD src0_sel:BYTE_3
	v_fmac_f32_e32 v97, v99, v10
	v_cvt_f32_i32_sdwa v99, sext(v49) dst_sel:DWORD dst_unused:UNUSED_PAD src0_sel:BYTE_3
	v_add_u32_dpp v96, v96, v96 row_half_mirror row_mask:0xf bank_mask:0xf bound_ctrl:1
	v_fmac_f32_e32 v97, v100, v14
	v_cvt_f32_i32_sdwa v100, sext(v50) dst_sel:DWORD dst_unused:UNUSED_PAD src0_sel:BYTE_3
	v_fmac_f32_e32 v97, v101, v18
	v_cvt_f32_i32_sdwa v101, sext(v51) dst_sel:DWORD dst_unused:UNUSED_PAD src0_sel:BYTE_3
	v_fmac_f32_e32 v97, v98, v7
	v_fmac_f32_e32 v97, v99, v11
	v_fmac_f32_e32 v97, v100, v15
	v_fmac_f32_e32 v97, v101, v19
	v_cndmask_b32_e64 v102, v102, v96, s[44:45]
	s_waitcnt lgkmcnt(0)
	v_add_f32_dpp v97, v97, v97 quad_perm:[1,0,3,2] row_mask:0xf bank_mask:0xf bound_ctrl:1
	v_lshl_add_u32 v106, v104, 7, v2
	v_lshl_add_u32 v107, v105, 7, v2
	v_add_f32_dpp v97, v97, v97 quad_perm:[2,3,0,1] row_mask:0xf bank_mask:0xf bound_ctrl:1
	global_load_dwordx4 v[48:51], v106, s[18:19]
	global_load_dwordx4 v[52:55], v107, s[18:19]
	v_add_f32_dpp v97, v97, v97 row_half_mirror row_mask:0xf bank_mask:0xf bound_ctrl:1
	v_cndmask_b32_e64 v103, v103, v97, s[44:45]
	ds_bpermute_b32 v104, v3, v22 offset:96
	ds_bpermute_b32 v105, v3, v26 offset:96
	s_waitcnt vmcnt(16)
	v_mov_b32_e32 v96, 0
	v_dot4c_i32_i8_e32 v96, v56, v60
	v_cvt_f32_i32_sdwa v98, sext(v56) dst_sel:DWORD dst_unused:UNUSED_PAD src0_sel:BYTE_0
	v_cvt_f32_i32_sdwa v99, sext(v57) dst_sel:DWORD dst_unused:UNUSED_PAD src0_sel:BYTE_0
	v_dot4c_i32_i8_e32 v96, v57, v61
	v_cvt_f32_i32_sdwa v100, sext(v58) dst_sel:DWORD dst_unused:UNUSED_PAD src0_sel:BYTE_0
	v_dot4c_i32_i8_e32 v96, v58, v62
	v_cvt_f32_i32_sdwa v101, sext(v59) dst_sel:DWORD dst_unused:UNUSED_PAD src0_sel:BYTE_0
	v_dot4c_i32_i8_e32 v96, v59, v63
	v_fma_f32 v97, v98, v4, 0
	v_cvt_f32_i32_sdwa v98, sext(v56) dst_sel:DWORD dst_unused:UNUSED_PAD src0_sel:BYTE_1
	v_fmac_f32_e32 v97, v99, v8
	v_cvt_f32_i32_sdwa v99, sext(v57) dst_sel:DWORD dst_unused:UNUSED_PAD src0_sel:BYTE_1
	v_fmac_f32_e32 v97, v100, v12
	v_cvt_f32_i32_sdwa v100, sext(v58) dst_sel:DWORD dst_unused:UNUSED_PAD src0_sel:BYTE_1
	v_fmac_f32_e32 v97, v101, v16
	v_cvt_f32_i32_sdwa v101, sext(v59) dst_sel:DWORD dst_unused:UNUSED_PAD src0_sel:BYTE_1
	v_add_u32_dpp v96, v96, v96 quad_perm:[1,0,3,2] row_mask:0xf bank_mask:0xf bound_ctrl:1
	v_fmac_f32_e32 v97, v98, v5
	v_cvt_f32_i32_sdwa v98, sext(v56) dst_sel:DWORD dst_unused:UNUSED_PAD src0_sel:BYTE_2
	v_fmac_f32_e32 v97, v99, v9
	v_cvt_f32_i32_sdwa v99, sext(v57) dst_sel:DWORD dst_unused:UNUSED_PAD src0_sel:BYTE_2
	v_fmac_f32_e32 v97, v100, v13
	v_cvt_f32_i32_sdwa v100, sext(v58) dst_sel:DWORD dst_unused:UNUSED_PAD src0_sel:BYTE_2
	v_add_u32_dpp v96, v96, v96 quad_perm:[2,3,0,1] row_mask:0xf bank_mask:0xf bound_ctrl:1
	v_fmac_f32_e32 v97, v101, v17
	v_cvt_f32_i32_sdwa v101, sext(v59) dst_sel:DWORD dst_unused:UNUSED_PAD src0_sel:BYTE_2
	v_fmac_f32_e32 v97, v98, v6
	v_cvt_f32_i32_sdwa v98, sext(v56) dst_sel:DWORD dst_unused:UNUSED_PAD src0_sel:BYTE_3
	v_fmac_f32_e32 v97, v99, v10
	v_cvt_f32_i32_sdwa v99, sext(v57) dst_sel:DWORD dst_unused:UNUSED_PAD src0_sel:BYTE_3
	v_add_u32_dpp v96, v96, v96 row_half_mirror row_mask:0xf bank_mask:0xf bound_ctrl:1
	v_fmac_f32_e32 v97, v100, v14
	v_cvt_f32_i32_sdwa v100, sext(v58) dst_sel:DWORD dst_unused:UNUSED_PAD src0_sel:BYTE_3
	v_fmac_f32_e32 v97, v101, v18
	v_cvt_f32_i32_sdwa v101, sext(v59) dst_sel:DWORD dst_unused:UNUSED_PAD src0_sel:BYTE_3
	v_fmac_f32_e32 v97, v98, v7
	v_fmac_f32_e32 v97, v99, v11
	v_fmac_f32_e32 v97, v100, v15
	v_fmac_f32_e32 v97, v101, v19
	v_cndmask_b32_e64 v102, v102, v96, s[46:47]
	s_waitcnt lgkmcnt(0)
	v_add_f32_dpp v97, v97, v97 quad_perm:[1,0,3,2] row_mask:0xf bank_mask:0xf bound_ctrl:1
	v_lshl_add_u32 v106, v104, 7, v2
	v_lshl_add_u32 v107, v105, 7, v2
	v_add_f32_dpp v97, v97, v97 quad_perm:[2,3,0,1] row_mask:0xf bank_mask:0xf bound_ctrl:1
	global_load_dwordx4 v[56:59], v106, s[18:19]
	global_load_dwordx4 v[60:63], v107, s[18:19]
	v_add_f32_dpp v97, v97, v97 row_half_mirror row_mask:0xf bank_mask:0xf bound_ctrl:1
	v_cndmask_b32_e64 v103, v103, v97, s[46:47]
	ds_bpermute_b32 v104, v3, v22 offset:128
	ds_bpermute_b32 v105, v3, v26 offset:128
	s_waitcnt vmcnt(16)
	v_mov_b32_e32 v96, 0
	v_dot4c_i32_i8_e32 v96, v64, v68
	v_cvt_f32_i32_sdwa v98, sext(v64) dst_sel:DWORD dst_unused:UNUSED_PAD src0_sel:BYTE_0
	v_cvt_f32_i32_sdwa v99, sext(v65) dst_sel:DWORD dst_unused:UNUSED_PAD src0_sel:BYTE_0
	v_dot4c_i32_i8_e32 v96, v65, v69
	v_cvt_f32_i32_sdwa v100, sext(v66) dst_sel:DWORD dst_unused:UNUSED_PAD src0_sel:BYTE_0
	v_dot4c_i32_i8_e32 v96, v66, v70
	v_cvt_f32_i32_sdwa v101, sext(v67) dst_sel:DWORD dst_unused:UNUSED_PAD src0_sel:BYTE_0
	v_dot4c_i32_i8_e32 v96, v67, v71
	v_fma_f32 v97, v98, v4, 0
	v_cvt_f32_i32_sdwa v98, sext(v64) dst_sel:DWORD dst_unused:UNUSED_PAD src0_sel:BYTE_1
	v_fmac_f32_e32 v97, v99, v8
	v_cvt_f32_i32_sdwa v99, sext(v65) dst_sel:DWORD dst_unused:UNUSED_PAD src0_sel:BYTE_1
	v_fmac_f32_e32 v97, v100, v12
	v_cvt_f32_i32_sdwa v100, sext(v66) dst_sel:DWORD dst_unused:UNUSED_PAD src0_sel:BYTE_1
	v_fmac_f32_e32 v97, v101, v16
	v_cvt_f32_i32_sdwa v101, sext(v67) dst_sel:DWORD dst_unused:UNUSED_PAD src0_sel:BYTE_1
	v_add_u32_dpp v96, v96, v96 quad_perm:[1,0,3,2] row_mask:0xf bank_mask:0xf bound_ctrl:1
	v_fmac_f32_e32 v97, v98, v5
	v_cvt_f32_i32_sdwa v98, sext(v64) dst_sel:DWORD dst_unused:UNUSED_PAD src0_sel:BYTE_2
	v_fmac_f32_e32 v97, v99, v9
	v_cvt_f32_i32_sdwa v99, sext(v65) dst_sel:DWORD dst_unused:UNUSED_PAD src0_sel:BYTE_2
	v_fmac_f32_e32 v97, v100, v13
	v_cvt_f32_i32_sdwa v100, sext(v66) dst_sel:DWORD dst_unused:UNUSED_PAD src0_sel:BYTE_2
	v_add_u32_dpp v96, v96, v96 quad_perm:[2,3,0,1] row_mask:0xf bank_mask:0xf bound_ctrl:1
	v_fmac_f32_e32 v97, v101, v17
	v_cvt_f32_i32_sdwa v101, sext(v67) dst_sel:DWORD dst_unused:UNUSED_PAD src0_sel:BYTE_2
	v_fmac_f32_e32 v97, v98, v6
	v_cvt_f32_i32_sdwa v98, sext(v64) dst_sel:DWORD dst_unused:UNUSED_PAD src0_sel:BYTE_3
	v_fmac_f32_e32 v97, v99, v10
	v_cvt_f32_i32_sdwa v99, sext(v65) dst_sel:DWORD dst_unused:UNUSED_PAD src0_sel:BYTE_3
	v_add_u32_dpp v96, v96, v96 row_half_mirror row_mask:0xf bank_mask:0xf bound_ctrl:1
	v_fmac_f32_e32 v97, v100, v14
	v_cvt_f32_i32_sdwa v100, sext(v66) dst_sel:DWORD dst_unused:UNUSED_PAD src0_sel:BYTE_3
	v_fmac_f32_e32 v97, v101, v18
	v_cvt_f32_i32_sdwa v101, sext(v67) dst_sel:DWORD dst_unused:UNUSED_PAD src0_sel:BYTE_3
	v_fmac_f32_e32 v97, v98, v7
	v_fmac_f32_e32 v97, v99, v11
	v_fmac_f32_e32 v97, v100, v15
	v_fmac_f32_e32 v97, v101, v19
	v_cndmask_b32_e64 v102, v102, v96, s[48:49]
	s_waitcnt lgkmcnt(0)
	v_add_f32_dpp v97, v97, v97 quad_perm:[1,0,3,2] row_mask:0xf bank_mask:0xf bound_ctrl:1
	v_lshl_add_u32 v106, v104, 7, v2
	v_lshl_add_u32 v107, v105, 7, v2
	v_add_f32_dpp v97, v97, v97 quad_perm:[2,3,0,1] row_mask:0xf bank_mask:0xf bound_ctrl:1
	global_load_dwordx4 v[64:67], v106, s[18:19]
	global_load_dwordx4 v[68:71], v107, s[18:19]
	v_add_f32_dpp v97, v97, v97 row_half_mirror row_mask:0xf bank_mask:0xf bound_ctrl:1
	v_cndmask_b32_e64 v103, v103, v97, s[48:49]
	ds_bpermute_b32 v104, v3, v22 offset:160
	ds_bpermute_b32 v105, v3, v26 offset:160
	s_waitcnt vmcnt(16)
	v_mov_b32_e32 v96, 0
	v_dot4c_i32_i8_e32 v96, v72, v76
	v_cvt_f32_i32_sdwa v98, sext(v72) dst_sel:DWORD dst_unused:UNUSED_PAD src0_sel:BYTE_0
	v_cvt_f32_i32_sdwa v99, sext(v73) dst_sel:DWORD dst_unused:UNUSED_PAD src0_sel:BYTE_0
	v_dot4c_i32_i8_e32 v96, v73, v77
	v_cvt_f32_i32_sdwa v100, sext(v74) dst_sel:DWORD dst_unused:UNUSED_PAD src0_sel:BYTE_0
	v_dot4c_i32_i8_e32 v96, v74, v78
	v_cvt_f32_i32_sdwa v101, sext(v75) dst_sel:DWORD dst_unused:UNUSED_PAD src0_sel:BYTE_0
	v_dot4c_i32_i8_e32 v96, v75, v79
	v_fma_f32 v97, v98, v4, 0
	v_cvt_f32_i32_sdwa v98, sext(v72) dst_sel:DWORD dst_unused:UNUSED_PAD src0_sel:BYTE_1
	v_fmac_f32_e32 v97, v99, v8
	v_cvt_f32_i32_sdwa v99, sext(v73) dst_sel:DWORD dst_unused:UNUSED_PAD src0_sel:BYTE_1
	v_fmac_f32_e32 v97, v100, v12
	v_cvt_f32_i32_sdwa v100, sext(v74) dst_sel:DWORD dst_unused:UNUSED_PAD src0_sel:BYTE_1
	v_fmac_f32_e32 v97, v101, v16
	v_cvt_f32_i32_sdwa v101, sext(v75) dst_sel:DWORD dst_unused:UNUSED_PAD src0_sel:BYTE_1
	v_add_u32_dpp v96, v96, v96 quad_perm:[1,0,3,2] row_mask:0xf bank_mask:0xf bound_ctrl:1
	v_fmac_f32_e32 v97, v98, v5
	v_cvt_f32_i32_sdwa v98, sext(v72) dst_sel:DWORD dst_unused:UNUSED_PAD src0_sel:BYTE_2
	v_fmac_f32_e32 v97, v99, v9
	v_cvt_f32_i32_sdwa v99, sext(v73) dst_sel:DWORD dst_unused:UNUSED_PAD src0_sel:BYTE_2
	v_fmac_f32_e32 v97, v100, v13
	v_cvt_f32_i32_sdwa v100, sext(v74) dst_sel:DWORD dst_unused:UNUSED_PAD src0_sel:BYTE_2
	v_add_u32_dpp v96, v96, v96 quad_perm:[2,3,0,1] row_mask:0xf bank_mask:0xf bound_ctrl:1
	v_fmac_f32_e32 v97, v101, v17
	v_cvt_f32_i32_sdwa v101, sext(v75) dst_sel:DWORD dst_unused:UNUSED_PAD src0_sel:BYTE_2
	v_fmac_f32_e32 v97, v98, v6
	v_cvt_f32_i32_sdwa v98, sext(v72) dst_sel:DWORD dst_unused:UNUSED_PAD src0_sel:BYTE_3
	v_fmac_f32_e32 v97, v99, v10
	v_cvt_f32_i32_sdwa v99, sext(v73) dst_sel:DWORD dst_unused:UNUSED_PAD src0_sel:BYTE_3
	v_add_u32_dpp v96, v96, v96 row_half_mirror row_mask:0xf bank_mask:0xf bound_ctrl:1
	v_fmac_f32_e32 v97, v100, v14
	v_cvt_f32_i32_sdwa v100, sext(v74) dst_sel:DWORD dst_unused:UNUSED_PAD src0_sel:BYTE_3
	v_fmac_f32_e32 v97, v101, v18
	v_cvt_f32_i32_sdwa v101, sext(v75) dst_sel:DWORD dst_unused:UNUSED_PAD src0_sel:BYTE_3
	v_fmac_f32_e32 v97, v98, v7
	v_fmac_f32_e32 v97, v99, v11
	v_fmac_f32_e32 v97, v100, v15
	v_fmac_f32_e32 v97, v101, v19
	v_cndmask_b32_e64 v102, v102, v96, s[50:51]
	s_waitcnt lgkmcnt(0)
	v_add_f32_dpp v97, v97, v97 quad_perm:[1,0,3,2] row_mask:0xf bank_mask:0xf bound_ctrl:1
	v_lshl_add_u32 v106, v104, 7, v2
	v_lshl_add_u32 v107, v105, 7, v2
	v_add_f32_dpp v97, v97, v97 quad_perm:[2,3,0,1] row_mask:0xf bank_mask:0xf bound_ctrl:1
	global_load_dwordx4 v[72:75], v106, s[18:19]
	global_load_dwordx4 v[76:79], v107, s[18:19]
	v_add_f32_dpp v97, v97, v97 row_half_mirror row_mask:0xf bank_mask:0xf bound_ctrl:1
	v_cndmask_b32_e64 v103, v103, v97, s[50:51]
	ds_bpermute_b32 v104, v3, v22 offset:192
	ds_bpermute_b32 v105, v3, v26 offset:192
	s_waitcnt vmcnt(16)
	v_mov_b32_e32 v96, 0
	v_dot4c_i32_i8_e32 v96, v80, v84
	v_cvt_f32_i32_sdwa v98, sext(v80) dst_sel:DWORD dst_unused:UNUSED_PAD src0_sel:BYTE_0
	v_cvt_f32_i32_sdwa v99, sext(v81) dst_sel:DWORD dst_unused:UNUSED_PAD src0_sel:BYTE_0
	v_dot4c_i32_i8_e32 v96, v81, v85
	v_cvt_f32_i32_sdwa v100, sext(v82) dst_sel:DWORD dst_unused:UNUSED_PAD src0_sel:BYTE_0
	v_dot4c_i32_i8_e32 v96, v82, v86
	v_cvt_f32_i32_sdwa v101, sext(v83) dst_sel:DWORD dst_unused:UNUSED_PAD src0_sel:BYTE_0
	v_dot4c_i32_i8_e32 v96, v83, v87
	v_fma_f32 v97, v98, v4, 0
	v_cvt_f32_i32_sdwa v98, sext(v80) dst_sel:DWORD dst_unused:UNUSED_PAD src0_sel:BYTE_1
	v_fmac_f32_e32 v97, v99, v8
	v_cvt_f32_i32_sdwa v99, sext(v81) dst_sel:DWORD dst_unused:UNUSED_PAD src0_sel:BYTE_1
	v_fmac_f32_e32 v97, v100, v12
	v_cvt_f32_i32_sdwa v100, sext(v82) dst_sel:DWORD dst_unused:UNUSED_PAD src0_sel:BYTE_1
	v_fmac_f32_e32 v97, v101, v16
	v_cvt_f32_i32_sdwa v101, sext(v83) dst_sel:DWORD dst_unused:UNUSED_PAD src0_sel:BYTE_1
	v_add_u32_dpp v96, v96, v96 quad_perm:[1,0,3,2] row_mask:0xf bank_mask:0xf bound_ctrl:1
	v_fmac_f32_e32 v97, v98, v5
	v_cvt_f32_i32_sdwa v98, sext(v80) dst_sel:DWORD dst_unused:UNUSED_PAD src0_sel:BYTE_2
	v_fmac_f32_e32 v97, v99, v9
	v_cvt_f32_i32_sdwa v99, sext(v81) dst_sel:DWORD dst_unused:UNUSED_PAD src0_sel:BYTE_2
	v_fmac_f32_e32 v97, v100, v13
	v_cvt_f32_i32_sdwa v100, sext(v82) dst_sel:DWORD dst_unused:UNUSED_PAD src0_sel:BYTE_2
	v_add_u32_dpp v96, v96, v96 quad_perm:[2,3,0,1] row_mask:0xf bank_mask:0xf bound_ctrl:1
	v_fmac_f32_e32 v97, v101, v17
	v_cvt_f32_i32_sdwa v101, sext(v83) dst_sel:DWORD dst_unused:UNUSED_PAD src0_sel:BYTE_2
	v_fmac_f32_e32 v97, v98, v6
	v_cvt_f32_i32_sdwa v98, sext(v80) dst_sel:DWORD dst_unused:UNUSED_PAD src0_sel:BYTE_3
	v_fmac_f32_e32 v97, v99, v10
	v_cvt_f32_i32_sdwa v99, sext(v81) dst_sel:DWORD dst_unused:UNUSED_PAD src0_sel:BYTE_3
	v_add_u32_dpp v96, v96, v96 row_half_mirror row_mask:0xf bank_mask:0xf bound_ctrl:1
	v_fmac_f32_e32 v97, v100, v14
	v_cvt_f32_i32_sdwa v100, sext(v82) dst_sel:DWORD dst_unused:UNUSED_PAD src0_sel:BYTE_3
	v_fmac_f32_e32 v97, v101, v18
	v_cvt_f32_i32_sdwa v101, sext(v83) dst_sel:DWORD dst_unused:UNUSED_PAD src0_sel:BYTE_3
	v_fmac_f32_e32 v97, v98, v7
	v_fmac_f32_e32 v97, v99, v11
	v_fmac_f32_e32 v97, v100, v15
	v_fmac_f32_e32 v97, v101, v19
	v_cndmask_b32_e64 v102, v102, v96, s[52:53]
	s_waitcnt lgkmcnt(0)
	v_add_f32_dpp v97, v97, v97 quad_perm:[1,0,3,2] row_mask:0xf bank_mask:0xf bound_ctrl:1
	v_lshl_add_u32 v106, v104, 7, v2
	v_lshl_add_u32 v107, v105, 7, v2
	v_add_f32_dpp v97, v97, v97 quad_perm:[2,3,0,1] row_mask:0xf bank_mask:0xf bound_ctrl:1
	global_load_dwordx4 v[80:83], v106, s[18:19]
	global_load_dwordx4 v[84:87], v107, s[18:19]
	v_add_f32_dpp v97, v97, v97 row_half_mirror row_mask:0xf bank_mask:0xf bound_ctrl:1
	v_cndmask_b32_e64 v103, v103, v97, s[52:53]
	ds_bpermute_b32 v104, v3, v22 offset:224
	ds_bpermute_b32 v105, v3, v26 offset:224
	s_waitcnt vmcnt(16)
	v_mov_b32_e32 v96, 0
	v_dot4c_i32_i8_e32 v96, v88, v92
	v_cvt_f32_i32_sdwa v98, sext(v88) dst_sel:DWORD dst_unused:UNUSED_PAD src0_sel:BYTE_0
	v_cvt_f32_i32_sdwa v99, sext(v89) dst_sel:DWORD dst_unused:UNUSED_PAD src0_sel:BYTE_0
	v_dot4c_i32_i8_e32 v96, v89, v93
	v_cvt_f32_i32_sdwa v100, sext(v90) dst_sel:DWORD dst_unused:UNUSED_PAD src0_sel:BYTE_0
	v_dot4c_i32_i8_e32 v96, v90, v94
	v_cvt_f32_i32_sdwa v101, sext(v91) dst_sel:DWORD dst_unused:UNUSED_PAD src0_sel:BYTE_0
	v_dot4c_i32_i8_e32 v96, v91, v95
	v_fma_f32 v97, v98, v4, 0
	v_cvt_f32_i32_sdwa v98, sext(v88) dst_sel:DWORD dst_unused:UNUSED_PAD src0_sel:BYTE_1
	v_fmac_f32_e32 v97, v99, v8
	v_cvt_f32_i32_sdwa v99, sext(v89) dst_sel:DWORD dst_unused:UNUSED_PAD src0_sel:BYTE_1
	v_fmac_f32_e32 v97, v100, v12
	v_cvt_f32_i32_sdwa v100, sext(v90) dst_sel:DWORD dst_unused:UNUSED_PAD src0_sel:BYTE_1
	v_fmac_f32_e32 v97, v101, v16
	v_cvt_f32_i32_sdwa v101, sext(v91) dst_sel:DWORD dst_unused:UNUSED_PAD src0_sel:BYTE_1
	v_add_u32_dpp v96, v96, v96 quad_perm:[1,0,3,2] row_mask:0xf bank_mask:0xf bound_ctrl:1
	v_fmac_f32_e32 v97, v98, v5
	v_cvt_f32_i32_sdwa v98, sext(v88) dst_sel:DWORD dst_unused:UNUSED_PAD src0_sel:BYTE_2
	v_fmac_f32_e32 v97, v99, v9
	v_cvt_f32_i32_sdwa v99, sext(v89) dst_sel:DWORD dst_unused:UNUSED_PAD src0_sel:BYTE_2
	v_fmac_f32_e32 v97, v100, v13
	v_cvt_f32_i32_sdwa v100, sext(v90) dst_sel:DWORD dst_unused:UNUSED_PAD src0_sel:BYTE_2
	v_add_u32_dpp v96, v96, v96 quad_perm:[2,3,0,1] row_mask:0xf bank_mask:0xf bound_ctrl:1
	v_fmac_f32_e32 v97, v101, v17
	v_cvt_f32_i32_sdwa v101, sext(v91) dst_sel:DWORD dst_unused:UNUSED_PAD src0_sel:BYTE_2
	v_fmac_f32_e32 v97, v98, v6
	v_cvt_f32_i32_sdwa v98, sext(v88) dst_sel:DWORD dst_unused:UNUSED_PAD src0_sel:BYTE_3
	v_fmac_f32_e32 v97, v99, v10
	v_cvt_f32_i32_sdwa v99, sext(v89) dst_sel:DWORD dst_unused:UNUSED_PAD src0_sel:BYTE_3
	v_add_u32_dpp v96, v96, v96 row_half_mirror row_mask:0xf bank_mask:0xf bound_ctrl:1
	v_fmac_f32_e32 v97, v100, v14
	v_cvt_f32_i32_sdwa v100, sext(v90) dst_sel:DWORD dst_unused:UNUSED_PAD src0_sel:BYTE_3
	v_fmac_f32_e32 v97, v101, v18
	v_cvt_f32_i32_sdwa v101, sext(v91) dst_sel:DWORD dst_unused:UNUSED_PAD src0_sel:BYTE_3
	v_fmac_f32_e32 v97, v98, v7
	v_fmac_f32_e32 v97, v99, v11
	v_fmac_f32_e32 v97, v100, v15
	v_fmac_f32_e32 v97, v101, v19
	v_cndmask_b32_e64 v102, v102, v96, s[54:55]
	s_waitcnt lgkmcnt(0)
	v_add_f32_dpp v97, v97, v97 quad_perm:[1,0,3,2] row_mask:0xf bank_mask:0xf bound_ctrl:1
	v_lshl_add_u32 v106, v104, 7, v2
	v_lshl_add_u32 v107, v105, 7, v2
	v_add_f32_dpp v97, v97, v97 quad_perm:[2,3,0,1] row_mask:0xf bank_mask:0xf bound_ctrl:1
	global_load_dwordx4 v[88:91], v106, s[18:19]
	global_load_dwordx4 v[92:95], v107, s[18:19]
	v_add_f32_dpp v97, v97, v97 row_half_mirror row_mask:0xf bank_mask:0xf bound_ctrl:1
	v_cndmask_b32_e64 v103, v103, v97, s[54:55]
	global_atomic_add v28, v102, s[20:21] offset:256
	global_atomic_add_f32 v28, v103, s[22:23] offset:256
	ds_bpermute_b32 v104, v3, v23
	ds_bpermute_b32 v105, v3, v27
	s_waitcnt vmcnt(16)
	v_mov_b32_e32 v96, 0
	v_dot4c_i32_i8_e32 v96, v32, v36
	v_cvt_f32_i32_sdwa v98, sext(v32) dst_sel:DWORD dst_unused:UNUSED_PAD src0_sel:BYTE_0
	v_cvt_f32_i32_sdwa v99, sext(v33) dst_sel:DWORD dst_unused:UNUSED_PAD src0_sel:BYTE_0
	v_dot4c_i32_i8_e32 v96, v33, v37
	v_cvt_f32_i32_sdwa v100, sext(v34) dst_sel:DWORD dst_unused:UNUSED_PAD src0_sel:BYTE_0
	v_dot4c_i32_i8_e32 v96, v34, v38
	v_cvt_f32_i32_sdwa v101, sext(v35) dst_sel:DWORD dst_unused:UNUSED_PAD src0_sel:BYTE_0
	v_dot4c_i32_i8_e32 v96, v35, v39
	v_fma_f32 v97, v98, v4, 0
	v_cvt_f32_i32_sdwa v98, sext(v32) dst_sel:DWORD dst_unused:UNUSED_PAD src0_sel:BYTE_1
	v_fmac_f32_e32 v97, v99, v8
	v_cvt_f32_i32_sdwa v99, sext(v33) dst_sel:DWORD dst_unused:UNUSED_PAD src0_sel:BYTE_1
	v_fmac_f32_e32 v97, v100, v12
	v_cvt_f32_i32_sdwa v100, sext(v34) dst_sel:DWORD dst_unused:UNUSED_PAD src0_sel:BYTE_1
	v_fmac_f32_e32 v97, v101, v16
	v_cvt_f32_i32_sdwa v101, sext(v35) dst_sel:DWORD dst_unused:UNUSED_PAD src0_sel:BYTE_1
	v_add_u32_dpp v96, v96, v96 quad_perm:[1,0,3,2] row_mask:0xf bank_mask:0xf bound_ctrl:1
	v_fmac_f32_e32 v97, v98, v5
	v_cvt_f32_i32_sdwa v98, sext(v32) dst_sel:DWORD dst_unused:UNUSED_PAD src0_sel:BYTE_2
	v_fmac_f32_e32 v97, v99, v9
	v_cvt_f32_i32_sdwa v99, sext(v33) dst_sel:DWORD dst_unused:UNUSED_PAD src0_sel:BYTE_2
	v_fmac_f32_e32 v97, v100, v13
	v_cvt_f32_i32_sdwa v100, sext(v34) dst_sel:DWORD dst_unused:UNUSED_PAD src0_sel:BYTE_2
	v_add_u32_dpp v96, v96, v96 quad_perm:[2,3,0,1] row_mask:0xf bank_mask:0xf bound_ctrl:1
	v_fmac_f32_e32 v97, v101, v17
	v_cvt_f32_i32_sdwa v101, sext(v35) dst_sel:DWORD dst_unused:UNUSED_PAD src0_sel:BYTE_2
	v_fmac_f32_e32 v97, v98, v6
	v_cvt_f32_i32_sdwa v98, sext(v32) dst_sel:DWORD dst_unused:UNUSED_PAD src0_sel:BYTE_3
	v_fmac_f32_e32 v97, v99, v10
	v_cvt_f32_i32_sdwa v99, sext(v33) dst_sel:DWORD dst_unused:UNUSED_PAD src0_sel:BYTE_3
	v_add_u32_dpp v96, v96, v96 row_half_mirror row_mask:0xf bank_mask:0xf bound_ctrl:1
	v_fmac_f32_e32 v97, v100, v14
	v_cvt_f32_i32_sdwa v100, sext(v34) dst_sel:DWORD dst_unused:UNUSED_PAD src0_sel:BYTE_3
	v_fmac_f32_e32 v97, v101, v18
	v_cvt_f32_i32_sdwa v101, sext(v35) dst_sel:DWORD dst_unused:UNUSED_PAD src0_sel:BYTE_3
	v_fmac_f32_e32 v97, v98, v7
	v_fmac_f32_e32 v97, v99, v11
	v_fmac_f32_e32 v97, v100, v15
	v_fmac_f32_e32 v97, v101, v19
	v_cndmask_b32_e64 v102, 0, v96, s[40:41]
	s_waitcnt lgkmcnt(0)
	v_add_f32_dpp v97, v97, v97 quad_perm:[1,0,3,2] row_mask:0xf bank_mask:0xf bound_ctrl:1
	v_lshl_add_u32 v106, v104, 7, v2
	v_lshl_add_u32 v107, v105, 7, v2
	v_add_f32_dpp v97, v97, v97 quad_perm:[2,3,0,1] row_mask:0xf bank_mask:0xf bound_ctrl:1
	global_load_dwordx4 v[32:35], v106, s[18:19]
	global_load_dwordx4 v[36:39], v107, s[18:19]
	v_add_f32_dpp v97, v97, v97 row_half_mirror row_mask:0xf bank_mask:0xf bound_ctrl:1
	v_cndmask_b32_e64 v103, 0, v97, s[40:41]
	ds_bpermute_b32 v104, v3, v23 offset:32
	ds_bpermute_b32 v105, v3, v27 offset:32
	s_waitcnt vmcnt(16)
	v_mov_b32_e32 v96, 0
	v_dot4c_i32_i8_e32 v96, v40, v44
	v_cvt_f32_i32_sdwa v98, sext(v40) dst_sel:DWORD dst_unused:UNUSED_PAD src0_sel:BYTE_0
	v_cvt_f32_i32_sdwa v99, sext(v41) dst_sel:DWORD dst_unused:UNUSED_PAD src0_sel:BYTE_0
	v_dot4c_i32_i8_e32 v96, v41, v45
	v_cvt_f32_i32_sdwa v100, sext(v42) dst_sel:DWORD dst_unused:UNUSED_PAD src0_sel:BYTE_0
	v_dot4c_i32_i8_e32 v96, v42, v46
	v_cvt_f32_i32_sdwa v101, sext(v43) dst_sel:DWORD dst_unused:UNUSED_PAD src0_sel:BYTE_0
	v_dot4c_i32_i8_e32 v96, v43, v47
	v_fma_f32 v97, v98, v4, 0
	v_cvt_f32_i32_sdwa v98, sext(v40) dst_sel:DWORD dst_unused:UNUSED_PAD src0_sel:BYTE_1
	v_fmac_f32_e32 v97, v99, v8
	v_cvt_f32_i32_sdwa v99, sext(v41) dst_sel:DWORD dst_unused:UNUSED_PAD src0_sel:BYTE_1
	v_fmac_f32_e32 v97, v100, v12
	v_cvt_f32_i32_sdwa v100, sext(v42) dst_sel:DWORD dst_unused:UNUSED_PAD src0_sel:BYTE_1
	v_fmac_f32_e32 v97, v101, v16
	v_cvt_f32_i32_sdwa v101, sext(v43) dst_sel:DWORD dst_unused:UNUSED_PAD src0_sel:BYTE_1
	v_add_u32_dpp v96, v96, v96 quad_perm:[1,0,3,2] row_mask:0xf bank_mask:0xf bound_ctrl:1
	v_fmac_f32_e32 v97, v98, v5
	v_cvt_f32_i32_sdwa v98, sext(v40) dst_sel:DWORD dst_unused:UNUSED_PAD src0_sel:BYTE_2
	v_fmac_f32_e32 v97, v99, v9
	v_cvt_f32_i32_sdwa v99, sext(v41) dst_sel:DWORD dst_unused:UNUSED_PAD src0_sel:BYTE_2
	v_fmac_f32_e32 v97, v100, v13
	v_cvt_f32_i32_sdwa v100, sext(v42) dst_sel:DWORD dst_unused:UNUSED_PAD src0_sel:BYTE_2
	v_add_u32_dpp v96, v96, v96 quad_perm:[2,3,0,1] row_mask:0xf bank_mask:0xf bound_ctrl:1
	v_fmac_f32_e32 v97, v101, v17
	v_cvt_f32_i32_sdwa v101, sext(v43) dst_sel:DWORD dst_unused:UNUSED_PAD src0_sel:BYTE_2
	v_fmac_f32_e32 v97, v98, v6
	v_cvt_f32_i32_sdwa v98, sext(v40) dst_sel:DWORD dst_unused:UNUSED_PAD src0_sel:BYTE_3
	v_fmac_f32_e32 v97, v99, v10
	v_cvt_f32_i32_sdwa v99, sext(v41) dst_sel:DWORD dst_unused:UNUSED_PAD src0_sel:BYTE_3
	v_add_u32_dpp v96, v96, v96 row_half_mirror row_mask:0xf bank_mask:0xf bound_ctrl:1
	v_fmac_f32_e32 v97, v100, v14
	v_cvt_f32_i32_sdwa v100, sext(v42) dst_sel:DWORD dst_unused:UNUSED_PAD src0_sel:BYTE_3
	v_fmac_f32_e32 v97, v101, v18
	v_cvt_f32_i32_sdwa v101, sext(v43) dst_sel:DWORD dst_unused:UNUSED_PAD src0_sel:BYTE_3
	v_fmac_f32_e32 v97, v98, v7
	v_fmac_f32_e32 v97, v99, v11
	v_fmac_f32_e32 v97, v100, v15
	v_fmac_f32_e32 v97, v101, v19
	v_cndmask_b32_e64 v102, v102, v96, s[42:43]
	s_waitcnt lgkmcnt(0)
	v_add_f32_dpp v97, v97, v97 quad_perm:[1,0,3,2] row_mask:0xf bank_mask:0xf bound_ctrl:1
	v_lshl_add_u32 v106, v104, 7, v2
	v_lshl_add_u32 v107, v105, 7, v2
	v_add_f32_dpp v97, v97, v97 quad_perm:[2,3,0,1] row_mask:0xf bank_mask:0xf bound_ctrl:1
	global_load_dwordx4 v[40:43], v106, s[18:19]
	global_load_dwordx4 v[44:47], v107, s[18:19]
	v_add_f32_dpp v97, v97, v97 row_half_mirror row_mask:0xf bank_mask:0xf bound_ctrl:1
	v_cndmask_b32_e64 v103, v103, v97, s[42:43]
	ds_bpermute_b32 v104, v3, v23 offset:64
	ds_bpermute_b32 v105, v3, v27 offset:64
	s_waitcnt vmcnt(16)
	v_mov_b32_e32 v96, 0
	v_dot4c_i32_i8_e32 v96, v48, v52
	v_cvt_f32_i32_sdwa v98, sext(v48) dst_sel:DWORD dst_unused:UNUSED_PAD src0_sel:BYTE_0
	v_cvt_f32_i32_sdwa v99, sext(v49) dst_sel:DWORD dst_unused:UNUSED_PAD src0_sel:BYTE_0
	v_dot4c_i32_i8_e32 v96, v49, v53
	v_cvt_f32_i32_sdwa v100, sext(v50) dst_sel:DWORD dst_unused:UNUSED_PAD src0_sel:BYTE_0
	v_dot4c_i32_i8_e32 v96, v50, v54
	v_cvt_f32_i32_sdwa v101, sext(v51) dst_sel:DWORD dst_unused:UNUSED_PAD src0_sel:BYTE_0
	v_dot4c_i32_i8_e32 v96, v51, v55
	v_fma_f32 v97, v98, v4, 0
	v_cvt_f32_i32_sdwa v98, sext(v48) dst_sel:DWORD dst_unused:UNUSED_PAD src0_sel:BYTE_1
	v_fmac_f32_e32 v97, v99, v8
	v_cvt_f32_i32_sdwa v99, sext(v49) dst_sel:DWORD dst_unused:UNUSED_PAD src0_sel:BYTE_1
	v_fmac_f32_e32 v97, v100, v12
	v_cvt_f32_i32_sdwa v100, sext(v50) dst_sel:DWORD dst_unused:UNUSED_PAD src0_sel:BYTE_1
	v_fmac_f32_e32 v97, v101, v16
	v_cvt_f32_i32_sdwa v101, sext(v51) dst_sel:DWORD dst_unused:UNUSED_PAD src0_sel:BYTE_1
	v_add_u32_dpp v96, v96, v96 quad_perm:[1,0,3,2] row_mask:0xf bank_mask:0xf bound_ctrl:1
	v_fmac_f32_e32 v97, v98, v5
	v_cvt_f32_i32_sdwa v98, sext(v48) dst_sel:DWORD dst_unused:UNUSED_PAD src0_sel:BYTE_2
	v_fmac_f32_e32 v97, v99, v9
	v_cvt_f32_i32_sdwa v99, sext(v49) dst_sel:DWORD dst_unused:UNUSED_PAD src0_sel:BYTE_2
	v_fmac_f32_e32 v97, v100, v13
	v_cvt_f32_i32_sdwa v100, sext(v50) dst_sel:DWORD dst_unused:UNUSED_PAD src0_sel:BYTE_2
	v_add_u32_dpp v96, v96, v96 quad_perm:[2,3,0,1] row_mask:0xf bank_mask:0xf bound_ctrl:1
	v_fmac_f32_e32 v97, v101, v17
	v_cvt_f32_i32_sdwa v101, sext(v51) dst_sel:DWORD dst_unused:UNUSED_PAD src0_sel:BYTE_2
	v_fmac_f32_e32 v97, v98, v6
	v_cvt_f32_i32_sdwa v98, sext(v48) dst_sel:DWORD dst_unused:UNUSED_PAD src0_sel:BYTE_3
	v_fmac_f32_e32 v97, v99, v10
	v_cvt_f32_i32_sdwa v99, sext(v49) dst_sel:DWORD dst_unused:UNUSED_PAD src0_sel:BYTE_3
	v_add_u32_dpp v96, v96, v96 row_half_mirror row_mask:0xf bank_mask:0xf bound_ctrl:1
	v_fmac_f32_e32 v97, v100, v14
	v_cvt_f32_i32_sdwa v100, sext(v50) dst_sel:DWORD dst_unused:UNUSED_PAD src0_sel:BYTE_3
	v_fmac_f32_e32 v97, v101, v18
	v_cvt_f32_i32_sdwa v101, sext(v51) dst_sel:DWORD dst_unused:UNUSED_PAD src0_sel:BYTE_3
	v_fmac_f32_e32 v97, v98, v7
	v_fmac_f32_e32 v97, v99, v11
	v_fmac_f32_e32 v97, v100, v15
	v_fmac_f32_e32 v97, v101, v19
	v_cndmask_b32_e64 v102, v102, v96, s[44:45]
	s_waitcnt lgkmcnt(0)
	v_add_f32_dpp v97, v97, v97 quad_perm:[1,0,3,2] row_mask:0xf bank_mask:0xf bound_ctrl:1
	v_lshl_add_u32 v106, v104, 7, v2
	v_lshl_add_u32 v107, v105, 7, v2
	v_add_f32_dpp v97, v97, v97 quad_perm:[2,3,0,1] row_mask:0xf bank_mask:0xf bound_ctrl:1
	global_load_dwordx4 v[48:51], v106, s[18:19]
	global_load_dwordx4 v[52:55], v107, s[18:19]
	v_add_f32_dpp v97, v97, v97 row_half_mirror row_mask:0xf bank_mask:0xf bound_ctrl:1
	v_cndmask_b32_e64 v103, v103, v97, s[44:45]
	ds_bpermute_b32 v104, v3, v23 offset:96
	ds_bpermute_b32 v105, v3, v27 offset:96
	s_waitcnt vmcnt(16)
	v_mov_b32_e32 v96, 0
	v_dot4c_i32_i8_e32 v96, v56, v60
	v_cvt_f32_i32_sdwa v98, sext(v56) dst_sel:DWORD dst_unused:UNUSED_PAD src0_sel:BYTE_0
	v_cvt_f32_i32_sdwa v99, sext(v57) dst_sel:DWORD dst_unused:UNUSED_PAD src0_sel:BYTE_0
	v_dot4c_i32_i8_e32 v96, v57, v61
	v_cvt_f32_i32_sdwa v100, sext(v58) dst_sel:DWORD dst_unused:UNUSED_PAD src0_sel:BYTE_0
	v_dot4c_i32_i8_e32 v96, v58, v62
	v_cvt_f32_i32_sdwa v101, sext(v59) dst_sel:DWORD dst_unused:UNUSED_PAD src0_sel:BYTE_0
	v_dot4c_i32_i8_e32 v96, v59, v63
	v_fma_f32 v97, v98, v4, 0
	v_cvt_f32_i32_sdwa v98, sext(v56) dst_sel:DWORD dst_unused:UNUSED_PAD src0_sel:BYTE_1
	v_fmac_f32_e32 v97, v99, v8
	v_cvt_f32_i32_sdwa v99, sext(v57) dst_sel:DWORD dst_unused:UNUSED_PAD src0_sel:BYTE_1
	v_fmac_f32_e32 v97, v100, v12
	v_cvt_f32_i32_sdwa v100, sext(v58) dst_sel:DWORD dst_unused:UNUSED_PAD src0_sel:BYTE_1
	v_fmac_f32_e32 v97, v101, v16
	v_cvt_f32_i32_sdwa v101, sext(v59) dst_sel:DWORD dst_unused:UNUSED_PAD src0_sel:BYTE_1
	v_add_u32_dpp v96, v96, v96 quad_perm:[1,0,3,2] row_mask:0xf bank_mask:0xf bound_ctrl:1
	v_fmac_f32_e32 v97, v98, v5
	v_cvt_f32_i32_sdwa v98, sext(v56) dst_sel:DWORD dst_unused:UNUSED_PAD src0_sel:BYTE_2
	v_fmac_f32_e32 v97, v99, v9
	v_cvt_f32_i32_sdwa v99, sext(v57) dst_sel:DWORD dst_unused:UNUSED_PAD src0_sel:BYTE_2
	v_fmac_f32_e32 v97, v100, v13
	v_cvt_f32_i32_sdwa v100, sext(v58) dst_sel:DWORD dst_unused:UNUSED_PAD src0_sel:BYTE_2
	v_add_u32_dpp v96, v96, v96 quad_perm:[2,3,0,1] row_mask:0xf bank_mask:0xf bound_ctrl:1
	v_fmac_f32_e32 v97, v101, v17
	v_cvt_f32_i32_sdwa v101, sext(v59) dst_sel:DWORD dst_unused:UNUSED_PAD src0_sel:BYTE_2
	v_fmac_f32_e32 v97, v98, v6
	v_cvt_f32_i32_sdwa v98, sext(v56) dst_sel:DWORD dst_unused:UNUSED_PAD src0_sel:BYTE_3
	v_fmac_f32_e32 v97, v99, v10
	v_cvt_f32_i32_sdwa v99, sext(v57) dst_sel:DWORD dst_unused:UNUSED_PAD src0_sel:BYTE_3
	v_add_u32_dpp v96, v96, v96 row_half_mirror row_mask:0xf bank_mask:0xf bound_ctrl:1
	v_fmac_f32_e32 v97, v100, v14
	v_cvt_f32_i32_sdwa v100, sext(v58) dst_sel:DWORD dst_unused:UNUSED_PAD src0_sel:BYTE_3
	v_fmac_f32_e32 v97, v101, v18
	v_cvt_f32_i32_sdwa v101, sext(v59) dst_sel:DWORD dst_unused:UNUSED_PAD src0_sel:BYTE_3
	v_fmac_f32_e32 v97, v98, v7
	v_fmac_f32_e32 v97, v99, v11
	v_fmac_f32_e32 v97, v100, v15
	v_fmac_f32_e32 v97, v101, v19
	v_cndmask_b32_e64 v102, v102, v96, s[46:47]
	s_waitcnt lgkmcnt(0)
	v_add_f32_dpp v97, v97, v97 quad_perm:[1,0,3,2] row_mask:0xf bank_mask:0xf bound_ctrl:1
	v_lshl_add_u32 v106, v104, 7, v2
	v_lshl_add_u32 v107, v105, 7, v2
	v_add_f32_dpp v97, v97, v97 quad_perm:[2,3,0,1] row_mask:0xf bank_mask:0xf bound_ctrl:1
	global_load_dwordx4 v[56:59], v106, s[18:19]
	global_load_dwordx4 v[60:63], v107, s[18:19]
	v_add_f32_dpp v97, v97, v97 row_half_mirror row_mask:0xf bank_mask:0xf bound_ctrl:1
	v_cndmask_b32_e64 v103, v103, v97, s[46:47]
	ds_bpermute_b32 v104, v3, v23 offset:128
	ds_bpermute_b32 v105, v3, v27 offset:128
	s_waitcnt vmcnt(16)
	v_mov_b32_e32 v96, 0
	v_dot4c_i32_i8_e32 v96, v64, v68
	v_cvt_f32_i32_sdwa v98, sext(v64) dst_sel:DWORD dst_unused:UNUSED_PAD src0_sel:BYTE_0
	v_cvt_f32_i32_sdwa v99, sext(v65) dst_sel:DWORD dst_unused:UNUSED_PAD src0_sel:BYTE_0
	v_dot4c_i32_i8_e32 v96, v65, v69
	v_cvt_f32_i32_sdwa v100, sext(v66) dst_sel:DWORD dst_unused:UNUSED_PAD src0_sel:BYTE_0
	v_dot4c_i32_i8_e32 v96, v66, v70
	v_cvt_f32_i32_sdwa v101, sext(v67) dst_sel:DWORD dst_unused:UNUSED_PAD src0_sel:BYTE_0
	v_dot4c_i32_i8_e32 v96, v67, v71
	v_fma_f32 v97, v98, v4, 0
	v_cvt_f32_i32_sdwa v98, sext(v64) dst_sel:DWORD dst_unused:UNUSED_PAD src0_sel:BYTE_1
	v_fmac_f32_e32 v97, v99, v8
	v_cvt_f32_i32_sdwa v99, sext(v65) dst_sel:DWORD dst_unused:UNUSED_PAD src0_sel:BYTE_1
	v_fmac_f32_e32 v97, v100, v12
	v_cvt_f32_i32_sdwa v100, sext(v66) dst_sel:DWORD dst_unused:UNUSED_PAD src0_sel:BYTE_1
	v_fmac_f32_e32 v97, v101, v16
	v_cvt_f32_i32_sdwa v101, sext(v67) dst_sel:DWORD dst_unused:UNUSED_PAD src0_sel:BYTE_1
	v_add_u32_dpp v96, v96, v96 quad_perm:[1,0,3,2] row_mask:0xf bank_mask:0xf bound_ctrl:1
	v_fmac_f32_e32 v97, v98, v5
	v_cvt_f32_i32_sdwa v98, sext(v64) dst_sel:DWORD dst_unused:UNUSED_PAD src0_sel:BYTE_2
	v_fmac_f32_e32 v97, v99, v9
	v_cvt_f32_i32_sdwa v99, sext(v65) dst_sel:DWORD dst_unused:UNUSED_PAD src0_sel:BYTE_2
	v_fmac_f32_e32 v97, v100, v13
	v_cvt_f32_i32_sdwa v100, sext(v66) dst_sel:DWORD dst_unused:UNUSED_PAD src0_sel:BYTE_2
	v_add_u32_dpp v96, v96, v96 quad_perm:[2,3,0,1] row_mask:0xf bank_mask:0xf bound_ctrl:1
	v_fmac_f32_e32 v97, v101, v17
	v_cvt_f32_i32_sdwa v101, sext(v67) dst_sel:DWORD dst_unused:UNUSED_PAD src0_sel:BYTE_2
	v_fmac_f32_e32 v97, v98, v6
	v_cvt_f32_i32_sdwa v98, sext(v64) dst_sel:DWORD dst_unused:UNUSED_PAD src0_sel:BYTE_3
	v_fmac_f32_e32 v97, v99, v10
	v_cvt_f32_i32_sdwa v99, sext(v65) dst_sel:DWORD dst_unused:UNUSED_PAD src0_sel:BYTE_3
	v_add_u32_dpp v96, v96, v96 row_half_mirror row_mask:0xf bank_mask:0xf bound_ctrl:1
	v_fmac_f32_e32 v97, v100, v14
	v_cvt_f32_i32_sdwa v100, sext(v66) dst_sel:DWORD dst_unused:UNUSED_PAD src0_sel:BYTE_3
	v_fmac_f32_e32 v97, v101, v18
	v_cvt_f32_i32_sdwa v101, sext(v67) dst_sel:DWORD dst_unused:UNUSED_PAD src0_sel:BYTE_3
	v_fmac_f32_e32 v97, v98, v7
	v_fmac_f32_e32 v97, v99, v11
	v_fmac_f32_e32 v97, v100, v15
	v_fmac_f32_e32 v97, v101, v19
	v_cndmask_b32_e64 v102, v102, v96, s[48:49]
	s_waitcnt lgkmcnt(0)
	v_add_f32_dpp v97, v97, v97 quad_perm:[1,0,3,2] row_mask:0xf bank_mask:0xf bound_ctrl:1
	v_lshl_add_u32 v106, v104, 7, v2
	v_lshl_add_u32 v107, v105, 7, v2
	v_add_f32_dpp v97, v97, v97 quad_perm:[2,3,0,1] row_mask:0xf bank_mask:0xf bound_ctrl:1
	global_load_dwordx4 v[64:67], v106, s[18:19]
	global_load_dwordx4 v[68:71], v107, s[18:19]
	v_add_f32_dpp v97, v97, v97 row_half_mirror row_mask:0xf bank_mask:0xf bound_ctrl:1
	v_cndmask_b32_e64 v103, v103, v97, s[48:49]
	ds_bpermute_b32 v104, v3, v23 offset:160
	ds_bpermute_b32 v105, v3, v27 offset:160
	s_waitcnt vmcnt(16)
	v_mov_b32_e32 v96, 0
	v_dot4c_i32_i8_e32 v96, v72, v76
	v_cvt_f32_i32_sdwa v98, sext(v72) dst_sel:DWORD dst_unused:UNUSED_PAD src0_sel:BYTE_0
	v_cvt_f32_i32_sdwa v99, sext(v73) dst_sel:DWORD dst_unused:UNUSED_PAD src0_sel:BYTE_0
	v_dot4c_i32_i8_e32 v96, v73, v77
	v_cvt_f32_i32_sdwa v100, sext(v74) dst_sel:DWORD dst_unused:UNUSED_PAD src0_sel:BYTE_0
	v_dot4c_i32_i8_e32 v96, v74, v78
	v_cvt_f32_i32_sdwa v101, sext(v75) dst_sel:DWORD dst_unused:UNUSED_PAD src0_sel:BYTE_0
	v_dot4c_i32_i8_e32 v96, v75, v79
	v_fma_f32 v97, v98, v4, 0
	v_cvt_f32_i32_sdwa v98, sext(v72) dst_sel:DWORD dst_unused:UNUSED_PAD src0_sel:BYTE_1
	v_fmac_f32_e32 v97, v99, v8
	v_cvt_f32_i32_sdwa v99, sext(v73) dst_sel:DWORD dst_unused:UNUSED_PAD src0_sel:BYTE_1
	v_fmac_f32_e32 v97, v100, v12
	v_cvt_f32_i32_sdwa v100, sext(v74) dst_sel:DWORD dst_unused:UNUSED_PAD src0_sel:BYTE_1
	v_fmac_f32_e32 v97, v101, v16
	v_cvt_f32_i32_sdwa v101, sext(v75) dst_sel:DWORD dst_unused:UNUSED_PAD src0_sel:BYTE_1
	v_add_u32_dpp v96, v96, v96 quad_perm:[1,0,3,2] row_mask:0xf bank_mask:0xf bound_ctrl:1
	v_fmac_f32_e32 v97, v98, v5
	v_cvt_f32_i32_sdwa v98, sext(v72) dst_sel:DWORD dst_unused:UNUSED_PAD src0_sel:BYTE_2
	v_fmac_f32_e32 v97, v99, v9
	v_cvt_f32_i32_sdwa v99, sext(v73) dst_sel:DWORD dst_unused:UNUSED_PAD src0_sel:BYTE_2
	v_fmac_f32_e32 v97, v100, v13
	v_cvt_f32_i32_sdwa v100, sext(v74) dst_sel:DWORD dst_unused:UNUSED_PAD src0_sel:BYTE_2
	v_add_u32_dpp v96, v96, v96 quad_perm:[2,3,0,1] row_mask:0xf bank_mask:0xf bound_ctrl:1
	v_fmac_f32_e32 v97, v101, v17
	v_cvt_f32_i32_sdwa v101, sext(v75) dst_sel:DWORD dst_unused:UNUSED_PAD src0_sel:BYTE_2
	v_fmac_f32_e32 v97, v98, v6
	v_cvt_f32_i32_sdwa v98, sext(v72) dst_sel:DWORD dst_unused:UNUSED_PAD src0_sel:BYTE_3
	v_fmac_f32_e32 v97, v99, v10
	v_cvt_f32_i32_sdwa v99, sext(v73) dst_sel:DWORD dst_unused:UNUSED_PAD src0_sel:BYTE_3
	v_add_u32_dpp v96, v96, v96 row_half_mirror row_mask:0xf bank_mask:0xf bound_ctrl:1
	v_fmac_f32_e32 v97, v100, v14
	v_cvt_f32_i32_sdwa v100, sext(v74) dst_sel:DWORD dst_unused:UNUSED_PAD src0_sel:BYTE_3
	v_fmac_f32_e32 v97, v101, v18
	v_cvt_f32_i32_sdwa v101, sext(v75) dst_sel:DWORD dst_unused:UNUSED_PAD src0_sel:BYTE_3
	v_fmac_f32_e32 v97, v98, v7
	v_fmac_f32_e32 v97, v99, v11
	v_fmac_f32_e32 v97, v100, v15
	v_fmac_f32_e32 v97, v101, v19
	v_cndmask_b32_e64 v102, v102, v96, s[50:51]
	s_waitcnt lgkmcnt(0)
	v_add_f32_dpp v97, v97, v97 quad_perm:[1,0,3,2] row_mask:0xf bank_mask:0xf bound_ctrl:1
	v_lshl_add_u32 v106, v104, 7, v2
	v_lshl_add_u32 v107, v105, 7, v2
	v_add_f32_dpp v97, v97, v97 quad_perm:[2,3,0,1] row_mask:0xf bank_mask:0xf bound_ctrl:1
	global_load_dwordx4 v[72:75], v106, s[18:19]
	global_load_dwordx4 v[76:79], v107, s[18:19]
	v_add_f32_dpp v97, v97, v97 row_half_mirror row_mask:0xf bank_mask:0xf bound_ctrl:1
	v_cndmask_b32_e64 v103, v103, v97, s[50:51]
	ds_bpermute_b32 v104, v3, v23 offset:192
	ds_bpermute_b32 v105, v3, v27 offset:192
	s_waitcnt vmcnt(16)
	v_mov_b32_e32 v96, 0
	v_dot4c_i32_i8_e32 v96, v80, v84
	v_cvt_f32_i32_sdwa v98, sext(v80) dst_sel:DWORD dst_unused:UNUSED_PAD src0_sel:BYTE_0
	v_cvt_f32_i32_sdwa v99, sext(v81) dst_sel:DWORD dst_unused:UNUSED_PAD src0_sel:BYTE_0
	v_dot4c_i32_i8_e32 v96, v81, v85
	v_cvt_f32_i32_sdwa v100, sext(v82) dst_sel:DWORD dst_unused:UNUSED_PAD src0_sel:BYTE_0
	v_dot4c_i32_i8_e32 v96, v82, v86
	v_cvt_f32_i32_sdwa v101, sext(v83) dst_sel:DWORD dst_unused:UNUSED_PAD src0_sel:BYTE_0
	v_dot4c_i32_i8_e32 v96, v83, v87
	v_fma_f32 v97, v98, v4, 0
	v_cvt_f32_i32_sdwa v98, sext(v80) dst_sel:DWORD dst_unused:UNUSED_PAD src0_sel:BYTE_1
	v_fmac_f32_e32 v97, v99, v8
	v_cvt_f32_i32_sdwa v99, sext(v81) dst_sel:DWORD dst_unused:UNUSED_PAD src0_sel:BYTE_1
	v_fmac_f32_e32 v97, v100, v12
	v_cvt_f32_i32_sdwa v100, sext(v82) dst_sel:DWORD dst_unused:UNUSED_PAD src0_sel:BYTE_1
	v_fmac_f32_e32 v97, v101, v16
	v_cvt_f32_i32_sdwa v101, sext(v83) dst_sel:DWORD dst_unused:UNUSED_PAD src0_sel:BYTE_1
	v_add_u32_dpp v96, v96, v96 quad_perm:[1,0,3,2] row_mask:0xf bank_mask:0xf bound_ctrl:1
	v_fmac_f32_e32 v97, v98, v5
	v_cvt_f32_i32_sdwa v98, sext(v80) dst_sel:DWORD dst_unused:UNUSED_PAD src0_sel:BYTE_2
	v_fmac_f32_e32 v97, v99, v9
	v_cvt_f32_i32_sdwa v99, sext(v81) dst_sel:DWORD dst_unused:UNUSED_PAD src0_sel:BYTE_2
	v_fmac_f32_e32 v97, v100, v13
	v_cvt_f32_i32_sdwa v100, sext(v82) dst_sel:DWORD dst_unused:UNUSED_PAD src0_sel:BYTE_2
	v_add_u32_dpp v96, v96, v96 quad_perm:[2,3,0,1] row_mask:0xf bank_mask:0xf bound_ctrl:1
	v_fmac_f32_e32 v97, v101, v17
	v_cvt_f32_i32_sdwa v101, sext(v83) dst_sel:DWORD dst_unused:UNUSED_PAD src0_sel:BYTE_2
	v_fmac_f32_e32 v97, v98, v6
	v_cvt_f32_i32_sdwa v98, sext(v80) dst_sel:DWORD dst_unused:UNUSED_PAD src0_sel:BYTE_3
	v_fmac_f32_e32 v97, v99, v10
	v_cvt_f32_i32_sdwa v99, sext(v81) dst_sel:DWORD dst_unused:UNUSED_PAD src0_sel:BYTE_3
	v_add_u32_dpp v96, v96, v96 row_half_mirror row_mask:0xf bank_mask:0xf bound_ctrl:1
	v_fmac_f32_e32 v97, v100, v14
	v_cvt_f32_i32_sdwa v100, sext(v82) dst_sel:DWORD dst_unused:UNUSED_PAD src0_sel:BYTE_3
	v_fmac_f32_e32 v97, v101, v18
	v_cvt_f32_i32_sdwa v101, sext(v83) dst_sel:DWORD dst_unused:UNUSED_PAD src0_sel:BYTE_3
	v_fmac_f32_e32 v97, v98, v7
	v_fmac_f32_e32 v97, v99, v11
	v_fmac_f32_e32 v97, v100, v15
	v_fmac_f32_e32 v97, v101, v19
	v_cndmask_b32_e64 v102, v102, v96, s[52:53]
	s_waitcnt lgkmcnt(0)
	v_add_f32_dpp v97, v97, v97 quad_perm:[1,0,3,2] row_mask:0xf bank_mask:0xf bound_ctrl:1
	v_lshl_add_u32 v106, v104, 7, v2
	v_lshl_add_u32 v107, v105, 7, v2
	v_add_f32_dpp v97, v97, v97 quad_perm:[2,3,0,1] row_mask:0xf bank_mask:0xf bound_ctrl:1
	global_load_dwordx4 v[80:83], v106, s[18:19]
	global_load_dwordx4 v[84:87], v107, s[18:19]
	v_add_f32_dpp v97, v97, v97 row_half_mirror row_mask:0xf bank_mask:0xf bound_ctrl:1
	v_cndmask_b32_e64 v103, v103, v97, s[52:53]
	ds_bpermute_b32 v104, v3, v23 offset:224
	ds_bpermute_b32 v105, v3, v27 offset:224
	s_waitcnt vmcnt(16)
	v_mov_b32_e32 v96, 0
	v_dot4c_i32_i8_e32 v96, v88, v92
	v_cvt_f32_i32_sdwa v98, sext(v88) dst_sel:DWORD dst_unused:UNUSED_PAD src0_sel:BYTE_0
	v_cvt_f32_i32_sdwa v99, sext(v89) dst_sel:DWORD dst_unused:UNUSED_PAD src0_sel:BYTE_0
	v_dot4c_i32_i8_e32 v96, v89, v93
	v_cvt_f32_i32_sdwa v100, sext(v90) dst_sel:DWORD dst_unused:UNUSED_PAD src0_sel:BYTE_0
	v_dot4c_i32_i8_e32 v96, v90, v94
	v_cvt_f32_i32_sdwa v101, sext(v91) dst_sel:DWORD dst_unused:UNUSED_PAD src0_sel:BYTE_0
	v_dot4c_i32_i8_e32 v96, v91, v95
	v_fma_f32 v97, v98, v4, 0
	v_cvt_f32_i32_sdwa v98, sext(v88) dst_sel:DWORD dst_unused:UNUSED_PAD src0_sel:BYTE_1
	v_fmac_f32_e32 v97, v99, v8
	v_cvt_f32_i32_sdwa v99, sext(v89) dst_sel:DWORD dst_unused:UNUSED_PAD src0_sel:BYTE_1
	v_fmac_f32_e32 v97, v100, v12
	v_cvt_f32_i32_sdwa v100, sext(v90) dst_sel:DWORD dst_unused:UNUSED_PAD src0_sel:BYTE_1
	v_fmac_f32_e32 v97, v101, v16
	v_cvt_f32_i32_sdwa v101, sext(v91) dst_sel:DWORD dst_unused:UNUSED_PAD src0_sel:BYTE_1
	v_add_u32_dpp v96, v96, v96 quad_perm:[1,0,3,2] row_mask:0xf bank_mask:0xf bound_ctrl:1
	v_fmac_f32_e32 v97, v98, v5
	v_cvt_f32_i32_sdwa v98, sext(v88) dst_sel:DWORD dst_unused:UNUSED_PAD src0_sel:BYTE_2
	v_fmac_f32_e32 v97, v99, v9
	v_cvt_f32_i32_sdwa v99, sext(v89) dst_sel:DWORD dst_unused:UNUSED_PAD src0_sel:BYTE_2
	v_fmac_f32_e32 v97, v100, v13
	v_cvt_f32_i32_sdwa v100, sext(v90) dst_sel:DWORD dst_unused:UNUSED_PAD src0_sel:BYTE_2
	v_add_u32_dpp v96, v96, v96 quad_perm:[2,3,0,1] row_mask:0xf bank_mask:0xf bound_ctrl:1
	v_fmac_f32_e32 v97, v101, v17
	v_cvt_f32_i32_sdwa v101, sext(v91) dst_sel:DWORD dst_unused:UNUSED_PAD src0_sel:BYTE_2
	v_fmac_f32_e32 v97, v98, v6
	v_cvt_f32_i32_sdwa v98, sext(v88) dst_sel:DWORD dst_unused:UNUSED_PAD src0_sel:BYTE_3
	v_fmac_f32_e32 v97, v99, v10
	v_cvt_f32_i32_sdwa v99, sext(v89) dst_sel:DWORD dst_unused:UNUSED_PAD src0_sel:BYTE_3
	v_add_u32_dpp v96, v96, v96 row_half_mirror row_mask:0xf bank_mask:0xf bound_ctrl:1
	v_fmac_f32_e32 v97, v100, v14
	v_cvt_f32_i32_sdwa v100, sext(v90) dst_sel:DWORD dst_unused:UNUSED_PAD src0_sel:BYTE_3
	v_fmac_f32_e32 v97, v101, v18
	v_cvt_f32_i32_sdwa v101, sext(v91) dst_sel:DWORD dst_unused:UNUSED_PAD src0_sel:BYTE_3
	v_fmac_f32_e32 v97, v98, v7
	v_fmac_f32_e32 v97, v99, v11
	v_fmac_f32_e32 v97, v100, v15
	v_fmac_f32_e32 v97, v101, v19
	v_cndmask_b32_e64 v102, v102, v96, s[54:55]
	s_waitcnt lgkmcnt(0)
	v_add_f32_dpp v97, v97, v97 quad_perm:[1,0,3,2] row_mask:0xf bank_mask:0xf bound_ctrl:1
	v_lshl_add_u32 v106, v104, 7, v2
	v_lshl_add_u32 v107, v105, 7, v2
	v_add_f32_dpp v97, v97, v97 quad_perm:[2,3,0,1] row_mask:0xf bank_mask:0xf bound_ctrl:1
	global_load_dwordx4 v[88:91], v106, s[18:19]
	global_load_dwordx4 v[92:95], v107, s[18:19]
	v_add_f32_dpp v97, v97, v97 row_half_mirror row_mask:0xf bank_mask:0xf bound_ctrl:1
	v_cndmask_b32_e64 v103, v103, v97, s[54:55]
	global_atomic_add v28, v102, s[20:21] offset:512
	global_atomic_add_f32 v28, v103, s[22:23] offset:512
	s_waitcnt vmcnt(16)
	v_mov_b32_e32 v96, 0
	v_dot4c_i32_i8_e32 v96, v32, v36
	v_cvt_f32_i32_sdwa v98, sext(v32) dst_sel:DWORD dst_unused:UNUSED_PAD src0_sel:BYTE_0
	v_cvt_f32_i32_sdwa v99, sext(v33) dst_sel:DWORD dst_unused:UNUSED_PAD src0_sel:BYTE_0
	v_dot4c_i32_i8_e32 v96, v33, v37
	v_cvt_f32_i32_sdwa v100, sext(v34) dst_sel:DWORD dst_unused:UNUSED_PAD src0_sel:BYTE_0
	v_dot4c_i32_i8_e32 v96, v34, v38
	v_cvt_f32_i32_sdwa v101, sext(v35) dst_sel:DWORD dst_unused:UNUSED_PAD src0_sel:BYTE_0
	v_dot4c_i32_i8_e32 v96, v35, v39
	v_fma_f32 v97, v98, v4, 0
	v_cvt_f32_i32_sdwa v98, sext(v32) dst_sel:DWORD dst_unused:UNUSED_PAD src0_sel:BYTE_1
	v_fmac_f32_e32 v97, v99, v8
	v_cvt_f32_i32_sdwa v99, sext(v33) dst_sel:DWORD dst_unused:UNUSED_PAD src0_sel:BYTE_1
	v_fmac_f32_e32 v97, v100, v12
	v_cvt_f32_i32_sdwa v100, sext(v34) dst_sel:DWORD dst_unused:UNUSED_PAD src0_sel:BYTE_1
	v_fmac_f32_e32 v97, v101, v16
	v_cvt_f32_i32_sdwa v101, sext(v35) dst_sel:DWORD dst_unused:UNUSED_PAD src0_sel:BYTE_1
	v_add_u32_dpp v96, v96, v96 quad_perm:[1,0,3,2] row_mask:0xf bank_mask:0xf bound_ctrl:1
	v_fmac_f32_e32 v97, v98, v5
	v_cvt_f32_i32_sdwa v98, sext(v32) dst_sel:DWORD dst_unused:UNUSED_PAD src0_sel:BYTE_2
	v_fmac_f32_e32 v97, v99, v9
	v_cvt_f32_i32_sdwa v99, sext(v33) dst_sel:DWORD dst_unused:UNUSED_PAD src0_sel:BYTE_2
	v_fmac_f32_e32 v97, v100, v13
	v_cvt_f32_i32_sdwa v100, sext(v34) dst_sel:DWORD dst_unused:UNUSED_PAD src0_sel:BYTE_2
	v_add_u32_dpp v96, v96, v96 quad_perm:[2,3,0,1] row_mask:0xf bank_mask:0xf bound_ctrl:1
	v_fmac_f32_e32 v97, v101, v17
	v_cvt_f32_i32_sdwa v101, sext(v35) dst_sel:DWORD dst_unused:UNUSED_PAD src0_sel:BYTE_2
	v_fmac_f32_e32 v97, v98, v6
	v_cvt_f32_i32_sdwa v98, sext(v32) dst_sel:DWORD dst_unused:UNUSED_PAD src0_sel:BYTE_3
	v_fmac_f32_e32 v97, v99, v10
	v_cvt_f32_i32_sdwa v99, sext(v33) dst_sel:DWORD dst_unused:UNUSED_PAD src0_sel:BYTE_3
	v_add_u32_dpp v96, v96, v96 row_half_mirror row_mask:0xf bank_mask:0xf bound_ctrl:1
	v_fmac_f32_e32 v97, v100, v14
	v_cvt_f32_i32_sdwa v100, sext(v34) dst_sel:DWORD dst_unused:UNUSED_PAD src0_sel:BYTE_3
	v_fmac_f32_e32 v97, v101, v18
	v_cvt_f32_i32_sdwa v101, sext(v35) dst_sel:DWORD dst_unused:UNUSED_PAD src0_sel:BYTE_3
	v_fmac_f32_e32 v97, v98, v7
	v_fmac_f32_e32 v97, v99, v11
	v_fmac_f32_e32 v97, v100, v15
	v_fmac_f32_e32 v97, v101, v19
	v_cndmask_b32_e64 v102, 0, v96, s[40:41]
	s_nop 0
	v_add_f32_dpp v97, v97, v97 quad_perm:[1,0,3,2] row_mask:0xf bank_mask:0xf bound_ctrl:1
	s_nop 1
	v_add_f32_dpp v97, v97, v97 quad_perm:[2,3,0,1] row_mask:0xf bank_mask:0xf bound_ctrl:1
	s_nop 1
	v_add_f32_dpp v97, v97, v97 row_half_mirror row_mask:0xf bank_mask:0xf bound_ctrl:1
	v_cndmask_b32_e64 v103, 0, v97, s[40:41]
	s_waitcnt vmcnt(14)
	v_mov_b32_e32 v96, 0
	v_dot4c_i32_i8_e32 v96, v40, v44
	v_cvt_f32_i32_sdwa v98, sext(v40) dst_sel:DWORD dst_unused:UNUSED_PAD src0_sel:BYTE_0
	v_cvt_f32_i32_sdwa v99, sext(v41) dst_sel:DWORD dst_unused:UNUSED_PAD src0_sel:BYTE_0
	v_dot4c_i32_i8_e32 v96, v41, v45
	v_cvt_f32_i32_sdwa v100, sext(v42) dst_sel:DWORD dst_unused:UNUSED_PAD src0_sel:BYTE_0
	v_dot4c_i32_i8_e32 v96, v42, v46
	v_cvt_f32_i32_sdwa v101, sext(v43) dst_sel:DWORD dst_unused:UNUSED_PAD src0_sel:BYTE_0
	v_dot4c_i32_i8_e32 v96, v43, v47
	v_fma_f32 v97, v98, v4, 0
	v_cvt_f32_i32_sdwa v98, sext(v40) dst_sel:DWORD dst_unused:UNUSED_PAD src0_sel:BYTE_1
	v_fmac_f32_e32 v97, v99, v8
	v_cvt_f32_i32_sdwa v99, sext(v41) dst_sel:DWORD dst_unused:UNUSED_PAD src0_sel:BYTE_1
	v_fmac_f32_e32 v97, v100, v12
	v_cvt_f32_i32_sdwa v100, sext(v42) dst_sel:DWORD dst_unused:UNUSED_PAD src0_sel:BYTE_1
	v_fmac_f32_e32 v97, v101, v16
	v_cvt_f32_i32_sdwa v101, sext(v43) dst_sel:DWORD dst_unused:UNUSED_PAD src0_sel:BYTE_1
	v_add_u32_dpp v96, v96, v96 quad_perm:[1,0,3,2] row_mask:0xf bank_mask:0xf bound_ctrl:1
	v_fmac_f32_e32 v97, v98, v5
	v_cvt_f32_i32_sdwa v98, sext(v40) dst_sel:DWORD dst_unused:UNUSED_PAD src0_sel:BYTE_2
	v_fmac_f32_e32 v97, v99, v9
	v_cvt_f32_i32_sdwa v99, sext(v41) dst_sel:DWORD dst_unused:UNUSED_PAD src0_sel:BYTE_2
	v_fmac_f32_e32 v97, v100, v13
	v_cvt_f32_i32_sdwa v100, sext(v42) dst_sel:DWORD dst_unused:UNUSED_PAD src0_sel:BYTE_2
	v_add_u32_dpp v96, v96, v96 quad_perm:[2,3,0,1] row_mask:0xf bank_mask:0xf bound_ctrl:1
	v_fmac_f32_e32 v97, v101, v17
	v_cvt_f32_i32_sdwa v101, sext(v43) dst_sel:DWORD dst_unused:UNUSED_PAD src0_sel:BYTE_2
	v_fmac_f32_e32 v97, v98, v6
	v_cvt_f32_i32_sdwa v98, sext(v40) dst_sel:DWORD dst_unused:UNUSED_PAD src0_sel:BYTE_3
	v_fmac_f32_e32 v97, v99, v10
	v_cvt_f32_i32_sdwa v99, sext(v41) dst_sel:DWORD dst_unused:UNUSED_PAD src0_sel:BYTE_3
	v_add_u32_dpp v96, v96, v96 row_half_mirror row_mask:0xf bank_mask:0xf bound_ctrl:1
	v_fmac_f32_e32 v97, v100, v14
	v_cvt_f32_i32_sdwa v100, sext(v42) dst_sel:DWORD dst_unused:UNUSED_PAD src0_sel:BYTE_3
	v_fmac_f32_e32 v97, v101, v18
	v_cvt_f32_i32_sdwa v101, sext(v43) dst_sel:DWORD dst_unused:UNUSED_PAD src0_sel:BYTE_3
	v_fmac_f32_e32 v97, v98, v7
	v_fmac_f32_e32 v97, v99, v11
	v_fmac_f32_e32 v97, v100, v15
	v_fmac_f32_e32 v97, v101, v19
	v_cndmask_b32_e64 v102, v102, v96, s[42:43]
	s_nop 0
	v_add_f32_dpp v97, v97, v97 quad_perm:[1,0,3,2] row_mask:0xf bank_mask:0xf bound_ctrl:1
	s_nop 1
	v_add_f32_dpp v97, v97, v97 quad_perm:[2,3,0,1] row_mask:0xf bank_mask:0xf bound_ctrl:1
	s_nop 1
	v_add_f32_dpp v97, v97, v97 row_half_mirror row_mask:0xf bank_mask:0xf bound_ctrl:1
	v_cndmask_b32_e64 v103, v103, v97, s[42:43]
	s_waitcnt vmcnt(12)
	v_mov_b32_e32 v96, 0
	v_dot4c_i32_i8_e32 v96, v48, v52
	v_cvt_f32_i32_sdwa v98, sext(v48) dst_sel:DWORD dst_unused:UNUSED_PAD src0_sel:BYTE_0
	v_cvt_f32_i32_sdwa v99, sext(v49) dst_sel:DWORD dst_unused:UNUSED_PAD src0_sel:BYTE_0
	v_dot4c_i32_i8_e32 v96, v49, v53
	v_cvt_f32_i32_sdwa v100, sext(v50) dst_sel:DWORD dst_unused:UNUSED_PAD src0_sel:BYTE_0
	v_dot4c_i32_i8_e32 v96, v50, v54
	v_cvt_f32_i32_sdwa v101, sext(v51) dst_sel:DWORD dst_unused:UNUSED_PAD src0_sel:BYTE_0
	v_dot4c_i32_i8_e32 v96, v51, v55
	v_fma_f32 v97, v98, v4, 0
	v_cvt_f32_i32_sdwa v98, sext(v48) dst_sel:DWORD dst_unused:UNUSED_PAD src0_sel:BYTE_1
	v_fmac_f32_e32 v97, v99, v8
	v_cvt_f32_i32_sdwa v99, sext(v49) dst_sel:DWORD dst_unused:UNUSED_PAD src0_sel:BYTE_1
	v_fmac_f32_e32 v97, v100, v12
	v_cvt_f32_i32_sdwa v100, sext(v50) dst_sel:DWORD dst_unused:UNUSED_PAD src0_sel:BYTE_1
	v_fmac_f32_e32 v97, v101, v16
	v_cvt_f32_i32_sdwa v101, sext(v51) dst_sel:DWORD dst_unused:UNUSED_PAD src0_sel:BYTE_1
	v_add_u32_dpp v96, v96, v96 quad_perm:[1,0,3,2] row_mask:0xf bank_mask:0xf bound_ctrl:1
	v_fmac_f32_e32 v97, v98, v5
	v_cvt_f32_i32_sdwa v98, sext(v48) dst_sel:DWORD dst_unused:UNUSED_PAD src0_sel:BYTE_2
	v_fmac_f32_e32 v97, v99, v9
	v_cvt_f32_i32_sdwa v99, sext(v49) dst_sel:DWORD dst_unused:UNUSED_PAD src0_sel:BYTE_2
	v_fmac_f32_e32 v97, v100, v13
	v_cvt_f32_i32_sdwa v100, sext(v50) dst_sel:DWORD dst_unused:UNUSED_PAD src0_sel:BYTE_2
	v_add_u32_dpp v96, v96, v96 quad_perm:[2,3,0,1] row_mask:0xf bank_mask:0xf bound_ctrl:1
	v_fmac_f32_e32 v97, v101, v17
	v_cvt_f32_i32_sdwa v101, sext(v51) dst_sel:DWORD dst_unused:UNUSED_PAD src0_sel:BYTE_2
	v_fmac_f32_e32 v97, v98, v6
	v_cvt_f32_i32_sdwa v98, sext(v48) dst_sel:DWORD dst_unused:UNUSED_PAD src0_sel:BYTE_3
	v_fmac_f32_e32 v97, v99, v10
	v_cvt_f32_i32_sdwa v99, sext(v49) dst_sel:DWORD dst_unused:UNUSED_PAD src0_sel:BYTE_3
	v_add_u32_dpp v96, v96, v96 row_half_mirror row_mask:0xf bank_mask:0xf bound_ctrl:1
	v_fmac_f32_e32 v97, v100, v14
	v_cvt_f32_i32_sdwa v100, sext(v50) dst_sel:DWORD dst_unused:UNUSED_PAD src0_sel:BYTE_3
	v_fmac_f32_e32 v97, v101, v18
	v_cvt_f32_i32_sdwa v101, sext(v51) dst_sel:DWORD dst_unused:UNUSED_PAD src0_sel:BYTE_3
	v_fmac_f32_e32 v97, v98, v7
	v_fmac_f32_e32 v97, v99, v11
	v_fmac_f32_e32 v97, v100, v15
	v_fmac_f32_e32 v97, v101, v19
	v_cndmask_b32_e64 v102, v102, v96, s[44:45]
	s_nop 0
	v_add_f32_dpp v97, v97, v97 quad_perm:[1,0,3,2] row_mask:0xf bank_mask:0xf bound_ctrl:1
	s_nop 1
	v_add_f32_dpp v97, v97, v97 quad_perm:[2,3,0,1] row_mask:0xf bank_mask:0xf bound_ctrl:1
	s_nop 1
	v_add_f32_dpp v97, v97, v97 row_half_mirror row_mask:0xf bank_mask:0xf bound_ctrl:1
	v_cndmask_b32_e64 v103, v103, v97, s[44:45]
	s_waitcnt vmcnt(10)
	v_mov_b32_e32 v96, 0
	v_dot4c_i32_i8_e32 v96, v56, v60
	v_cvt_f32_i32_sdwa v98, sext(v56) dst_sel:DWORD dst_unused:UNUSED_PAD src0_sel:BYTE_0
	v_cvt_f32_i32_sdwa v99, sext(v57) dst_sel:DWORD dst_unused:UNUSED_PAD src0_sel:BYTE_0
	v_dot4c_i32_i8_e32 v96, v57, v61
	v_cvt_f32_i32_sdwa v100, sext(v58) dst_sel:DWORD dst_unused:UNUSED_PAD src0_sel:BYTE_0
	v_dot4c_i32_i8_e32 v96, v58, v62
	v_cvt_f32_i32_sdwa v101, sext(v59) dst_sel:DWORD dst_unused:UNUSED_PAD src0_sel:BYTE_0
	v_dot4c_i32_i8_e32 v96, v59, v63
	v_fma_f32 v97, v98, v4, 0
	v_cvt_f32_i32_sdwa v98, sext(v56) dst_sel:DWORD dst_unused:UNUSED_PAD src0_sel:BYTE_1
	v_fmac_f32_e32 v97, v99, v8
	v_cvt_f32_i32_sdwa v99, sext(v57) dst_sel:DWORD dst_unused:UNUSED_PAD src0_sel:BYTE_1
	v_fmac_f32_e32 v97, v100, v12
	v_cvt_f32_i32_sdwa v100, sext(v58) dst_sel:DWORD dst_unused:UNUSED_PAD src0_sel:BYTE_1
	v_fmac_f32_e32 v97, v101, v16
	v_cvt_f32_i32_sdwa v101, sext(v59) dst_sel:DWORD dst_unused:UNUSED_PAD src0_sel:BYTE_1
	v_add_u32_dpp v96, v96, v96 quad_perm:[1,0,3,2] row_mask:0xf bank_mask:0xf bound_ctrl:1
	v_fmac_f32_e32 v97, v98, v5
	v_cvt_f32_i32_sdwa v98, sext(v56) dst_sel:DWORD dst_unused:UNUSED_PAD src0_sel:BYTE_2
	v_fmac_f32_e32 v97, v99, v9
	v_cvt_f32_i32_sdwa v99, sext(v57) dst_sel:DWORD dst_unused:UNUSED_PAD src0_sel:BYTE_2
	v_fmac_f32_e32 v97, v100, v13
	v_cvt_f32_i32_sdwa v100, sext(v58) dst_sel:DWORD dst_unused:UNUSED_PAD src0_sel:BYTE_2
	v_add_u32_dpp v96, v96, v96 quad_perm:[2,3,0,1] row_mask:0xf bank_mask:0xf bound_ctrl:1
	v_fmac_f32_e32 v97, v101, v17
	v_cvt_f32_i32_sdwa v101, sext(v59) dst_sel:DWORD dst_unused:UNUSED_PAD src0_sel:BYTE_2
	v_fmac_f32_e32 v97, v98, v6
	v_cvt_f32_i32_sdwa v98, sext(v56) dst_sel:DWORD dst_unused:UNUSED_PAD src0_sel:BYTE_3
	v_fmac_f32_e32 v97, v99, v10
	v_cvt_f32_i32_sdwa v99, sext(v57) dst_sel:DWORD dst_unused:UNUSED_PAD src0_sel:BYTE_3
	v_add_u32_dpp v96, v96, v96 row_half_mirror row_mask:0xf bank_mask:0xf bound_ctrl:1
	v_fmac_f32_e32 v97, v100, v14
	v_cvt_f32_i32_sdwa v100, sext(v58) dst_sel:DWORD dst_unused:UNUSED_PAD src0_sel:BYTE_3
	v_fmac_f32_e32 v97, v101, v18
	v_cvt_f32_i32_sdwa v101, sext(v59) dst_sel:DWORD dst_unused:UNUSED_PAD src0_sel:BYTE_3
	v_fmac_f32_e32 v97, v98, v7
	v_fmac_f32_e32 v97, v99, v11
	v_fmac_f32_e32 v97, v100, v15
	v_fmac_f32_e32 v97, v101, v19
	v_cndmask_b32_e64 v102, v102, v96, s[46:47]
	s_nop 0
	v_add_f32_dpp v97, v97, v97 quad_perm:[1,0,3,2] row_mask:0xf bank_mask:0xf bound_ctrl:1
	s_nop 1
	v_add_f32_dpp v97, v97, v97 quad_perm:[2,3,0,1] row_mask:0xf bank_mask:0xf bound_ctrl:1
	s_nop 1
	v_add_f32_dpp v97, v97, v97 row_half_mirror row_mask:0xf bank_mask:0xf bound_ctrl:1
	v_cndmask_b32_e64 v103, v103, v97, s[46:47]
	s_waitcnt vmcnt(8)
	v_mov_b32_e32 v96, 0
	v_dot4c_i32_i8_e32 v96, v64, v68
	v_cvt_f32_i32_sdwa v98, sext(v64) dst_sel:DWORD dst_unused:UNUSED_PAD src0_sel:BYTE_0
	v_cvt_f32_i32_sdwa v99, sext(v65) dst_sel:DWORD dst_unused:UNUSED_PAD src0_sel:BYTE_0
	v_dot4c_i32_i8_e32 v96, v65, v69
	v_cvt_f32_i32_sdwa v100, sext(v66) dst_sel:DWORD dst_unused:UNUSED_PAD src0_sel:BYTE_0
	v_dot4c_i32_i8_e32 v96, v66, v70
	v_cvt_f32_i32_sdwa v101, sext(v67) dst_sel:DWORD dst_unused:UNUSED_PAD src0_sel:BYTE_0
	v_dot4c_i32_i8_e32 v96, v67, v71
	v_fma_f32 v97, v98, v4, 0
	v_cvt_f32_i32_sdwa v98, sext(v64) dst_sel:DWORD dst_unused:UNUSED_PAD src0_sel:BYTE_1
	v_fmac_f32_e32 v97, v99, v8
	v_cvt_f32_i32_sdwa v99, sext(v65) dst_sel:DWORD dst_unused:UNUSED_PAD src0_sel:BYTE_1
	v_fmac_f32_e32 v97, v100, v12
	v_cvt_f32_i32_sdwa v100, sext(v66) dst_sel:DWORD dst_unused:UNUSED_PAD src0_sel:BYTE_1
	v_fmac_f32_e32 v97, v101, v16
	v_cvt_f32_i32_sdwa v101, sext(v67) dst_sel:DWORD dst_unused:UNUSED_PAD src0_sel:BYTE_1
	v_add_u32_dpp v96, v96, v96 quad_perm:[1,0,3,2] row_mask:0xf bank_mask:0xf bound_ctrl:1
	v_fmac_f32_e32 v97, v98, v5
	v_cvt_f32_i32_sdwa v98, sext(v64) dst_sel:DWORD dst_unused:UNUSED_PAD src0_sel:BYTE_2
	v_fmac_f32_e32 v97, v99, v9
	v_cvt_f32_i32_sdwa v99, sext(v65) dst_sel:DWORD dst_unused:UNUSED_PAD src0_sel:BYTE_2
	v_fmac_f32_e32 v97, v100, v13
	v_cvt_f32_i32_sdwa v100, sext(v66) dst_sel:DWORD dst_unused:UNUSED_PAD src0_sel:BYTE_2
	v_add_u32_dpp v96, v96, v96 quad_perm:[2,3,0,1] row_mask:0xf bank_mask:0xf bound_ctrl:1
	v_fmac_f32_e32 v97, v101, v17
	v_cvt_f32_i32_sdwa v101, sext(v67) dst_sel:DWORD dst_unused:UNUSED_PAD src0_sel:BYTE_2
	v_fmac_f32_e32 v97, v98, v6
	v_cvt_f32_i32_sdwa v98, sext(v64) dst_sel:DWORD dst_unused:UNUSED_PAD src0_sel:BYTE_3
	v_fmac_f32_e32 v97, v99, v10
	v_cvt_f32_i32_sdwa v99, sext(v65) dst_sel:DWORD dst_unused:UNUSED_PAD src0_sel:BYTE_3
	v_add_u32_dpp v96, v96, v96 row_half_mirror row_mask:0xf bank_mask:0xf bound_ctrl:1
	v_fmac_f32_e32 v97, v100, v14
	v_cvt_f32_i32_sdwa v100, sext(v66) dst_sel:DWORD dst_unused:UNUSED_PAD src0_sel:BYTE_3
	v_fmac_f32_e32 v97, v101, v18
	v_cvt_f32_i32_sdwa v101, sext(v67) dst_sel:DWORD dst_unused:UNUSED_PAD src0_sel:BYTE_3
	v_fmac_f32_e32 v97, v98, v7
	v_fmac_f32_e32 v97, v99, v11
	v_fmac_f32_e32 v97, v100, v15
	v_fmac_f32_e32 v97, v101, v19
	v_cndmask_b32_e64 v102, v102, v96, s[48:49]
	s_nop 0
	v_add_f32_dpp v97, v97, v97 quad_perm:[1,0,3,2] row_mask:0xf bank_mask:0xf bound_ctrl:1
	s_nop 1
	v_add_f32_dpp v97, v97, v97 quad_perm:[2,3,0,1] row_mask:0xf bank_mask:0xf bound_ctrl:1
	s_nop 1
	v_add_f32_dpp v97, v97, v97 row_half_mirror row_mask:0xf bank_mask:0xf bound_ctrl:1
	v_cndmask_b32_e64 v103, v103, v97, s[48:49]
	s_waitcnt vmcnt(6)
	v_mov_b32_e32 v96, 0
	v_dot4c_i32_i8_e32 v96, v72, v76
	v_cvt_f32_i32_sdwa v98, sext(v72) dst_sel:DWORD dst_unused:UNUSED_PAD src0_sel:BYTE_0
	v_cvt_f32_i32_sdwa v99, sext(v73) dst_sel:DWORD dst_unused:UNUSED_PAD src0_sel:BYTE_0
	v_dot4c_i32_i8_e32 v96, v73, v77
	v_cvt_f32_i32_sdwa v100, sext(v74) dst_sel:DWORD dst_unused:UNUSED_PAD src0_sel:BYTE_0
	v_dot4c_i32_i8_e32 v96, v74, v78
	v_cvt_f32_i32_sdwa v101, sext(v75) dst_sel:DWORD dst_unused:UNUSED_PAD src0_sel:BYTE_0
	v_dot4c_i32_i8_e32 v96, v75, v79
	v_fma_f32 v97, v98, v4, 0
	v_cvt_f32_i32_sdwa v98, sext(v72) dst_sel:DWORD dst_unused:UNUSED_PAD src0_sel:BYTE_1
	v_fmac_f32_e32 v97, v99, v8
	v_cvt_f32_i32_sdwa v99, sext(v73) dst_sel:DWORD dst_unused:UNUSED_PAD src0_sel:BYTE_1
	v_fmac_f32_e32 v97, v100, v12
	v_cvt_f32_i32_sdwa v100, sext(v74) dst_sel:DWORD dst_unused:UNUSED_PAD src0_sel:BYTE_1
	v_fmac_f32_e32 v97, v101, v16
	v_cvt_f32_i32_sdwa v101, sext(v75) dst_sel:DWORD dst_unused:UNUSED_PAD src0_sel:BYTE_1
	v_add_u32_dpp v96, v96, v96 quad_perm:[1,0,3,2] row_mask:0xf bank_mask:0xf bound_ctrl:1
	v_fmac_f32_e32 v97, v98, v5
	v_cvt_f32_i32_sdwa v98, sext(v72) dst_sel:DWORD dst_unused:UNUSED_PAD src0_sel:BYTE_2
	v_fmac_f32_e32 v97, v99, v9
	v_cvt_f32_i32_sdwa v99, sext(v73) dst_sel:DWORD dst_unused:UNUSED_PAD src0_sel:BYTE_2
	v_fmac_f32_e32 v97, v100, v13
	v_cvt_f32_i32_sdwa v100, sext(v74) dst_sel:DWORD dst_unused:UNUSED_PAD src0_sel:BYTE_2
	v_add_u32_dpp v96, v96, v96 quad_perm:[2,3,0,1] row_mask:0xf bank_mask:0xf bound_ctrl:1
	v_fmac_f32_e32 v97, v101, v17
	v_cvt_f32_i32_sdwa v101, sext(v75) dst_sel:DWORD dst_unused:UNUSED_PAD src0_sel:BYTE_2
	v_fmac_f32_e32 v97, v98, v6
	v_cvt_f32_i32_sdwa v98, sext(v72) dst_sel:DWORD dst_unused:UNUSED_PAD src0_sel:BYTE_3
	v_fmac_f32_e32 v97, v99, v10
	v_cvt_f32_i32_sdwa v99, sext(v73) dst_sel:DWORD dst_unused:UNUSED_PAD src0_sel:BYTE_3
	v_add_u32_dpp v96, v96, v96 row_half_mirror row_mask:0xf bank_mask:0xf bound_ctrl:1
	v_fmac_f32_e32 v97, v100, v14
	v_cvt_f32_i32_sdwa v100, sext(v74) dst_sel:DWORD dst_unused:UNUSED_PAD src0_sel:BYTE_3
	v_fmac_f32_e32 v97, v101, v18
	v_cvt_f32_i32_sdwa v101, sext(v75) dst_sel:DWORD dst_unused:UNUSED_PAD src0_sel:BYTE_3
	v_fmac_f32_e32 v97, v98, v7
	v_fmac_f32_e32 v97, v99, v11
	v_fmac_f32_e32 v97, v100, v15
	v_fmac_f32_e32 v97, v101, v19
	v_cndmask_b32_e64 v102, v102, v96, s[50:51]
	s_nop 0
	v_add_f32_dpp v97, v97, v97 quad_perm:[1,0,3,2] row_mask:0xf bank_mask:0xf bound_ctrl:1
	s_nop 1
	v_add_f32_dpp v97, v97, v97 quad_perm:[2,3,0,1] row_mask:0xf bank_mask:0xf bound_ctrl:1
	s_nop 1
	v_add_f32_dpp v97, v97, v97 row_half_mirror row_mask:0xf bank_mask:0xf bound_ctrl:1
	v_cndmask_b32_e64 v103, v103, v97, s[50:51]
	s_waitcnt vmcnt(4)
	v_mov_b32_e32 v96, 0
	v_dot4c_i32_i8_e32 v96, v80, v84
	v_cvt_f32_i32_sdwa v98, sext(v80) dst_sel:DWORD dst_unused:UNUSED_PAD src0_sel:BYTE_0
	v_cvt_f32_i32_sdwa v99, sext(v81) dst_sel:DWORD dst_unused:UNUSED_PAD src0_sel:BYTE_0
	v_dot4c_i32_i8_e32 v96, v81, v85
	v_cvt_f32_i32_sdwa v100, sext(v82) dst_sel:DWORD dst_unused:UNUSED_PAD src0_sel:BYTE_0
	v_dot4c_i32_i8_e32 v96, v82, v86
	v_cvt_f32_i32_sdwa v101, sext(v83) dst_sel:DWORD dst_unused:UNUSED_PAD src0_sel:BYTE_0
	v_dot4c_i32_i8_e32 v96, v83, v87
	v_fma_f32 v97, v98, v4, 0
	v_cvt_f32_i32_sdwa v98, sext(v80) dst_sel:DWORD dst_unused:UNUSED_PAD src0_sel:BYTE_1
	v_fmac_f32_e32 v97, v99, v8
	v_cvt_f32_i32_sdwa v99, sext(v81) dst_sel:DWORD dst_unused:UNUSED_PAD src0_sel:BYTE_1
	v_fmac_f32_e32 v97, v100, v12
	v_cvt_f32_i32_sdwa v100, sext(v82) dst_sel:DWORD dst_unused:UNUSED_PAD src0_sel:BYTE_1
	v_fmac_f32_e32 v97, v101, v16
	v_cvt_f32_i32_sdwa v101, sext(v83) dst_sel:DWORD dst_unused:UNUSED_PAD src0_sel:BYTE_1
	v_add_u32_dpp v96, v96, v96 quad_perm:[1,0,3,2] row_mask:0xf bank_mask:0xf bound_ctrl:1
	v_fmac_f32_e32 v97, v98, v5
	v_cvt_f32_i32_sdwa v98, sext(v80) dst_sel:DWORD dst_unused:UNUSED_PAD src0_sel:BYTE_2
	v_fmac_f32_e32 v97, v99, v9
	v_cvt_f32_i32_sdwa v99, sext(v81) dst_sel:DWORD dst_unused:UNUSED_PAD src0_sel:BYTE_2
	v_fmac_f32_e32 v97, v100, v13
	v_cvt_f32_i32_sdwa v100, sext(v82) dst_sel:DWORD dst_unused:UNUSED_PAD src0_sel:BYTE_2
	v_add_u32_dpp v96, v96, v96 quad_perm:[2,3,0,1] row_mask:0xf bank_mask:0xf bound_ctrl:1
	v_fmac_f32_e32 v97, v101, v17
	v_cvt_f32_i32_sdwa v101, sext(v83) dst_sel:DWORD dst_unused:UNUSED_PAD src0_sel:BYTE_2
	v_fmac_f32_e32 v97, v98, v6
	v_cvt_f32_i32_sdwa v98, sext(v80) dst_sel:DWORD dst_unused:UNUSED_PAD src0_sel:BYTE_3
	v_fmac_f32_e32 v97, v99, v10
	v_cvt_f32_i32_sdwa v99, sext(v81) dst_sel:DWORD dst_unused:UNUSED_PAD src0_sel:BYTE_3
	v_add_u32_dpp v96, v96, v96 row_half_mirror row_mask:0xf bank_mask:0xf bound_ctrl:1
	v_fmac_f32_e32 v97, v100, v14
	v_cvt_f32_i32_sdwa v100, sext(v82) dst_sel:DWORD dst_unused:UNUSED_PAD src0_sel:BYTE_3
	v_fmac_f32_e32 v97, v101, v18
	v_cvt_f32_i32_sdwa v101, sext(v83) dst_sel:DWORD dst_unused:UNUSED_PAD src0_sel:BYTE_3
	v_fmac_f32_e32 v97, v98, v7
	v_fmac_f32_e32 v97, v99, v11
	v_fmac_f32_e32 v97, v100, v15
	v_fmac_f32_e32 v97, v101, v19
	v_cndmask_b32_e64 v102, v102, v96, s[52:53]
	s_nop 0
	v_add_f32_dpp v97, v97, v97 quad_perm:[1,0,3,2] row_mask:0xf bank_mask:0xf bound_ctrl:1
	s_nop 1
	v_add_f32_dpp v97, v97, v97 quad_perm:[2,3,0,1] row_mask:0xf bank_mask:0xf bound_ctrl:1
	s_nop 1
	v_add_f32_dpp v97, v97, v97 row_half_mirror row_mask:0xf bank_mask:0xf bound_ctrl:1
	v_cndmask_b32_e64 v103, v103, v97, s[52:53]
	s_waitcnt vmcnt(2)
	v_mov_b32_e32 v96, 0
	v_dot4c_i32_i8_e32 v96, v88, v92
	v_cvt_f32_i32_sdwa v98, sext(v88) dst_sel:DWORD dst_unused:UNUSED_PAD src0_sel:BYTE_0
	v_cvt_f32_i32_sdwa v99, sext(v89) dst_sel:DWORD dst_unused:UNUSED_PAD src0_sel:BYTE_0
	v_dot4c_i32_i8_e32 v96, v89, v93
	v_cvt_f32_i32_sdwa v100, sext(v90) dst_sel:DWORD dst_unused:UNUSED_PAD src0_sel:BYTE_0
	v_dot4c_i32_i8_e32 v96, v90, v94
	v_cvt_f32_i32_sdwa v101, sext(v91) dst_sel:DWORD dst_unused:UNUSED_PAD src0_sel:BYTE_0
	v_dot4c_i32_i8_e32 v96, v91, v95
	v_fma_f32 v97, v98, v4, 0
	v_cvt_f32_i32_sdwa v98, sext(v88) dst_sel:DWORD dst_unused:UNUSED_PAD src0_sel:BYTE_1
	v_fmac_f32_e32 v97, v99, v8
	v_cvt_f32_i32_sdwa v99, sext(v89) dst_sel:DWORD dst_unused:UNUSED_PAD src0_sel:BYTE_1
	v_fmac_f32_e32 v97, v100, v12
	v_cvt_f32_i32_sdwa v100, sext(v90) dst_sel:DWORD dst_unused:UNUSED_PAD src0_sel:BYTE_1
	v_fmac_f32_e32 v97, v101, v16
	v_cvt_f32_i32_sdwa v101, sext(v91) dst_sel:DWORD dst_unused:UNUSED_PAD src0_sel:BYTE_1
	v_add_u32_dpp v96, v96, v96 quad_perm:[1,0,3,2] row_mask:0xf bank_mask:0xf bound_ctrl:1
	v_fmac_f32_e32 v97, v98, v5
	v_cvt_f32_i32_sdwa v98, sext(v88) dst_sel:DWORD dst_unused:UNUSED_PAD src0_sel:BYTE_2
	v_fmac_f32_e32 v97, v99, v9
	v_cvt_f32_i32_sdwa v99, sext(v89) dst_sel:DWORD dst_unused:UNUSED_PAD src0_sel:BYTE_2
	v_fmac_f32_e32 v97, v100, v13
	v_cvt_f32_i32_sdwa v100, sext(v90) dst_sel:DWORD dst_unused:UNUSED_PAD src0_sel:BYTE_2
	v_add_u32_dpp v96, v96, v96 quad_perm:[2,3,0,1] row_mask:0xf bank_mask:0xf bound_ctrl:1
	v_fmac_f32_e32 v97, v101, v17
	v_cvt_f32_i32_sdwa v101, sext(v91) dst_sel:DWORD dst_unused:UNUSED_PAD src0_sel:BYTE_2
	v_fmac_f32_e32 v97, v98, v6
	v_cvt_f32_i32_sdwa v98, sext(v88) dst_sel:DWORD dst_unused:UNUSED_PAD src0_sel:BYTE_3
	v_fmac_f32_e32 v97, v99, v10
	v_cvt_f32_i32_sdwa v99, sext(v89) dst_sel:DWORD dst_unused:UNUSED_PAD src0_sel:BYTE_3
	v_add_u32_dpp v96, v96, v96 row_half_mirror row_mask:0xf bank_mask:0xf bound_ctrl:1
	v_fmac_f32_e32 v97, v100, v14
	v_cvt_f32_i32_sdwa v100, sext(v90) dst_sel:DWORD dst_unused:UNUSED_PAD src0_sel:BYTE_3
	v_fmac_f32_e32 v97, v101, v18
	v_cvt_f32_i32_sdwa v101, sext(v91) dst_sel:DWORD dst_unused:UNUSED_PAD src0_sel:BYTE_3
	v_fmac_f32_e32 v97, v98, v7
	v_fmac_f32_e32 v97, v99, v11
	v_fmac_f32_e32 v97, v100, v15
	v_fmac_f32_e32 v97, v101, v19
	v_cndmask_b32_e64 v102, v102, v96, s[54:55]
	s_nop 0
	v_add_f32_dpp v97, v97, v97 quad_perm:[1,0,3,2] row_mask:0xf bank_mask:0xf bound_ctrl:1
	s_nop 1
	v_add_f32_dpp v97, v97, v97 quad_perm:[2,3,0,1] row_mask:0xf bank_mask:0xf bound_ctrl:1
	s_nop 1
	v_add_f32_dpp v97, v97, v97 row_half_mirror row_mask:0xf bank_mask:0xf bound_ctrl:1
	v_cndmask_b32_e64 v103, v103, v97, s[54:55]
	global_atomic_add v28, v102, s[20:21] offset:768
	global_atomic_add_f32 v28, v103, s[22:23] offset:768
	s_endpgm

	.amdhsa_kernel _Z15k3_pairs_slicedPKDv4_jPKfPKiS5_PiPf
		.amdhsa_group_segment_fixed_size 0
		.amdhsa_private_segment_fixed_size 0
		.amdhsa_kernarg_size 48
		.amdhsa_user_sgpr_count 2
		.amdhsa_user_sgpr_dispatch_ptr 0
		.amdhsa_user_sgpr_queue_ptr 0
		.amdhsa_user_sgpr_kernarg_segment_ptr 1
		.amdhsa_user_sgpr_dispatch_id 0
		.amdhsa_user_sgpr_kernarg_preload_length 0
		.amdhsa_user_sgpr_kernarg_preload_offset 0
		.amdhsa_user_sgpr_private_segment_size 0
		.amdhsa_uses_dynamic_stack 0
		.amdhsa_enable_private_segment 0
		.amdhsa_system_sgpr_workgroup_id_x 1
		.amdhsa_system_sgpr_workgroup_id_y 0
		.amdhsa_system_sgpr_workgroup_id_z 0
		.amdhsa_system_sgpr_workgroup_info 0
		.amdhsa_system_vgpr_workitem_id 0
		.amdhsa_next_free_vgpr 108
		.amdhsa_next_free_sgpr 60
		.amdhsa_accum_offset 108
		.amdhsa_reserve_vcc 1
		.amdhsa_float_round_mode_32 0
		.amdhsa_float_round_mode_16_64 0
		.amdhsa_float_denorm_mode_32 3
		.amdhsa_float_denorm_mode_16_64 3
		.amdhsa_dx10_clamp 1
		.amdhsa_ieee_mode 1
		.amdhsa_fp16_overflow 0
		.amdhsa_tg_split 0
		.amdhsa_exception_fp_ieee_invalid_op 0
		.amdhsa_exception_fp_denorm_src 0
		.amdhsa_exception_fp_ieee_div_zero 0
		.amdhsa_exception_fp_ieee_overflow 0
		.amdhsa_exception_fp_ieee_underflow 0
		.amdhsa_exception_fp_ieee_inexact 0
		.amdhsa_exception_int_div_zero 0
	.end_amdhsa_kernel
